# speedup vs baseline: 1.0098x; 1.0031x over previous
_Z8k_stageAPKfS0_S0_S0_PDF16_PKDF16_S0_S1_ii:
	s_load_dwordx2 s[64:65], s[0:1], 0x40
	v_readfirstlane_b32 s94, v0
	s_nop 0
	s_lshr_b32 s94, s94, 6
	s_load_dwordx8 s[4:11], s[0:1], 0x0
	v_readfirstlane_b32 s14, v0
	s_lshr_b32 s15, s2, 5
	s_lshl_b32 s2, s2, 7
	s_lshr_b32 s20, s14, 6
	s_and_b32 s12, s2, 0xf80
	s_lshl_b32 s13, s15, 12
	s_mov_b32 s18, s3
	s_cmpk_lt_u32 s14, 0x100
	s_waitcnt lgkmcnt(0)
	s_cselect_b32 s2, s4, s6
	s_cselect_b32 s3, s5, s7
	s_cselect_b32 s4, s8, s10
	s_cselect_b32 s5, s9, s11
	s_cmp_eq_u32 s18, 0
	s_cselect_b32 s3, s3, s5
	s_cselect_b32 s2, s2, s4
	s_lshr_b32 s5, s14, 1
	s_lshl_b32 s4, s15, 7
	s_and_b32 s5, s5, 0x60
	v_bfe_u32 v1, v0, 5, 1
	s_or_b32 s4, s5, s4
	v_lshl_or_b32 v82, v1, 3, s4
	v_mov_b32_e32 v83, 0
	v_lshlrev_b64 v[2:3], 14, v[82:83]
	v_lshlrev_b32_e32 v78, 2, v0
	s_mov_b32 s17, 0
	v_lshl_add_u64 v[2:3], s[2:3], 0, v[2:3]
	s_lshl_b32 s16, s12, 2
	v_and_b32_e32 v79, 0x7c, v78
	v_lshl_add_u64 v[2:3], v[2:3], 0, s[16:17]
	v_lshlrev_b32_e32 v82, 2, v79
	v_lshl_add_u64 v[42:43], v[2:3], 0, v[82:83]
	s_movk_i32 s21, 0x4000
	v_add_co_u32_e32 v10, vcc, s21, v42
	s_mov_b32 s2, 0x8000
	s_nop 0
	v_addc_co_u32_e32 v11, vcc, 0, v43, vcc
	v_add_co_u32_e32 v18, vcc, s2, v42
	s_mov_b32 s2, 0xc000
	s_nop 0
	v_addc_co_u32_e32 v19, vcc, 0, v43, vcc
	v_add_co_u32_e32 v20, vcc, s2, v42
	s_mov_b32 s14, 0x10000
	s_nop 0
	v_addc_co_u32_e32 v21, vcc, 0, v43, vcc
	v_add_co_u32_e32 v26, vcc, s14, v42
	s_mov_b32 s2, 0x14000
	s_nop 0
	v_addc_co_u32_e32 v27, vcc, 0, v43, vcc
	v_add_co_u32_e32 v28, vcc, s2, v42
	s_mov_b32 s2, 0x18000
	s_nop 0
	v_addc_co_u32_e32 v29, vcc, 0, v43, vcc
	v_add_co_u32_e32 v34, vcc, s2, v42
	s_mov_b32 s2, 0x1c000
	s_nop 0
	v_addc_co_u32_e32 v35, vcc, 0, v43, vcc
	v_add_co_u32_e32 v36, vcc, s2, v42
	s_mov_b32 s2, 0x40000
	s_nop 0
	v_addc_co_u32_e32 v37, vcc, 0, v43, vcc
	v_add_co_u32_e32 v66, vcc, s2, v42
	s_mov_b32 s2, 0x44000
	s_nop 0
	v_addc_co_u32_e32 v67, vcc, 0, v43, vcc
	v_add_co_u32_e32 v68, vcc, s2, v42
	s_mov_b32 s2, 0x48000
	s_nop 0
	v_addc_co_u32_e32 v69, vcc, 0, v43, vcc
	global_load_dwordx4 v[2:5], v[42:43], off nt
	global_load_dwordx4 v[6:9], v[10:11], off nt
	v_add_co_u32_e32 v44, vcc, s2, v42
	global_load_dwordx4 v[10:13], v[18:19], off nt
	global_load_dwordx4 v[14:17], v[20:21], off nt
	s_nop 0
	global_load_dwordx4 v[18:21], v[26:27], off nt
	global_load_dwordx4 v[22:25], v[28:29], off nt
	s_nop 0
	global_load_dwordx4 v[26:29], v[34:35], off nt
	global_load_dwordx4 v[30:33], v[36:37], off nt
	v_addc_co_u32_e32 v45, vcc, 0, v43, vcc
	s_mov_b32 s2, 0x4c000
	v_add_co_u32_e32 v46, vcc, s2, v42
	s_mov_b32 s2, 0x50000
	s_nop 0
	v_addc_co_u32_e32 v47, vcc, 0, v43, vcc
	v_add_co_u32_e32 v70, vcc, s2, v42
	s_mov_b32 s2, 0x54000
	s_nop 0
	v_addc_co_u32_e32 v71, vcc, 0, v43, vcc
	v_add_co_u32_e32 v72, vcc, s2, v42
	s_mov_b32 s2, 0x58000
	s_nop 0
	v_addc_co_u32_e32 v73, vcc, 0, v43, vcc
	v_add_co_u32_e32 v74, vcc, s2, v42
	s_mov_b32 s2, 0x5c000
	s_nop 0
	v_addc_co_u32_e32 v75, vcc, 0, v43, vcc
	v_add_co_u32_e32 v76, vcc, s2, v42
	global_load_dwordx4 v[34:37], v[44:45], off nt
	global_load_dwordx4 v[38:41], v[46:47], off nt
	v_addc_co_u32_e32 v77, vcc, 0, v43, vcc
	global_load_dwordx4 v[42:45], v[74:75], off nt
	global_load_dwordx4 v[46:49], v[76:77], off nt
	global_load_dwordx4 v[50:53], v[70:71], off nt
	global_load_dwordx4 v[54:57], v[72:73], off nt
	global_load_dwordx4 v[58:61], v[66:67], off nt
	global_load_dwordx4 v[62:65], v[68:69], off nt
	v_lshl_or_b32 v1, s20, 2, v1
	v_lshrrev_b32_e32 v70, 5, v0
	v_or_b32_e32 v141, 0x200, v0
	v_or_b32_e32 v142, 0x600, v0
	s_or_b32 s16, s13, s12
	s_ashr_i32 s19, s18, 31
	s_lshl_b64 s[12:13], s[16:17], 9
	s_mov_b32 s15, 0x20000
	v_or_b32_e32 v144, 0xa00, v0
	v_bfe_u32 v140, v0, 4, 2
	v_and_b32_e32 v145, 15, v0
	v_lshlrev_b32_e32 v220, 9, v145
	s_waitcnt vmcnt(14)
	v_cvt_pk_f16_f32 v66, v2, v6
	v_lshlrev_b32_e32 v6, 9, v79
	v_bitop3_b32 v2, v78, v1, 12 bitop3:0x6c
	s_waitcnt vmcnt(12)
	v_cvt_pk_f16_f32 v67, v10, v14
	s_waitcnt vmcnt(10)
	v_cvt_pk_f16_f32 v68, v18, v22
	s_waitcnt vmcnt(8)
	v_cvt_pk_f16_f32 v69, v26, v30
	v_lshl_add_u32 v2, v2, 4, v6
	ds_write_b128 v2, v[66:69]
	v_cvt_pk_f16_f32 v66, v3, v7
	v_or_b32_e32 v7, 1, v79
	v_lshlrev_b32_e32 v10, 9, v7
	v_bitop3_b32 v2, v7, v1, 13 bitop3:0x6c
	v_cvt_pk_f16_f32 v69, v27, v31
	v_cvt_pk_f16_f32 v68, v19, v23
	v_cvt_pk_f16_f32 v67, v11, v15
	v_lshl_add_u32 v2, v2, 4, v10
	ds_write_b128 v2, v[66:69]
	v_cvt_pk_f16_f32 v66, v4, v8
	v_or_b32_e32 v8, 2, v79
	v_lshlrev_b32_e32 v11, 9, v8
	v_bitop3_b32 v2, v8, v1, 14 bitop3:0x6c
	v_cvt_pk_f16_f32 v69, v28, v32
	v_cvt_pk_f16_f32 v68, v20, v24
	v_cvt_pk_f16_f32 v67, v12, v16
	v_lshl_add_u32 v2, v2, 4, v11
	v_cvt_pk_f16_f32 v12, v5, v9
	v_or_b32_e32 v9, 3, v79
	ds_write_b128 v2, v[66:69]
	v_lshlrev_b32_e32 v16, 9, v9
	v_bitop3_b32 v2, v9, v1, 15 bitop3:0x6c
	v_cvt_pk_f16_f32 v15, v29, v33
	v_cvt_pk_f16_f32 v14, v21, v25
	v_cvt_pk_f16_f32 v13, v13, v17
	v_lshl_add_u32 v2, v2, 4, v16
	v_or_b32_e32 v1, 2, v1
	ds_write_b128 v2, v[12:15]
	v_bitop3_b32 v12, v78, v1, 12 bitop3:0x6c
	s_waitcnt vmcnt(4)
	v_cvt_pk_f16_f32 v5, v42, v46
	s_waitcnt vmcnt(2)
	v_cvt_pk_f16_f32 v4, v50, v54
	v_cvt_pk_f16_f32 v3, v34, v38
	s_waitcnt vmcnt(0)
	v_cvt_pk_f16_f32 v2, v58, v62
	v_lshl_add_u32 v6, v12, 4, v6
	ds_write_b128 v6, v[2:5]
	v_bitop3_b32 v6, v7, v1, 13 bitop3:0x6c
	v_cvt_pk_f16_f32 v5, v43, v47
	v_cvt_pk_f16_f32 v4, v51, v55
	v_cvt_pk_f16_f32 v3, v35, v39
	v_cvt_pk_f16_f32 v2, v59, v63
	v_lshl_add_u32 v6, v6, 4, v10
	ds_write_b128 v6, v[2:5]
	v_bitop3_b32 v6, v8, v1, 14 bitop3:0x6c
	v_cvt_pk_f16_f32 v5, v44, v48
	v_cvt_pk_f16_f32 v4, v52, v56
	v_cvt_pk_f16_f32 v3, v36, v40
	v_cvt_pk_f16_f32 v2, v60, v64
	v_lshl_add_u32 v6, v6, 4, v11
	v_bitop3_b32 v1, v9, v1, 15 bitop3:0x6c
	ds_write_b128 v6, v[2:5]
	v_cvt_pk_f16_f32 v5, v45, v49
	v_cvt_pk_f16_f32 v4, v53, v57
	v_cvt_pk_f16_f32 v3, v37, v41
	v_cvt_pk_f16_f32 v2, v61, v65
	v_lshl_add_u32 v1, v1, 4, v16
	ds_write_b128 v1, v[2:5]
	v_bitop3_b32 v2, v70, v0, 31 bitop3:0x78
	v_lshlrev_b32_e32 v1, 9, v70
	v_lshlrev_b32_e32 v22, 4, v2
	v_or_b32_e32 v10, v22, v1
	s_waitcnt lgkmcnt(0)
	s_barrier
	ds_read_b128 v[2:5], v10
	s_load_dwordx8 s[4:11], s[0:1], 0x20
	s_load_dwordx2 s[2:3], s[0:1], 0x40
	v_lshlrev_b32_e32 v24, 4, v0
	v_and_b32_e32 v25, 0x1e00, v24
	v_or_b32_e32 v26, v22, v25
	s_waitcnt lgkmcnt(0)
	v_pk_max_f16 v6, v5, v5
	v_and_b32_e32 v18, 31, v0
	v_pk_max_f16 v9, v6, 0
	v_pk_max_f16 v6, v4, v4
	v_lshlrev_b32_e32 v29, 4, v18
	v_pk_max_f16 v8, v6, 0
	v_pk_max_f16 v6, v3, v3
	s_lshl_b64 s[0:1], s[18:19], 23
	v_pk_max_f16 v7, v6, 0
	v_pk_max_f16 v6, v2, v2
	s_add_u32 s0, s4, s0
	v_pk_max_f16 v6, v6, 0
	ds_write_b128 v10, v[6:9]
	v_lshlrev_b32_e32 v6, 4, v141
	v_and_b32_e32 v23, 0x3e00, v6
	v_or_b32_e32 v14, v22, v23
	ds_read_b128 v[6:9], v14
	s_addc_u32 s1, s5, s1
	s_add_u32 s12, s0, s12
	s_addc_u32 s0, s1, s13
	s_and_b32 s13, s0, 0xffff
	s_waitcnt lgkmcnt(0)
	v_pk_max_f16 v10, v9, v9
	v_or_b32_e32 v1, v1, v29
	v_pk_max_f16 v13, v10, 0
	v_pk_max_f16 v10, v8, v8
	buffer_store_dwordx4 v[2:5], v1, s[12:15], 0 offen sc1
	v_pk_max_f16 v12, v10, 0
	v_pk_max_f16 v10, v7, v7
	v_or_b32_e32 v1, v23, v29
	v_pk_max_f16 v11, v10, 0
	v_pk_max_f16 v10, v6, v6
	buffer_store_dwordx4 v[6:9], v1, s[12:15], 0 offen sc1
	v_pk_max_f16 v10, v10, 0
	ds_write_b128 v14, v[10:13]
	ds_read_b128 v[10:13], v26 offset:16384
	v_or_b32_e32 v25, v25, v29
	v_or_b32_e32 v6, 0x4000, v25
	s_mov_b32 s0, 0xfe00
	s_waitcnt lgkmcnt(0)
	v_pk_max_f16 v14, v13, v13
	s_nop 0
	v_pk_max_f16 v17, v14, 0
	v_pk_max_f16 v14, v12, v12
	buffer_store_dwordx4 v[10:13], v6, s[12:15], 0 offen sc1
	v_pk_max_f16 v16, v14, 0
	v_pk_max_f16 v14, v11, v11
	s_nop 0
	v_pk_max_f16 v15, v14, 0
	v_pk_max_f16 v14, v10, v10
	s_nop 0
	v_pk_max_f16 v14, v14, 0
	ds_write_b128 v26, v[14:17] offset:16384
	v_lshlrev_b32_e32 v14, 4, v142
	v_and_b32_e32 v27, 0x7e00, v14
	v_or_b32_e32 v28, v22, v27
	ds_read_b128 v[14:17], v28
	v_or_b32_e32 v10, v27, v29
	s_waitcnt lgkmcnt(0)
	v_pk_max_f16 v18, v17, v17
	s_nop 0
	v_pk_max_f16 v21, v18, 0
	v_pk_max_f16 v18, v16, v16
	buffer_store_dwordx4 v[14:17], v10, s[12:15], 0 offen sc1
	v_pk_max_f16 v20, v18, 0
	v_pk_max_f16 v18, v15, v15
	v_or_b32_e32 v10, 0x8000, v25
	v_pk_max_f16 v19, v18, 0
	v_pk_max_f16 v18, v14, v14
	s_nop 0
	v_pk_max_f16 v18, v18, 0
	ds_write_b128 v28, v[18:21]
	ds_read_b128 v[18:21], v26 offset:32768
	s_waitcnt lgkmcnt(0)
	v_pk_max_f16 v1, v21, v21
	s_nop 0
	v_pk_max_f16 v5, v1, 0
	v_pk_max_f16 v1, v20, v20
	buffer_store_dwordx4 v[18:21], v10, s[12:15], 0 offen sc1
	v_pk_max_f16 v4, v1, 0
	v_pk_max_f16 v1, v19, v19
	s_nop 0
	v_pk_max_f16 v3, v1, 0
	v_pk_max_f16 v1, v18, v18
	s_nop 0
	v_pk_max_f16 v2, v1, 0
	v_lshlrev_b32_e32 v1, 4, v144
	v_and_b32_e32 v1, 0xbe00, v1
	ds_write_b128 v26, v[2:5] offset:32768
	v_or_b32_e32 v23, v22, v1
	ds_read_b128 v[2:5], v23
	v_or_b32_e32 v1, v1, v29
	s_waitcnt lgkmcnt(0)
	v_pk_max_f16 v6, v5, v5
	s_nop 0
	v_pk_max_f16 v9, v6, 0
	v_pk_max_f16 v6, v4, v4
	buffer_store_dwordx4 v[2:5], v1, s[12:15], 0 offen sc1
	v_pk_max_f16 v8, v6, 0
	v_pk_max_f16 v6, v3, v3
	v_or_b32_e32 v1, 0xc000, v25
	v_pk_max_f16 v7, v6, 0
	v_pk_max_f16 v6, v2, v2
	s_nop 0
	v_pk_max_f16 v6, v6, 0
	ds_write_b128 v23, v[6:9]
	ds_read_b128 v[6:9], v26 offset:49152
	s_waitcnt lgkmcnt(0)
	v_pk_max_f16 v10, v9, v9
	s_nop 0
	v_pk_max_f16 v13, v10, 0
	v_pk_max_f16 v10, v8, v8
	buffer_store_dwordx4 v[6:9], v1, s[12:15], 0 offen sc1
	v_pk_max_f16 v12, v10, 0
	v_pk_max_f16 v10, v7, v7
	s_nop 0
	v_pk_max_f16 v11, v10, 0
	v_pk_max_f16 v10, v6, v6
	s_nop 0
	v_pk_max_f16 v10, v10, 0
	ds_write_b128 v26, v[10:13] offset:49152
	v_mov_b32_e32 v10, 0xe000
	v_bitop3_b32 v14, v24, s0, v10 bitop3:0xc8
	s_mul_i32 s0, s3, s18
	v_or_b32_e32 v15, v22, v14
	s_add_i32 s0, s0, s2
	ds_read_b128 v[10:13], v15
	s_mul_i32 s2, s0, 0x60000
	s_mul_hi_i32 s1, s0, 0x60000
	s_add_u32 s2, s6, s2
	s_mulk_i32 s0, 0x300
	s_addc_u32 s3, s7, s1
	s_ashr_i32 s1, s0, 31
	s_lshl_b64 s[0:1], s[0:1], 2
	v_or_b32_e32 v1, v14, v29
	s_add_u32 s4, s8, s0
	s_waitcnt lgkmcnt(0)
	buffer_store_dwordx4 v[10:13], v1, s[12:15], 0 offen sc1
	v_pk_max_f16 v1, v13, v13
	s_addc_u32 s5, s9, s1
	s_mul_i32 s0, s18, 0x1800000
	v_pk_max_f16 v5, v1, 0
	v_pk_max_f16 v1, v12, v12
	s_mul_hi_i32 s1, s18, 0x1800000
	s_add_u32 s0, s10, s0
	v_pk_max_f16 v4, v1, 0
	v_pk_max_f16 v1, v11, v11
	s_addc_u32 s1, s11, s1
	v_pk_max_f16 v3, v1, 0
	v_pk_max_f16 v1, v10, v10
	s_and_b32 s1, s1, 0xffff
	s_mul_i32 s7, s20, 0x6000
	v_pk_max_f16 v2, v1, 0
	v_and_b32_e32 v1, 63, v0
	s_mul_hi_u32 s6, s20, 0x6000
	s_add_u32 s2, s2, s7
	s_addc_u32 s3, s3, s6
	v_lshlrev_b32_e32 v82, 4, v1
	v_lshl_add_u64 v[118:119], s[2:3], 0, v[82:83]
	s_movk_i32 s6, 0x1000
	v_add_co_u32_e32 v50, vcc, s6, v118
	s_movk_i32 s6, 0x2000
	s_nop 0
	v_addc_co_u32_e32 v51, vcc, 0, v119, vcc
	ds_write_b128 v15, v[2:5]
	v_add_co_u32_e32 v52, vcc, s6, v118
	global_load_dwordx4 v[2:5], v82, s[2:3] offset:1024
	global_load_dwordx4 v[6:9], v82, s[2:3] offset:2048
	v_addc_co_u32_e32 v53, vcc, 0, v119, vcc
	global_load_dwordx4 v[10:13], v82, s[2:3] offset:3072
	global_load_dwordx4 v[14:17], v[52:53], off offset:-4096
	global_load_dwordx4 v[18:21], v[50:51], off offset:1024
	global_load_dwordx4 v[22:25], v[50:51], off offset:2048
	global_load_dwordx4 v[26:29], v82, s[2:3]
	global_load_dwordx4 v[30:33], v[50:51], off offset:3072
	global_load_dwordx4 v[34:37], v[52:53], off
	global_load_dwordx4 v[38:41], v[52:53], off offset:1024
	global_load_dwordx4 v[42:45], v[52:53], off offset:2048
	global_load_dwordx4 v[46:49], v[52:53], off offset:3072
	s_movk_i32 s2, 0x3000
	v_add_co_u32_e32 v116, vcc, s2, v118
	s_waitcnt lgkmcnt(0)
	s_nop 0
	v_addc_co_u32_e32 v117, vcc, 0, v119, vcc
	v_add_co_u32_e32 v132, vcc, s21, v118
	s_barrier
	s_nop 0
	v_addc_co_u32_e32 v133, vcc, 0, v119, vcc
	global_load_dwordx4 v[50:53], v[132:133], off offset:-4096
	global_load_dwordx4 v[54:57], v[116:117], off offset:1024
	global_load_dwordx4 v[58:61], v[116:117], off offset:2048
	v_bitop3_b32 v1, v140, v0, 15 bitop3:0x78
	v_lshl_or_b32 v134, v1, 4, v220
	ds_read_b128 v[62:65], v134
	ds_read_b128 v[66:69], v134 offset:8192
	ds_read_b128 v[70:73], v134 offset:16384
	ds_read_b128 v[74:77], v134 offset:24576
	ds_read_b128 v[78:81], v134 offset:32768
	ds_read_b128 v[84:87], v134 offset:40960
	ds_read_b128 v[88:91], v134 offset:49152
	ds_read_b128 v[92:95], v134 offset:57344
	s_mul_i32 s7, s20, 48
	v_lshl_or_b32 v82, v140, 2, s7
	s_mul_i32 s7, s20, 0x60
	s_add_i32 s7, s7, 0x10000
	v_mul_u32_u24_e32 v1, 0x556, v0
	v_lshl_or_b32 v250, v140, 3, s7
	s_or_b32 s7, s16, 64
	v_lshrrev_b32_e32 v143, 16, v1
	s_movk_i32 s6, 0x600
	s_mov_b32 s2, 0x1800000
	s_mov_b32 s3, s15
	v_or_b32_e32 v139, s7, v143
	s_waitcnt vmcnt(8) lgkmcnt(7)
	v_mfma_f32_16x16x32_f16 v[96:99], v[26:29], v[62:65], 0
	s_waitcnt lgkmcnt(6)
	v_mfma_f32_16x16x32_f16 v[100:103], v[26:29], v[66:69], 0
	s_waitcnt lgkmcnt(5)
	v_mfma_f32_16x16x32_f16 v[104:107], v[26:29], v[70:73], 0
	s_waitcnt lgkmcnt(4)
	v_mfma_f32_16x16x32_f16 v[108:111], v[26:29], v[74:77], 0
	s_waitcnt lgkmcnt(3)
	v_mfma_f32_16x16x32_f16 v[112:115], v[26:29], v[78:81], 0
	s_waitcnt lgkmcnt(2)
	v_mfma_f32_16x16x32_f16 v[120:123], v[26:29], v[84:87], 0
	s_waitcnt lgkmcnt(1)
	v_mfma_f32_16x16x32_f16 v[124:127], v[26:29], v[88:91], 0
	s_waitcnt lgkmcnt(0)
	v_mfma_f32_16x16x32_f16 v[26:29], v[26:29], v[92:95], 0
	v_mfma_f32_16x16x32_f16 v[128:131], v[2:5], v[62:65], 0
	v_mfma_f32_16x16x32_f16 v[146:149], v[2:5], v[66:69], 0
	v_mfma_f32_16x16x32_f16 v[150:153], v[2:5], v[70:73], 0
	v_mfma_f32_16x16x32_f16 v[154:157], v[2:5], v[74:77], 0
	v_mfma_f32_16x16x32_f16 v[158:161], v[2:5], v[78:81], 0
	v_mfma_f32_16x16x32_f16 v[162:165], v[2:5], v[84:87], 0
	v_mfma_f32_16x16x32_f16 v[166:169], v[2:5], v[88:91], 0
	v_mfma_f32_16x16x32_f16 v[2:5], v[2:5], v[92:95], 0
	v_mfma_f32_16x16x32_f16 v[62:65], v[6:9], v[62:65], 0
	v_mfma_f32_16x16x32_f16 v[66:69], v[6:9], v[66:69], 0
	v_mfma_f32_16x16x32_f16 v[70:73], v[6:9], v[70:73], 0
	v_mfma_f32_16x16x32_f16 v[74:77], v[6:9], v[74:77], 0
	v_mfma_f32_16x16x32_f16 v[78:81], v[6:9], v[78:81], 0
	v_mfma_f32_16x16x32_f16 v[84:87], v[6:9], v[84:87], 0
	v_mfma_f32_16x16x32_f16 v[88:91], v[6:9], v[88:91], 0
	v_mfma_f32_16x16x32_f16 v[6:9], v[6:9], v[92:95], 0
	global_load_dwordx4 v[92:95], v[116:117], off offset:3072
	global_load_dwordx4 v[170:173], v[132:133], off
	global_load_dwordx4 v[174:177], v[132:133], off offset:1024
	v_bitop3_b32 v1, v140, v145, 4 bitop3:0x36
	v_lshl_or_b32 v1, v1, 4, v220
	ds_read_b128 v[178:181], v1
	ds_read_b128 v[182:185], v1 offset:8192
	ds_read_b128 v[186:189], v1 offset:16384
	ds_read_b128 v[190:193], v1 offset:24576
	ds_read_b128 v[194:197], v1 offset:32768
	ds_read_b128 v[198:201], v1 offset:40960
	ds_read_b128 v[202:205], v1 offset:49152
	ds_read_b128 v[206:209], v1 offset:57344
	s_waitcnt lgkmcnt(7)
	v_mfma_f32_16x16x32_f16 v[96:99], v[10:13], v[178:181], v[96:99]
	s_waitcnt lgkmcnt(6)
	v_mfma_f32_16x16x32_f16 v[100:103], v[10:13], v[182:185], v[100:103]
	s_waitcnt lgkmcnt(5)
	v_mfma_f32_16x16x32_f16 v[104:107], v[10:13], v[186:189], v[104:107]
	s_waitcnt lgkmcnt(4)
	v_mfma_f32_16x16x32_f16 v[108:111], v[10:13], v[190:193], v[108:111]
	s_waitcnt lgkmcnt(3)
	v_mfma_f32_16x16x32_f16 v[112:115], v[10:13], v[194:197], v[112:115]
	s_waitcnt lgkmcnt(2)
	v_mfma_f32_16x16x32_f16 v[120:123], v[10:13], v[198:201], v[120:123]
	s_waitcnt lgkmcnt(1)
	v_mfma_f32_16x16x32_f16 v[124:127], v[10:13], v[202:205], v[124:127]
	s_waitcnt lgkmcnt(0)
	v_mfma_f32_16x16x32_f16 v[10:13], v[10:13], v[206:209], v[26:29]
	v_mfma_f32_16x16x32_f16 v[26:29], v[14:17], v[178:181], v[128:131]
	v_mfma_f32_16x16x32_f16 v[128:131], v[14:17], v[182:185], v[146:149]
	v_mfma_f32_16x16x32_f16 v[146:149], v[14:17], v[186:189], v[150:153]
	v_mfma_f32_16x16x32_f16 v[150:153], v[14:17], v[190:193], v[154:157]
	v_mfma_f32_16x16x32_f16 v[154:157], v[14:17], v[194:197], v[158:161]
	v_mfma_f32_16x16x32_f16 v[158:161], v[14:17], v[198:201], v[162:165]
	v_mfma_f32_16x16x32_f16 v[162:165], v[14:17], v[202:205], v[166:169]
	v_mfma_f32_16x16x32_f16 v[2:5], v[14:17], v[206:209], v[2:5]
	v_mfma_f32_16x16x32_f16 v[14:17], v[18:21], v[178:181], v[62:65]
	v_mfma_f32_16x16x32_f16 v[62:65], v[18:21], v[182:185], v[66:69]
	v_mfma_f32_16x16x32_f16 v[66:69], v[18:21], v[186:189], v[70:73]
	v_mfma_f32_16x16x32_f16 v[70:73], v[18:21], v[190:193], v[74:77]
	v_mfma_f32_16x16x32_f16 v[74:77], v[18:21], v[194:197], v[78:81]
	v_mfma_f32_16x16x32_f16 v[78:81], v[18:21], v[198:201], v[84:87]
	v_mfma_f32_16x16x32_f16 v[84:87], v[18:21], v[202:205], v[88:91]
	v_mfma_f32_16x16x32_f16 v[6:9], v[18:21], v[206:209], v[6:9]
	s_movk_i32 s8, 0x5000
	v_add_co_u32_e32 v116, vcc, s8, v118
	global_load_dwordx4 v[88:91], v[132:133], off offset:2048
	global_load_dwordx4 v[166:169], v[132:133], off offset:3072
	v_addc_co_u32_e32 v117, vcc, 0, v119, vcc
	global_load_dwordx4 v[178:181], v[116:117], off
	v_bitop3_b32 v18, v140, v145, 8 bitop3:0x36
	v_lshl_or_b32 v133, v18, 4, v220
	ds_read_b128 v[18:21], v133
	ds_read_b128 v[182:185], v133 offset:8192
	ds_read_b128 v[186:189], v133 offset:16384
	ds_read_b128 v[190:193], v133 offset:24576
	ds_read_b128 v[194:197], v133 offset:32768
	ds_read_b128 v[198:201], v133 offset:40960
	ds_read_b128 v[202:205], v133 offset:49152
	ds_read_b128 v[206:209], v133 offset:57344
	s_waitcnt lgkmcnt(7)
	v_mfma_f32_16x16x32_f16 v[96:99], v[22:25], v[18:21], v[96:99]
	s_waitcnt lgkmcnt(6)
	v_mfma_f32_16x16x32_f16 v[100:103], v[22:25], v[182:185], v[100:103]
	s_waitcnt lgkmcnt(5)
	v_mfma_f32_16x16x32_f16 v[104:107], v[22:25], v[186:189], v[104:107]
	s_waitcnt lgkmcnt(4)
	v_mfma_f32_16x16x32_f16 v[108:111], v[22:25], v[190:193], v[108:111]
	s_waitcnt lgkmcnt(3)
	v_mfma_f32_16x16x32_f16 v[112:115], v[22:25], v[194:197], v[112:115]
	s_waitcnt lgkmcnt(2)
	v_mfma_f32_16x16x32_f16 v[120:123], v[22:25], v[198:201], v[120:123]
	s_waitcnt lgkmcnt(1)
	v_mfma_f32_16x16x32_f16 v[124:127], v[22:25], v[202:205], v[124:127]
	s_waitcnt lgkmcnt(0)
	v_mfma_f32_16x16x32_f16 v[10:13], v[22:25], v[206:209], v[10:13]
	s_waitcnt vmcnt(13)
	v_mfma_f32_16x16x32_f16 v[22:25], v[30:33], v[18:21], v[26:29]
	v_mfma_f32_16x16x32_f16 v[26:29], v[30:33], v[182:185], v[128:131]
	v_mfma_f32_16x16x32_f16 v[128:131], v[30:33], v[186:189], v[146:149]
	v_mfma_f32_16x16x32_f16 v[146:149], v[30:33], v[190:193], v[150:153]
	v_mfma_f32_16x16x32_f16 v[150:153], v[30:33], v[194:197], v[154:157]
	v_mfma_f32_16x16x32_f16 v[154:157], v[30:33], v[198:201], v[158:161]
	v_mfma_f32_16x16x32_f16 v[158:161], v[30:33], v[202:205], v[162:165]
	v_mfma_f32_16x16x32_f16 v[2:5], v[30:33], v[206:209], v[2:5]
	s_waitcnt vmcnt(12)
	v_mfma_f32_16x16x32_f16 v[14:17], v[34:37], v[18:21], v[14:17]
	v_mfma_f32_16x16x32_f16 v[18:21], v[34:37], v[182:185], v[62:65]
	v_mfma_f32_16x16x32_f16 v[30:33], v[34:37], v[186:189], v[66:69]
	v_mfma_f32_16x16x32_f16 v[62:65], v[34:37], v[190:193], v[70:73]
	v_mfma_f32_16x16x32_f16 v[66:69], v[34:37], v[194:197], v[74:77]
	v_mfma_f32_16x16x32_f16 v[70:73], v[34:37], v[198:201], v[78:81]
	v_mfma_f32_16x16x32_f16 v[74:77], v[34:37], v[202:205], v[84:87]
	v_mfma_f32_16x16x32_f16 v[6:9], v[34:37], v[206:209], v[6:9]
	s_nop 0
	global_load_dwordx4 v[78:81], v[116:117], off offset:1024
	global_load_dwordx4 v[162:165], v[116:117], off offset:2048
	global_load_dwordx4 v[182:185], v[116:117], off offset:3072
	v_bitop3_b32 v34, v140, v145, 12 bitop3:0x36
	v_lshl_or_b32 v135, v34, 4, v220
	ds_read_b128 v[34:37], v135
	ds_read_b128 v[84:87], v135 offset:8192
	ds_read_b128 v[186:189], v135 offset:16384
	ds_read_b128 v[190:193], v135 offset:24576
	ds_read_b128 v[194:197], v135 offset:32768
	ds_read_b128 v[198:201], v135 offset:40960
	ds_read_b128 v[202:205], v135 offset:49152
	ds_read_b128 v[206:209], v135 offset:57344
	s_waitcnt vmcnt(14) lgkmcnt(7)
	v_mfma_f32_16x16x32_f16 v[96:99], v[38:41], v[34:37], v[96:99]
	s_waitcnt lgkmcnt(6)
	v_mfma_f32_16x16x32_f16 v[100:103], v[38:41], v[84:87], v[100:103]
	s_waitcnt lgkmcnt(5)
	v_mfma_f32_16x16x32_f16 v[104:107], v[38:41], v[186:189], v[104:107]
	s_waitcnt lgkmcnt(4)
	v_mfma_f32_16x16x32_f16 v[108:111], v[38:41], v[190:193], v[108:111]
	s_waitcnt lgkmcnt(3)
	v_mfma_f32_16x16x32_f16 v[112:115], v[38:41], v[194:197], v[112:115]
	s_waitcnt lgkmcnt(2)
	v_mfma_f32_16x16x32_f16 v[120:123], v[38:41], v[198:201], v[120:123]
	s_waitcnt lgkmcnt(1)
	v_mfma_f32_16x16x32_f16 v[124:127], v[38:41], v[202:205], v[124:127]
	s_waitcnt lgkmcnt(0)
	v_mfma_f32_16x16x32_f16 v[210:213], v[38:41], v[206:209], v[10:13]
	s_waitcnt vmcnt(13)
	v_mfma_f32_16x16x32_f16 v[22:25], v[42:45], v[34:37], v[22:25]
	v_mfma_f32_16x16x32_f16 v[214:217], v[42:45], v[84:87], v[26:29]
	v_mfma_f32_16x16x32_f16 v[128:131], v[42:45], v[186:189], v[128:131]
	v_mfma_f32_16x16x32_f16 v[146:149], v[42:45], v[190:193], v[146:149]
	v_mfma_f32_16x16x32_f16 v[150:153], v[42:45], v[194:197], v[150:153]
	v_mfma_f32_16x16x32_f16 v[154:157], v[42:45], v[198:201], v[154:157]
	v_mfma_f32_16x16x32_f16 v[158:161], v[42:45], v[202:205], v[158:161]
	v_mfma_f32_16x16x32_f16 v[2:5], v[42:45], v[206:209], v[2:5]
	s_waitcnt vmcnt(12)
	v_mfma_f32_16x16x32_f16 v[14:17], v[46:49], v[34:37], v[14:17]
	v_mfma_f32_16x16x32_f16 v[18:21], v[46:49], v[84:87], v[18:21]
	v_mfma_f32_16x16x32_f16 v[30:33], v[46:49], v[186:189], v[30:33]
	v_mfma_f32_16x16x32_f16 v[34:37], v[46:49], v[190:193], v[62:65]
	v_mfma_f32_16x16x32_f16 v[42:45], v[46:49], v[194:197], v[66:69]
	v_mfma_f32_16x16x32_f16 v[62:65], v[46:49], v[198:201], v[70:73]
	v_mfma_f32_16x16x32_f16 v[66:69], v[46:49], v[202:205], v[74:77]
	v_mfma_f32_16x16x32_f16 v[6:9], v[46:49], v[206:209], v[6:9]
	s_mov_b32 s8, 0x30000
	v_add_co_u32_e32 v116, vcc, s8, v118
	s_mov_b32 s8, 0x31000
	s_nop 0
	v_addc_co_u32_e32 v117, vcc, 0, v119, vcc
	v_add_co_u32_e32 v218, vcc, s8, v118
	v_bitop3_b32 v46, v140, v145, 16 bitop3:0x36
	s_nop 0
	v_addc_co_u32_e32 v219, vcc, 0, v119, vcc
	global_load_dwordx4 v[38:41], v[218:219], off offset:-4096
	global_load_dwordx4 v[26:29], v[116:117], off offset:1024
	global_load_dwordx4 v[10:13], v[116:117], off offset:2048
	v_lshl_or_b32 v136, v46, 4, v220
	ds_read_b128 v[46:49], v136
	ds_read_b128 v[70:73], v136 offset:8192
	ds_read_b128 v[74:77], v136 offset:16384
	ds_read_b128 v[84:87], v136 offset:24576
	ds_read_b128 v[186:189], v136 offset:32768
	ds_read_b128 v[190:193], v136 offset:40960
	ds_read_b128 v[194:197], v136 offset:49152
	ds_read_b128 v[198:201], v136 offset:57344
	s_waitcnt vmcnt(14) lgkmcnt(7)
	v_mfma_f32_16x16x32_f16 v[96:99], v[50:53], v[46:49], v[96:99]
	s_waitcnt lgkmcnt(6)
	v_mfma_f32_16x16x32_f16 v[100:103], v[50:53], v[70:73], v[100:103]
	s_waitcnt lgkmcnt(5)
	v_mfma_f32_16x16x32_f16 v[104:107], v[50:53], v[74:77], v[104:107]
	s_waitcnt lgkmcnt(4)
	v_mfma_f32_16x16x32_f16 v[108:111], v[50:53], v[84:87], v[108:111]
	s_waitcnt lgkmcnt(3)
	v_mfma_f32_16x16x32_f16 v[112:115], v[50:53], v[186:189], v[112:115]
	s_waitcnt lgkmcnt(2)
	v_mfma_f32_16x16x32_f16 v[120:123], v[50:53], v[190:193], v[120:123]
	s_waitcnt lgkmcnt(1)
	v_mfma_f32_16x16x32_f16 v[124:127], v[50:53], v[194:197], v[124:127]
	s_waitcnt lgkmcnt(0)
	v_mfma_f32_16x16x32_f16 v[50:53], v[50:53], v[198:201], v[210:213]
	s_waitcnt vmcnt(13)
	v_mfma_f32_16x16x32_f16 v[202:205], v[54:57], v[46:49], v[22:25]
	v_mfma_f32_16x16x32_f16 v[206:209], v[54:57], v[70:73], v[214:217]
	v_mfma_f32_16x16x32_f16 v[128:131], v[54:57], v[74:77], v[128:131]
	v_mfma_f32_16x16x32_f16 v[146:149], v[54:57], v[84:87], v[146:149]
	v_mfma_f32_16x16x32_f16 v[150:153], v[54:57], v[186:189], v[150:153]
	v_mfma_f32_16x16x32_f16 v[154:157], v[54:57], v[190:193], v[154:157]
	v_mfma_f32_16x16x32_f16 v[158:161], v[54:57], v[194:197], v[158:161]
	v_mfma_f32_16x16x32_f16 v[54:57], v[54:57], v[198:201], v[2:5]
	s_waitcnt vmcnt(12)
	v_mfma_f32_16x16x32_f16 v[14:17], v[58:61], v[46:49], v[14:17]
	v_mfma_f32_16x16x32_f16 v[18:21], v[58:61], v[70:73], v[18:21]
	v_mfma_f32_16x16x32_f16 v[30:33], v[58:61], v[74:77], v[30:33]
	v_mfma_f32_16x16x32_f16 v[34:37], v[58:61], v[84:87], v[34:37]
	v_mfma_f32_16x16x32_f16 v[42:45], v[58:61], v[186:189], v[42:45]
	v_mfma_f32_16x16x32_f16 v[46:49], v[58:61], v[190:193], v[62:65]
	v_mfma_f32_16x16x32_f16 v[62:65], v[58:61], v[194:197], v[66:69]
	v_mfma_f32_16x16x32_f16 v[58:61], v[58:61], v[198:201], v[6:9]
	global_load_dwordx4 v[22:25], v[116:117], off offset:3072
	s_nop 1
	global_load_dwordx4 v[6:9], v[218:219], off
	global_load_dwordx4 v[2:5], v[218:219], off offset:1024
	v_bitop3_b32 v66, v140, v145, 20 bitop3:0x36
	v_lshl_or_b32 v137, v66, 4, v220
	ds_read_b128 v[66:69], v137
	ds_read_b128 v[70:73], v137 offset:8192
	ds_read_b128 v[74:77], v137 offset:16384
	ds_read_b128 v[84:87], v137 offset:24576
	ds_read_b128 v[186:189], v137 offset:32768
	ds_read_b128 v[190:193], v137 offset:40960
	ds_read_b128 v[194:197], v137 offset:49152
	ds_read_b128 v[198:201], v137 offset:57344
	s_waitcnt vmcnt(14) lgkmcnt(7)
	v_mfma_f32_16x16x32_f16 v[96:99], v[92:95], v[66:69], v[96:99]
	s_waitcnt lgkmcnt(6)
	v_mfma_f32_16x16x32_f16 v[100:103], v[92:95], v[70:73], v[100:103]
	s_waitcnt lgkmcnt(5)
	v_mfma_f32_16x16x32_f16 v[104:107], v[92:95], v[74:77], v[104:107]
	s_waitcnt lgkmcnt(4)
	v_mfma_f32_16x16x32_f16 v[108:111], v[92:95], v[84:87], v[108:111]
	s_waitcnt lgkmcnt(3)
	v_mfma_f32_16x16x32_f16 v[112:115], v[92:95], v[186:189], v[112:115]
	s_waitcnt lgkmcnt(2)
	v_mfma_f32_16x16x32_f16 v[210:213], v[92:95], v[190:193], v[120:123]
	s_waitcnt lgkmcnt(1)
	v_mfma_f32_16x16x32_f16 v[124:127], v[92:95], v[194:197], v[124:127]
	s_waitcnt lgkmcnt(0)
	v_mfma_f32_16x16x32_f16 v[50:53], v[92:95], v[198:201], v[50:53]
	s_waitcnt vmcnt(13)
	v_mfma_f32_16x16x32_f16 v[92:95], v[170:173], v[66:69], v[202:205]
	v_mfma_f32_16x16x32_f16 v[202:205], v[170:173], v[70:73], v[206:209]
	v_mfma_f32_16x16x32_f16 v[128:131], v[170:173], v[74:77], v[128:131]
	v_mfma_f32_16x16x32_f16 v[146:149], v[170:173], v[84:87], v[146:149]
	v_mfma_f32_16x16x32_f16 v[150:153], v[170:173], v[186:189], v[150:153]
	v_mfma_f32_16x16x32_f16 v[154:157], v[170:173], v[190:193], v[154:157]
	v_mfma_f32_16x16x32_f16 v[158:161], v[170:173], v[194:197], v[158:161]
	v_mfma_f32_16x16x32_f16 v[54:57], v[170:173], v[198:201], v[54:57]
	s_waitcnt vmcnt(12)
	v_mfma_f32_16x16x32_f16 v[66:69], v[174:177], v[66:69], v[14:17]
	v_mfma_f32_16x16x32_f16 v[70:73], v[174:177], v[70:73], v[18:21]
	v_mfma_f32_16x16x32_f16 v[74:77], v[174:177], v[74:77], v[30:33]
	v_mfma_f32_16x16x32_f16 v[34:37], v[174:177], v[84:87], v[34:37]
	v_mfma_f32_16x16x32_f16 v[42:45], v[174:177], v[186:189], v[42:45]
	v_mfma_f32_16x16x32_f16 v[46:49], v[174:177], v[190:193], v[46:49]
	v_mfma_f32_16x16x32_f16 v[62:65], v[174:177], v[194:197], v[62:65]
	v_mfma_f32_16x16x32_f16 v[58:61], v[174:177], v[198:201], v[58:61]
	s_mov_b32 s8, 0x33000
	v_add_co_u32_e32 v122, vcc, s8, v118
	global_load_dwordx4 v[30:33], v[218:219], off offset:2048
	global_load_dwordx4 v[14:17], v[218:219], off offset:3072
	v_addc_co_u32_e32 v123, vcc, 0, v119, vcc
	global_load_dwordx4 v[18:21], v[122:123], off offset:-4096
	v_bitop3_b32 v84, v140, v145, 24 bitop3:0x36
	v_lshl_or_b32 v138, v84, 4, v220
	ds_read_b128 v[84:87], v138
	ds_read_b128 v[170:173], v138 offset:8192
	ds_read_b128 v[174:177], v138 offset:16384
	ds_read_b128 v[186:189], v138 offset:24576
	ds_read_b128 v[190:193], v138 offset:32768
	ds_read_b128 v[194:197], v138 offset:40960
	ds_read_b128 v[198:201], v138 offset:49152
	ds_read_b128 v[206:209], v138 offset:57344
	s_mov_b32 s8, 0x32000
	v_add_co_u32_e32 v116, vcc, s8, v118
	s_nop 1
	v_addc_co_u32_e32 v117, vcc, 0, v119, vcc
	s_waitcnt vmcnt(14) lgkmcnt(7)
	v_mfma_f32_16x16x32_f16 v[96:99], v[88:91], v[84:87], v[96:99]
	s_waitcnt lgkmcnt(6)
	v_mfma_f32_16x16x32_f16 v[100:103], v[88:91], v[170:173], v[100:103]
	s_waitcnt lgkmcnt(5)
	v_mfma_f32_16x16x32_f16 v[104:107], v[88:91], v[174:177], v[104:107]
	s_waitcnt lgkmcnt(4)
	v_mfma_f32_16x16x32_f16 v[108:111], v[88:91], v[186:189], v[108:111]
	s_waitcnt lgkmcnt(3)
	v_mfma_f32_16x16x32_f16 v[112:115], v[88:91], v[190:193], v[112:115]
	s_waitcnt lgkmcnt(2)
	v_mfma_f32_16x16x32_f16 v[210:213], v[88:91], v[194:197], v[210:213]
	s_waitcnt lgkmcnt(1)
	v_mfma_f32_16x16x32_f16 v[124:127], v[88:91], v[198:201], v[124:127]
	s_waitcnt lgkmcnt(0)
	v_mfma_f32_16x16x32_f16 v[50:53], v[88:91], v[206:209], v[50:53]
	s_waitcnt vmcnt(13)
	v_mfma_f32_16x16x32_f16 v[90:93], v[166:169], v[84:87], v[92:95]
	v_mfma_f32_16x16x32_f16 v[202:205], v[166:169], v[170:173], v[202:205]
	v_mfma_f32_16x16x32_f16 v[128:131], v[166:169], v[174:177], v[128:131]
	v_mfma_f32_16x16x32_f16 v[146:149], v[166:169], v[186:189], v[146:149]
	v_mfma_f32_16x16x32_f16 v[150:153], v[166:169], v[190:193], v[150:153]
	v_mfma_f32_16x16x32_f16 v[154:157], v[166:169], v[194:197], v[154:157]
	v_mfma_f32_16x16x32_f16 v[158:161], v[166:169], v[198:201], v[158:161]
	v_mfma_f32_16x16x32_f16 v[54:57], v[166:169], v[206:209], v[54:57]
	s_waitcnt vmcnt(12)
	v_mfma_f32_16x16x32_f16 v[166:169], v[178:181], v[84:87], v[66:69]
	v_mfma_f32_16x16x32_f16 v[170:173], v[178:181], v[170:173], v[70:73]
	v_mfma_f32_16x16x32_f16 v[174:177], v[178:181], v[174:177], v[74:77]
	v_mfma_f32_16x16x32_f16 v[186:189], v[178:181], v[186:189], v[34:37]
	v_mfma_f32_16x16x32_f16 v[190:193], v[178:181], v[190:193], v[42:45]
	v_mfma_f32_16x16x32_f16 v[194:197], v[178:181], v[194:197], v[46:49]
	v_mfma_f32_16x16x32_f16 v[198:201], v[178:181], v[198:201], v[62:65]
	v_mfma_f32_16x16x32_f16 v[178:181], v[178:181], v[206:209], v[58:61]
	s_nop 0
	global_load_dwordx4 v[46:49], v[116:117], off offset:1024
	global_load_dwordx4 v[42:45], v[116:117], off offset:2048
	global_load_dwordx4 v[34:37], v[116:117], off offset:3072
	v_bitop3_b32 v58, v140, v145, 28 bitop3:0x36
	v_lshl_or_b32 v140, v58, 4, v220
	ds_read_b128 v[58:61], v140
	ds_read_b128 v[62:65], v140 offset:8192
	ds_read_b128 v[206:209], v140 offset:16384
	ds_read_b128 v[214:217], v140 offset:24576
	ds_read_b128 v[218:221], v140 offset:32768
	ds_read_b128 v[222:225], v140 offset:40960
	ds_read_b128 v[226:229], v140 offset:49152
	ds_read_b128 v[230:233], v140 offset:57344
	s_waitcnt vmcnt(14) lgkmcnt(7)
	v_mfma_f32_16x16x32_f16 v[234:237], v[78:81], v[58:61], v[96:99]
	s_waitcnt lgkmcnt(6)
	v_mfma_f32_16x16x32_f16 v[238:241], v[78:81], v[62:65], v[100:103]
	s_waitcnt lgkmcnt(5)
	v_mfma_f32_16x16x32_f16 v[242:245], v[78:81], v[206:209], v[104:107]
	s_waitcnt lgkmcnt(4)
	v_mfma_f32_16x16x32_f16 v[246:249], v[78:81], v[214:217], v[108:111]
	s_waitcnt lgkmcnt(3)
	v_mfma_f32_16x16x32_f16 v[106:109], v[78:81], v[218:221], v[112:115]
	s_waitcnt lgkmcnt(2)
	v_mfma_f32_16x16x32_f16 v[102:105], v[78:81], v[222:225], v[210:213]
	s_waitcnt lgkmcnt(1)
	v_mfma_f32_16x16x32_f16 v[94:97], v[78:81], v[226:229], v[124:127]
	s_waitcnt lgkmcnt(0)
	v_mfma_f32_16x16x32_f16 v[86:89], v[78:81], v[230:233], v[50:53]
	s_waitcnt vmcnt(13)
	v_mfma_f32_16x16x32_f16 v[124:127], v[162:165], v[58:61], v[90:93]
	v_mfma_f32_16x16x32_f16 v[202:205], v[162:165], v[62:65], v[202:205]
	v_mfma_f32_16x16x32_f16 v[210:213], v[162:165], v[206:209], v[128:131]
	v_mfma_f32_16x16x32_f16 v[146:149], v[162:165], v[214:217], v[146:149]
	v_mfma_f32_16x16x32_f16 v[78:81], v[162:165], v[218:221], v[150:153]
	v_mfma_f32_16x16x32_f16 v[74:77], v[162:165], v[222:225], v[154:157]
	v_mfma_f32_16x16x32_f16 v[70:73], v[162:165], v[226:229], v[158:161]
	v_mfma_f32_16x16x32_f16 v[66:69], v[162:165], v[230:233], v[54:57]
	s_waitcnt vmcnt(12)
	v_mfma_f32_16x16x32_f16 v[150:153], v[182:185], v[58:61], v[166:169]
	v_mfma_f32_16x16x32_f16 v[154:157], v[182:185], v[62:65], v[170:173]
	v_mfma_f32_16x16x32_f16 v[114:117], v[182:185], v[206:209], v[174:177]
	v_mfma_f32_16x16x32_f16 v[110:113], v[182:185], v[214:217], v[186:189]
	v_mfma_f32_16x16x32_f16 v[62:65], v[182:185], v[218:221], v[190:193]
	v_mfma_f32_16x16x32_f16 v[58:61], v[182:185], v[222:225], v[194:197]
	v_mfma_f32_16x16x32_f16 v[54:57], v[182:185], v[226:229], v[198:201]
	v_mfma_f32_16x16x32_f16 v[50:53], v[182:185], v[230:233], v[178:181]
	v_lshl_add_u64 v[120:121], v[82:83], 2, s[4:5]
	global_load_dwordx4 v[98:101], v[120:121], off
	global_load_dwordx4 v[90:93], v[120:121], off offset:64
	global_load_dwordx4 v[82:85], v[120:121], off offset:128
	s_movk_i32 s5, 0x310
	v_mad_u32_u24 v130, v145, s5, v250
	v_mov_b32_e32 v158, v239
	v_mov_b32_e32 v159, v240
	v_mov_b32_e32 v160, v243
	v_mov_b32_e32 v161, v244
	v_mov_b32_e32 v162, v247
	v_mov_b32_e32 v163, v248
	v_mov_b32_e32 v164, v203
	v_mov_b32_e32 v165, v204
	v_mov_b32_e32 v169, v148
	v_mov_b32_e32 v166, v211
	v_mov_b32_e32 v167, v212
	v_mov_b32_e32 v168, v147
	s_barrier
	v_add_u32_e32 v132, 0x3000, v130
	v_add_u32_e32 v131, 0x6000, v130
	s_mov_b32 s4, 0xfffffd0
	v_mul_lo_u32 v176, v143, s4
	s_waitcnt vmcnt(2)
	v_pk_add_f32 v[170:171], v[234:235], v[98:99]
	v_pk_add_f32 v[172:173], v[236:237], v[100:101]
	v_add_f32_e32 v145, v238, v98
	v_pk_mov_b32 v[128:129], v[98:99], v[100:101] op_sel:[1,0]
	v_add_f32_e32 v99, v241, v101
	s_waitcnt vmcnt(1)
	v_pk_add_f32 v[124:125], v[124:125], v[90:91]
	v_pk_add_f32 v[174:175], v[126:127], v[92:93]
	v_add_f32_e32 v180, v202, v90
	v_pk_mov_b32 v[126:127], v[90:91], v[92:93] op_sel:[1,0]
	v_add_f32_e32 v91, v205, v93
	v_add_f32_e32 v100, v242, v98
	v_add_f32_e32 v177, v245, v101
	v_add_f32_e32 v92, v210, v90
	v_add_f32_e32 v181, v213, v93
	v_add_f32_e32 v183, v149, v93
	v_cvt_pk_f16_f32 v149, v172, v173
	v_cvt_f16_f32_e32 v145, v145
	v_cvt_f16_f32_e32 v99, v99
	v_cvt_f16_f32_e32 v173, v180
	v_cvt_f16_f32_e32 v91, v91
	v_cvt_pk_f16_f32 v148, v170, v171
	v_cvt_f16_f32_e32 v100, v100
	v_cvt_f16_f32_e32 v170, v177
	v_cvt_pk_f16_f32 v124, v124, v125
	v_cvt_pk_f16_f32 v125, v174, v175
	v_cvt_f16_f32_e32 v92, v92
	v_cvt_f16_f32_e32 v174, v181
	v_add_f32_e32 v182, v146, v90
	s_waitcnt vmcnt(0)
	v_pk_add_f32 v[146:147], v[150:151], v[82:83]
	v_pk_add_f32 v[150:151], v[158:159], v[128:129]
	v_pk_add_f32 v[158:159], v[160:161], v[128:129]
	v_pk_add_f32 v[160:161], v[162:163], v[128:129]
	v_pk_add_f32 v[162:163], v[164:165], v[126:127]
	v_pk_add_f32 v[164:165], v[166:167], v[126:127]
	v_cvt_pk_f16_f32 v146, v146, v147
	v_cvt_pk_f16_f32 v147, v150, v151
	v_cvt_pk_f16_f32 v150, v158, v159
	v_cvt_pk_f16_f32 v159, v162, v163
	v_cvt_pk_f16_f32 v151, v160, v161
	v_cvt_pk_f16_f32 v161, v164, v165
	ds_write2_b64 v130, v[148:149], v[124:125] offset1:4
	v_pack_b32_f16 v124, v145, v147
	v_alignbit_b32 v125, v99, v147, 16
	v_pack_b32_f16 v158, v173, v159
	v_alignbit_b32 v159, v91, v159, 16
	v_pack_b32_f16 v148, v100, v150
	v_alignbit_b32 v149, v170, v150, 16
	v_pack_b32_f16 v160, v92, v161
	v_alignbit_b32 v161, v174, v161, 16
	ds_write2_b64 v132, v[124:125], v[158:159] offset0:32 offset1:36
	ds_write2_b64 v131, v[148:149], v[160:161] offset0:64 offset1:68
	v_pk_add_f32 v[124:125], v[152:153], v[84:85]
	v_add_f32_e32 v92, v154, v82
	v_cvt_pk_f16_f32 v147, v124, v125
	v_pk_mov_b32 v[124:125], v[82:83], v[84:85] op_sel:[1,0]
	v_add_f32_e32 v83, v157, v85
	v_cvt_f16_f32_e32 v92, v92
	v_cvt_f16_f32_e32 v83, v83
	ds_write_b64 v130, v[146:147] offset:64
	v_mov_b32_e32 v146, v155
	v_mov_b32_e32 v147, v156
	v_pk_add_f32 v[146:147], v[146:147], v[124:125]
	v_add_f32_e32 v178, v246, v98
	v_cvt_pk_f16_f32 v84, v146, v147
	v_pack_b32_f16 v146, v92, v84
	v_alignbit_b32 v147, v83, v84, 16
	v_add_f32_e32 v83, v114, v82
	v_add_f32_e32 v84, v117, v85
	v_cvt_f16_f32_e32 v83, v83
	v_cvt_f16_f32_e32 v84, v84
	v_mov_b32_e32 v114, v115
	v_mov_b32_e32 v115, v116
	v_pk_add_f32 v[114:115], v[114:115], v[124:125]
	v_add_f32_e32 v179, v249, v101
	v_cvt_pk_f16_f32 v92, v114, v115
	v_pack_b32_f16 v114, v83, v92
	v_alignbit_b32 v115, v84, v92, 16
	v_add_f32_e32 v83, v110, v82
	v_add_f32_e32 v84, v113, v85
	v_cvt_f16_f32_e32 v83, v83
	v_cvt_f16_f32_e32 v84, v84
	v_mov_b32_e32 v110, v111
	v_mov_b32_e32 v111, v112
	v_cvt_f16_f32_e32 v171, v178
	v_cvt_f16_f32_e32 v172, v179
	v_cvt_f16_f32_e32 v175, v182
	v_pk_add_f32 v[166:167], v[168:169], v[126:127]
	v_cvt_f16_f32_e32 v168, v183
	v_pk_add_f32 v[110:111], v[110:111], v[124:125]
	v_cvt_pk_f16_f32 v163, v166, v167
	v_cvt_pk_f16_f32 v92, v110, v111
	v_pack_b32_f16 v110, v83, v92
	v_alignbit_b32 v111, v84, v92, 16
	v_or_b32_e32 v83, s16, v143
	ds_write_b64 v130, v[110:111] offset:37696
	v_add_lshl_u32 v111, v176, v0, 4
	v_mul_lo_u32 v112, v83, s6
	v_mul_u32_u24_e32 v83, 0x310, v143
	v_mul_u32_u24_e32 v84, 0x556, v141
	v_pack_b32_f16 v150, v171, v151
	v_alignbit_b32 v151, v172, v151, 16
	v_pack_b32_f16 v162, v175, v163
	v_alignbit_b32 v163, v168, v163, 16
	v_add_u32_e32 v91, 0x9000, v130
	v_add3_u32 v83, v111, v83, s14
	v_lshrrev_b32_e32 v154, 16, v84
	ds_write2_b64 v91, v[150:151], v[162:163] offset0:96 offset1:100
	ds_write_b64 v130, v[146:147] offset:12608
	ds_write_b64 v130, v[114:115] offset:25152
	s_waitcnt lgkmcnt(0)
	s_barrier
	ds_read_b128 v[114:117], v83
	v_mul_lo_u32 v84, v154, s4
	v_add_lshl_u32 v113, v84, v141, 4
	v_mul_u32_u24_e32 v84, 0x310, v154
	v_add3_u32 v84, v113, v84, s14
	ds_read_b128 v[146:149], v84
	v_add_u32_e32 v92, v111, v112
	s_waitcnt lgkmcnt(1)
	buffer_store_dwordx4 v[114:117], v92, s[0:3], 0 offen sc1
	v_or_b32_e32 v92, s16, v154
	s_nop 0
	v_mul_lo_u32 v114, v92, s6
	v_add_u32_e32 v92, v113, v114
	s_waitcnt lgkmcnt(0)
	buffer_store_dwordx4 v[146:149], v92, s[0:3], 0 offen sc1
	v_or_b32_e32 v92, 0x400, v0
	v_mul_u32_u24_e32 v99, 0x556, v92
	v_lshrrev_b32_e32 v155, 16, v99
	v_mul_lo_u32 v99, v155, s4
	v_add_lshl_u32 v115, v99, v92, 4
	v_mul_u32_u24_e32 v92, 0x310, v155
	v_mul_u32_u24_e32 v99, 0x556, v142
	v_add3_u32 v92, v115, v92, s14
	v_lshrrev_b32_e32 v156, 16, v99
	ds_read_b128 v[146:149], v92
	v_mul_lo_u32 v99, v156, s4
	v_add_lshl_u32 v117, v99, v142, 4
	v_mul_u32_u24_e32 v99, 0x310, v156
	v_or_b32_e32 v100, s16, v155
	v_add3_u32 v99, v117, v99, s14
	v_mul_lo_u32 v116, v100, s6
	ds_read_b128 v[150:153], v99
	v_add_u32_e32 v100, v115, v116
	s_waitcnt lgkmcnt(1)
	buffer_store_dwordx4 v[146:149], v100, s[0:3], 0 offen sc1
	v_or_b32_e32 v100, s16, v156
	v_mul_lo_u32 v142, v100, s6
	v_add_u32_e32 v100, v117, v142
	v_or_b32_e32 v0, 0x800, v0
	s_waitcnt lgkmcnt(0)
	buffer_store_dwordx4 v[150:153], v100, s[0:3], 0 offen sc1
	v_mul_u32_u24_e32 v100, 0xaab, v0
	v_lshrrev_b32_e32 v157, 17, v100
	v_mul_lo_u32 v100, v157, s4
	v_or_b32_e32 v110, s16, v157
	v_add_lshl_u32 v143, v100, v0, 4
	v_mul_lo_u32 v141, v110, s6
	v_mul_u32_u24_e32 v100, 0x310, v157
	v_mul_u32_u24_e32 v110, 0xaab, v144
	v_add3_u32 v100, v100, v143, s14
	v_lshrrev_b32_e32 v158, 17, v110
	ds_read_b128 v[146:149], v100
	v_mul_lo_u32 v110, v158, s4
	v_add_lshl_u32 v144, v110, v144, 4
	v_mul_u32_u24_e32 v110, 0x310, v158
	v_add3_u32 v110, v110, v144, s14
	ds_read_b128 v[150:153], v110
	v_add_u32_e32 v0, v143, v141
	s_waitcnt lgkmcnt(1)
	buffer_store_dwordx4 v[146:149], v0, s[0:3], 0 offen sc1
	v_or_b32_e32 v0, s16, v158
	v_mul_lo_u32 v145, v0, s6
	v_add_u32_e32 v0, v144, v145
	s_waitcnt lgkmcnt(0)
	buffer_store_dwordx4 v[150:153], v0, s[0:3], 0 offen sc1
	v_add_f32_e32 v0, v106, v98
	v_cvt_f16_f32_e32 v0, v0
	v_mov_b32_e32 v106, v107
	v_mov_b32_e32 v107, v108
	v_pk_add_f32 v[106:107], v[106:107], v[128:129]
	v_add_f32_e32 v108, v109, v101
	v_cvt_pk_f16_f32 v107, v106, v107
	v_pack_b32_f16 v106, v0, v107
	v_add_f32_e32 v0, v102, v98
	v_cvt_f16_f32_e32 v0, v0
	v_mov_b32_e32 v102, v103
	v_mov_b32_e32 v103, v104
	v_pk_add_f32 v[102:103], v[102:103], v[128:129]
	v_add_f32_e32 v104, v105, v101
	v_cvt_pk_f16_f32 v103, v102, v103
	v_pack_b32_f16 v102, v0, v103
	v_add_f32_e32 v0, v94, v98
	v_cvt_f16_f32_e32 v0, v0
	v_mov_b32_e32 v94, v95
	v_mov_b32_e32 v95, v96
	v_pk_add_f32 v[94:95], v[94:95], v[128:129]
	v_add_f32_e32 v96, v97, v101
	v_cvt_pk_f16_f32 v95, v94, v95
	v_pack_b32_f16 v94, v0, v95
	v_add_f32_e32 v0, v86, v98
	v_cvt_f16_f32_e32 v0, v0
	v_mov_b32_e32 v86, v87
	v_mov_b32_e32 v87, v88
	v_pk_add_f32 v[86:87], v[86:87], v[128:129]
	v_add_f32_e32 v88, v89, v101
	v_cvt_pk_f16_f32 v87, v86, v87
	v_pack_b32_f16 v86, v0, v87
	v_add_f32_e32 v0, v78, v90
	v_cvt_f16_f32_e32 v0, v0
	v_mov_b32_e32 v78, v79
	v_mov_b32_e32 v79, v80
	v_pk_add_f32 v[78:79], v[78:79], v[126:127]
	v_add_f32_e32 v80, v81, v93
	v_cvt_pk_f16_f32 v79, v78, v79
	v_pack_b32_f16 v78, v0, v79
	v_add_f32_e32 v0, v74, v90
	v_cvt_f16_f32_e32 v0, v0
	v_mov_b32_e32 v74, v75
	v_mov_b32_e32 v75, v76
	v_pk_add_f32 v[74:75], v[74:75], v[126:127]
	v_add_f32_e32 v76, v77, v93
	v_cvt_pk_f16_f32 v75, v74, v75
	v_pack_b32_f16 v74, v0, v75
	v_add_f32_e32 v0, v70, v90
	v_cvt_f16_f32_e32 v0, v0
	v_mov_b32_e32 v70, v71
	v_mov_b32_e32 v71, v72
	v_pk_add_f32 v[70:71], v[70:71], v[126:127]
	v_add_f32_e32 v72, v73, v93
	v_cvt_pk_f16_f32 v71, v70, v71
	v_pack_b32_f16 v70, v0, v71
	v_add_f32_e32 v0, v66, v90
	v_cvt_f16_f32_e32 v0, v0
	v_mov_b32_e32 v66, v67
	v_mov_b32_e32 v67, v68
	v_pk_add_f32 v[66:67], v[66:67], v[126:127]
	v_add_f32_e32 v68, v69, v93
	v_cvt_pk_f16_f32 v67, v66, v67
	v_pack_b32_f16 v66, v0, v67
	v_add_f32_e32 v0, v62, v82
	v_cvt_f16_f32_e32 v0, v0
	v_mov_b32_e32 v62, v63
	v_mov_b32_e32 v63, v64
	v_pk_add_f32 v[62:63], v[62:63], v[124:125]
	v_add_f32_e32 v64, v65, v85
	v_cvt_pk_f16_f32 v63, v62, v63
	v_pack_b32_f16 v62, v0, v63
	v_add_f32_e32 v0, v58, v82
	v_cvt_f16_f32_e32 v0, v0
	v_mov_b32_e32 v58, v59
	v_mov_b32_e32 v59, v60
	v_pk_add_f32 v[58:59], v[58:59], v[124:125]
	v_add_f32_e32 v60, v61, v85
	v_cvt_pk_f16_f32 v59, v58, v59
	v_pack_b32_f16 v58, v0, v59
	v_add_f32_e32 v0, v54, v82
	v_cvt_f16_f32_e32 v0, v0
	v_mov_b32_e32 v54, v55
	v_mov_b32_e32 v55, v56
	v_pk_add_f32 v[54:55], v[54:55], v[124:125]
	v_add_f32_e32 v56, v57, v85
	v_cvt_pk_f16_f32 v55, v54, v55
	v_pack_b32_f16 v54, v0, v55
	v_add_f32_e32 v0, v50, v82
	v_mov_b32_e32 v50, v51
	v_mov_b32_e32 v51, v52
	v_add_f32_e32 v52, v53, v85
	v_cvt_f16_f32_e32 v108, v108
	v_cvt_f16_f32_e32 v104, v104
	v_cvt_f16_f32_e32 v96, v96
	v_cvt_f16_f32_e32 v88, v88
	v_cvt_f16_f32_e32 v80, v80
	v_cvt_f16_f32_e32 v76, v76
	v_cvt_f16_f32_e32 v72, v72
	v_cvt_f16_f32_e32 v68, v68
	v_cvt_f16_f32_e32 v64, v64
	v_cvt_f16_f32_e32 v60, v60
	v_cvt_f16_f32_e32 v56, v56
	v_cvt_f16_f32_e32 v0, v0
	v_cvt_f16_f32_e32 v52, v52
	v_pk_add_f32 v[50:51], v[50:51], v[124:125]
	v_alignbit_b32 v107, v108, v107, 16
	v_cvt_pk_f16_f32 v51, v50, v51
	v_alignbit_b32 v103, v104, v103, 16
	v_alignbit_b32 v95, v96, v95, 16
	v_alignbit_b32 v87, v88, v87, 16
	v_alignbit_b32 v79, v80, v79, 16
	v_alignbit_b32 v75, v76, v75, 16
	v_alignbit_b32 v71, v72, v71, 16
	v_alignbit_b32 v67, v68, v67, 16
	v_alignbit_b32 v63, v64, v63, 16
	v_alignbit_b32 v59, v60, v59, 16
	v_alignbit_b32 v55, v56, v55, 16
	v_pack_b32_f16 v50, v0, v51
	v_alignbit_b32 v51, v52, v51, 16
	s_barrier
	ds_write2_b64 v130, v[106:107], v[78:79] offset1:4
	ds_write2_b64 v132, v[102:103], v[74:75] offset0:32 offset1:36
	ds_write2_b64 v131, v[94:95], v[70:71] offset0:64 offset1:68
	ds_write2_b64 v91, v[86:87], v[66:67] offset0:96 offset1:100
	ds_write_b64 v130, v[62:63] offset:64
	ds_write_b64 v130, v[58:59] offset:12608
	ds_write_b64 v130, v[54:55] offset:25152
	ds_write_b64 v130, v[50:51] offset:37696
	s_waitcnt lgkmcnt(0)
	s_barrier
	global_load_dwordx4 v[50:53], v[122:123], off
	global_load_dwordx4 v[54:57], v[122:123], off offset:1024
	global_load_dwordx4 v[58:61], v[122:123], off offset:2048
	ds_read_b128 v[62:65], v83
	ds_read_b128 v[70:73], v84
	v_mul_lo_u32 v68, v139, s6
	v_add_u32_e32 v0, v68, v111
	ds_read_b128 v[74:77], v99
	s_waitcnt lgkmcnt(2)
	buffer_store_dwordx4 v[62:65], v0, s[0:3], 0 offen sc1
	v_or_b32_e32 v0, s7, v154
	v_mul_lo_u32 v69, v0, s6
	ds_read_b128 v[62:65], v92
	v_add_u32_e32 v0, v113, v69
	s_waitcnt lgkmcnt(2)
	buffer_store_dwordx4 v[70:73], v0, s[0:3], 0 offen sc1
	v_or_b32_e32 v0, s7, v155
	s_nop 0
	v_mul_lo_u32 v72, v0, s6
	v_add_u32_e32 v0, v115, v72
	s_waitcnt lgkmcnt(0)
	buffer_store_dwordx4 v[62:65], v0, s[0:3], 0 offen sc1
	v_or_b32_e32 v0, s7, v156
	v_mul_lo_u32 v70, v0, s6
	ds_read_b128 v[62:65], v100
	v_add_u32_e32 v0, v117, v70
	buffer_store_dwordx4 v[74:77], v0, s[0:3], 0 offen sc1
	v_or_b32_e32 v0, s7, v157
	v_mul_lo_u32 v71, v0, s6
	v_add_u32_e32 v0, v143, v71
	ds_read_b128 v[74:77], v110
	s_waitcnt lgkmcnt(1)
	buffer_store_dwordx4 v[62:65], v0, s[0:3], 0 offen sc1
	ds_read_b128 v[62:65], v134
	ds_read_b128 v[78:81], v134 offset:8192
	ds_read_b128 v[86:89], v134 offset:16384
	ds_read_b128 v[94:97], v134 offset:24576
	ds_read_b128 v[102:105], v134 offset:32768
	ds_read_b128 v[106:109], v134 offset:40960
	ds_read_b128 v[124:127], v134 offset:49152
	ds_read_b128 v[146:149], v134 offset:57344
	v_or_b32_e32 v0, s7, v158
	v_mul_lo_u32 v73, v0, s6
	v_add_u32_e32 v0, v144, v73
	s_waitcnt lgkmcnt(8)
	buffer_store_dwordx4 v[74:77], v0, s[0:3], 0 offen sc1
	s_waitcnt lgkmcnt(7)
	s_nop 0
	v_mfma_f32_16x16x32_f16 v[74:77], v[38:41], v[62:65], 0
	s_waitcnt lgkmcnt(6)
	v_mfma_f32_16x16x32_f16 v[150:153], v[38:41], v[78:81], 0
	s_waitcnt lgkmcnt(5)
	v_mfma_f32_16x16x32_f16 v[154:157], v[38:41], v[86:89], 0
	s_waitcnt lgkmcnt(4)
	v_mfma_f32_16x16x32_f16 v[158:161], v[38:41], v[94:97], 0
	s_waitcnt lgkmcnt(3)
	v_mfma_f32_16x16x32_f16 v[162:165], v[38:41], v[102:105], 0
	s_waitcnt lgkmcnt(2)
	v_mfma_f32_16x16x32_f16 v[166:169], v[38:41], v[106:109], 0
	s_waitcnt lgkmcnt(1)
	v_mfma_f32_16x16x32_f16 v[170:173], v[38:41], v[124:127], 0
	s_waitcnt lgkmcnt(0)
	v_mfma_f32_16x16x32_f16 v[38:41], v[38:41], v[146:149], 0
	v_mfma_f32_16x16x32_f16 v[174:177], v[26:29], v[62:65], 0
	v_mfma_f32_16x16x32_f16 v[178:181], v[26:29], v[78:81], 0
	v_mfma_f32_16x16x32_f16 v[182:185], v[26:29], v[86:89], 0
	v_mfma_f32_16x16x32_f16 v[186:189], v[26:29], v[94:97], 0
	v_mfma_f32_16x16x32_f16 v[190:193], v[26:29], v[102:105], 0
	v_mfma_f32_16x16x32_f16 v[194:197], v[26:29], v[106:109], 0
	v_mfma_f32_16x16x32_f16 v[198:201], v[26:29], v[124:127], 0
	v_mfma_f32_16x16x32_f16 v[26:29], v[26:29], v[146:149], 0
	v_mfma_f32_16x16x32_f16 v[62:65], v[10:13], v[62:65], 0
	v_mfma_f32_16x16x32_f16 v[78:81], v[10:13], v[78:81], 0
	v_mfma_f32_16x16x32_f16 v[86:89], v[10:13], v[86:89], 0
	v_mfma_f32_16x16x32_f16 v[94:97], v[10:13], v[94:97], 0
	v_mfma_f32_16x16x32_f16 v[102:105], v[10:13], v[102:105], 0
	v_mfma_f32_16x16x32_f16 v[106:109], v[10:13], v[106:109], 0
	v_mfma_f32_16x16x32_f16 v[124:127], v[10:13], v[124:127], 0
	v_mfma_f32_16x16x32_f16 v[10:13], v[10:13], v[146:149], 0
	s_mov_b32 s4, 0x34000
	v_add_co_u32_e32 v66, vcc, s4, v118
	s_mov_b32 s4, 0x35000
	s_nop 0
	v_addc_co_u32_e32 v67, vcc, 0, v119, vcc
	v_add_co_u32_e32 v118, vcc, s4, v118
	s_nop 1
	v_addc_co_u32_e32 v119, vcc, 0, v119, vcc
	global_load_dwordx4 v[146:149], v[118:119], off offset:-4096
	global_load_dwordx4 v[202:205], v[122:123], off offset:3072
	global_load_dwordx4 v[206:209], v[66:67], off offset:1024
	ds_read_b128 v[210:213], v1
	ds_read_b128 v[214:217], v1 offset:8192
	ds_read_b128 v[218:221], v1 offset:16384
	ds_read_b128 v[222:225], v1 offset:24576
	ds_read_b128 v[226:229], v1 offset:32768
	ds_read_b128 v[230:233], v1 offset:40960
	ds_read_b128 v[234:237], v1 offset:49152
	ds_read_b128 v[238:241], v1 offset:57344
	s_waitcnt lgkmcnt(7)
	v_mfma_f32_16x16x32_f16 v[74:77], v[22:25], v[210:213], v[74:77]
	s_waitcnt lgkmcnt(6)
	v_mfma_f32_16x16x32_f16 v[150:153], v[22:25], v[214:217], v[150:153]
	s_waitcnt lgkmcnt(5)
	v_mfma_f32_16x16x32_f16 v[154:157], v[22:25], v[218:221], v[154:157]
	s_waitcnt lgkmcnt(4)
	v_mfma_f32_16x16x32_f16 v[158:161], v[22:25], v[222:225], v[158:161]
	s_waitcnt lgkmcnt(3)
	v_mfma_f32_16x16x32_f16 v[162:165], v[22:25], v[226:229], v[162:165]
	s_waitcnt lgkmcnt(2)
	v_mfma_f32_16x16x32_f16 v[166:169], v[22:25], v[230:233], v[166:169]
	s_waitcnt lgkmcnt(1)
	v_mfma_f32_16x16x32_f16 v[170:173], v[22:25], v[234:237], v[170:173]
	s_waitcnt lgkmcnt(0)
	v_mfma_f32_16x16x32_f16 v[22:25], v[22:25], v[238:241], v[38:41]
	v_mfma_f32_16x16x32_f16 v[38:41], v[6:9], v[210:213], v[174:177]
	v_mfma_f32_16x16x32_f16 v[174:177], v[6:9], v[214:217], v[178:181]
	v_mfma_f32_16x16x32_f16 v[178:181], v[6:9], v[218:221], v[182:185]
	v_mfma_f32_16x16x32_f16 v[182:185], v[6:9], v[222:225], v[186:189]
	v_mfma_f32_16x16x32_f16 v[186:189], v[6:9], v[226:229], v[190:193]
	v_mfma_f32_16x16x32_f16 v[190:193], v[6:9], v[230:233], v[194:197]
	v_mfma_f32_16x16x32_f16 v[194:197], v[6:9], v[234:237], v[198:201]
	v_mfma_f32_16x16x32_f16 v[6:9], v[6:9], v[238:241], v[26:29]
	v_mfma_f32_16x16x32_f16 v[26:29], v[2:5], v[210:213], v[62:65]
	v_mfma_f32_16x16x32_f16 v[62:65], v[2:5], v[214:217], v[78:81]
	v_mfma_f32_16x16x32_f16 v[78:81], v[2:5], v[218:221], v[86:89]
	v_mfma_f32_16x16x32_f16 v[86:89], v[2:5], v[222:225], v[94:97]
	v_mfma_f32_16x16x32_f16 v[94:97], v[2:5], v[226:229], v[102:105]
	v_mfma_f32_16x16x32_f16 v[102:105], v[2:5], v[230:233], v[106:109]
	v_mfma_f32_16x16x32_f16 v[106:109], v[2:5], v[234:237], v[124:127]
	v_mfma_f32_16x16x32_f16 v[0:3], v[2:5], v[238:241], v[10:13]
	s_nop 2
	global_load_dwordx4 v[10:13], v[66:67], off offset:2048
	global_load_dwordx4 v[122:125], v[66:67], off offset:3072
	global_load_dwordx4 v[126:129], v[118:119], off
	ds_read_b128 v[198:201], v133
	ds_read_b128 v[210:213], v133 offset:8192
	ds_read_b128 v[214:217], v133 offset:16384
	ds_read_b128 v[218:221], v133 offset:24576
	ds_read_b128 v[222:225], v133 offset:32768
	ds_read_b128 v[226:229], v133 offset:40960
	ds_read_b128 v[230:233], v133 offset:49152
	ds_read_b128 v[234:237], v133 offset:57344
	s_waitcnt lgkmcnt(7)
	v_mfma_f32_16x16x32_f16 v[74:77], v[30:33], v[198:201], v[74:77]
	s_waitcnt lgkmcnt(6)
	v_mfma_f32_16x16x32_f16 v[150:153], v[30:33], v[210:213], v[150:153]
	s_waitcnt lgkmcnt(5)
	v_mfma_f32_16x16x32_f16 v[154:157], v[30:33], v[214:217], v[154:157]
	s_waitcnt lgkmcnt(4)
	v_mfma_f32_16x16x32_f16 v[158:161], v[30:33], v[218:221], v[158:161]
	s_waitcnt lgkmcnt(3)
	v_mfma_f32_16x16x32_f16 v[162:165], v[30:33], v[222:225], v[162:165]
	s_waitcnt lgkmcnt(2)
	v_mfma_f32_16x16x32_f16 v[166:169], v[30:33], v[226:229], v[166:169]
	s_waitcnt lgkmcnt(1)
	v_mfma_f32_16x16x32_f16 v[170:173], v[30:33], v[230:233], v[170:173]
	s_waitcnt lgkmcnt(0)
	v_mfma_f32_16x16x32_f16 v[22:25], v[30:33], v[234:237], v[22:25]
	v_mfma_f32_16x16x32_f16 v[30:33], v[14:17], v[198:201], v[38:41]
	v_mfma_f32_16x16x32_f16 v[38:41], v[14:17], v[210:213], v[174:177]
	v_mfma_f32_16x16x32_f16 v[174:177], v[14:17], v[214:217], v[178:181]
	v_mfma_f32_16x16x32_f16 v[178:181], v[14:17], v[218:221], v[182:185]
	v_mfma_f32_16x16x32_f16 v[182:185], v[14:17], v[222:225], v[186:189]
	v_mfma_f32_16x16x32_f16 v[186:189], v[14:17], v[226:229], v[190:193]
	v_mfma_f32_16x16x32_f16 v[190:193], v[14:17], v[230:233], v[194:197]
	v_mfma_f32_16x16x32_f16 v[4:7], v[14:17], v[234:237], v[6:9]
	v_mfma_f32_16x16x32_f16 v[14:17], v[18:21], v[198:201], v[26:29]
	v_mfma_f32_16x16x32_f16 v[26:29], v[18:21], v[210:213], v[62:65]
	v_mfma_f32_16x16x32_f16 v[62:65], v[18:21], v[214:217], v[78:81]
	v_mfma_f32_16x16x32_f16 v[78:81], v[18:21], v[218:221], v[86:89]
	v_mfma_f32_16x16x32_f16 v[86:89], v[18:21], v[222:225], v[94:97]
	v_mfma_f32_16x16x32_f16 v[94:97], v[18:21], v[226:229], v[102:105]
	v_mfma_f32_16x16x32_f16 v[102:105], v[18:21], v[230:233], v[106:109]
	v_mfma_f32_16x16x32_f16 v[0:3], v[18:21], v[234:237], v[0:3]
	global_load_dwordx4 v[18:21], v[118:119], off offset:1024
	s_nop 0
	global_load_dwordx4 v[106:109], v[118:119], off offset:2048
	global_load_dwordx4 v[194:197], v[118:119], off offset:3072
	ds_read_b128 v[198:201], v135
	ds_read_b128 v[210:213], v135 offset:8192
	ds_read_b128 v[214:217], v135 offset:16384
	ds_read_b128 v[218:221], v135 offset:24576
	ds_read_b128 v[222:225], v135 offset:32768
	ds_read_b128 v[226:229], v135 offset:40960
	ds_read_b128 v[230:233], v135 offset:49152
	ds_read_b128 v[234:237], v135 offset:57344
	s_waitcnt lgkmcnt(7)
	v_mfma_f32_16x16x32_f16 v[74:77], v[46:49], v[198:201], v[74:77]
	s_waitcnt lgkmcnt(6)
	v_mfma_f32_16x16x32_f16 v[150:153], v[46:49], v[210:213], v[150:153]
	s_waitcnt lgkmcnt(5)
	v_mfma_f32_16x16x32_f16 v[154:157], v[46:49], v[214:217], v[154:157]
	s_waitcnt lgkmcnt(4)
	v_mfma_f32_16x16x32_f16 v[158:161], v[46:49], v[218:221], v[158:161]
	s_waitcnt lgkmcnt(3)
	v_mfma_f32_16x16x32_f16 v[162:165], v[46:49], v[222:225], v[162:165]
	s_waitcnt lgkmcnt(2)
	v_mfma_f32_16x16x32_f16 v[166:169], v[46:49], v[226:229], v[166:169]
	s_waitcnt lgkmcnt(1)
	v_mfma_f32_16x16x32_f16 v[170:173], v[46:49], v[230:233], v[170:173]
	s_waitcnt lgkmcnt(0)
	v_mfma_f32_16x16x32_f16 v[22:25], v[46:49], v[234:237], v[22:25]
	v_mfma_f32_16x16x32_f16 v[30:33], v[42:45], v[198:201], v[30:33]
	v_mfma_f32_16x16x32_f16 v[38:41], v[42:45], v[210:213], v[38:41]
	v_mfma_f32_16x16x32_f16 v[46:49], v[42:45], v[214:217], v[174:177]
	v_mfma_f32_16x16x32_f16 v[174:177], v[42:45], v[218:221], v[178:181]
	v_mfma_f32_16x16x32_f16 v[178:181], v[42:45], v[222:225], v[182:185]
	v_mfma_f32_16x16x32_f16 v[182:185], v[42:45], v[226:229], v[186:189]
	v_mfma_f32_16x16x32_f16 v[186:189], v[42:45], v[230:233], v[190:193]
	v_mfma_f32_16x16x32_f16 v[4:7], v[42:45], v[234:237], v[4:7]
	v_mfma_f32_16x16x32_f16 v[14:17], v[34:37], v[198:201], v[14:17]
	v_mfma_f32_16x16x32_f16 v[26:29], v[34:37], v[210:213], v[26:29]
	v_mfma_f32_16x16x32_f16 v[42:45], v[34:37], v[214:217], v[62:65]
	v_mfma_f32_16x16x32_f16 v[62:65], v[34:37], v[218:221], v[78:81]
	v_mfma_f32_16x16x32_f16 v[78:81], v[34:37], v[222:225], v[86:89]
	v_mfma_f32_16x16x32_f16 v[86:89], v[34:37], v[226:229], v[94:97]
	v_mfma_f32_16x16x32_f16 v[94:97], v[34:37], v[230:233], v[102:105]
	v_mfma_f32_16x16x32_f16 v[0:3], v[34:37], v[234:237], v[0:3]
	ds_read_b128 v[34:37], v136
	s_nop 0
	ds_read_b128 v[102:105], v136 offset:8192
	ds_read_b128 v[190:193], v136 offset:16384
	ds_read_b128 v[198:201], v136 offset:24576
	ds_read_b128 v[210:213], v136 offset:32768
	ds_read_b128 v[214:217], v136 offset:40960
	ds_read_b128 v[218:221], v136 offset:49152
	ds_read_b128 v[222:225], v136 offset:57344
	s_waitcnt vmcnt(17) lgkmcnt(7)
	v_mfma_f32_16x16x32_f16 v[74:77], v[50:53], v[34:37], v[74:77]
	s_waitcnt lgkmcnt(6)
	v_mfma_f32_16x16x32_f16 v[150:153], v[50:53], v[102:105], v[150:153]
	s_waitcnt lgkmcnt(5)
	v_mfma_f32_16x16x32_f16 v[154:157], v[50:53], v[190:193], v[154:157]
	s_waitcnt lgkmcnt(4)
	v_mfma_f32_16x16x32_f16 v[158:161], v[50:53], v[198:201], v[158:161]
	s_waitcnt lgkmcnt(3)
	v_mfma_f32_16x16x32_f16 v[162:165], v[50:53], v[210:213], v[162:165]
	s_waitcnt lgkmcnt(2)
	v_mfma_f32_16x16x32_f16 v[166:169], v[50:53], v[214:217], v[166:169]
	s_waitcnt lgkmcnt(1)
	v_mfma_f32_16x16x32_f16 v[170:173], v[50:53], v[218:221], v[170:173]
	s_waitcnt lgkmcnt(0)
	v_mfma_f32_16x16x32_f16 v[22:25], v[50:53], v[222:225], v[22:25]
	s_waitcnt vmcnt(16)
	v_mfma_f32_16x16x32_f16 v[30:33], v[54:57], v[34:37], v[30:33]
	v_mfma_f32_16x16x32_f16 v[38:41], v[54:57], v[102:105], v[38:41]
	v_mfma_f32_16x16x32_f16 v[46:49], v[54:57], v[190:193], v[46:49]
	v_mfma_f32_16x16x32_f16 v[50:53], v[54:57], v[198:201], v[174:177]
	v_mfma_f32_16x16x32_f16 v[174:177], v[54:57], v[210:213], v[178:181]
	v_mfma_f32_16x16x32_f16 v[178:181], v[54:57], v[214:217], v[182:185]
	v_mfma_f32_16x16x32_f16 v[182:185], v[54:57], v[218:221], v[186:189]
	v_mfma_f32_16x16x32_f16 v[4:7], v[54:57], v[222:225], v[4:7]
	s_waitcnt vmcnt(15)
	v_mfma_f32_16x16x32_f16 v[14:17], v[58:61], v[34:37], v[14:17]
	v_mfma_f32_16x16x32_f16 v[26:29], v[58:61], v[102:105], v[26:29]
	v_mfma_f32_16x16x32_f16 v[34:37], v[58:61], v[190:193], v[42:45]
	v_mfma_f32_16x16x32_f16 v[42:45], v[58:61], v[198:201], v[62:65]
	v_mfma_f32_16x16x32_f16 v[54:57], v[58:61], v[210:213], v[78:81]
	v_mfma_f32_16x16x32_f16 v[62:65], v[58:61], v[214:217], v[86:89]
	v_mfma_f32_16x16x32_f16 v[78:81], v[58:61], v[218:221], v[94:97]
	v_mfma_f32_16x16x32_f16 v[0:3], v[58:61], v[222:225], v[0:3]
	ds_read_b128 v[58:61], v137
	ds_read_b128 v[86:89], v137 offset:8192
	ds_read_b128 v[94:97], v137 offset:16384
	ds_read_b128 v[102:105], v137 offset:24576
	ds_read_b128 v[186:189], v137 offset:32768
	ds_read_b128 v[190:193], v137 offset:40960
	ds_read_b128 v[198:201], v137 offset:49152
	ds_read_b128 v[134:137], v137 offset:57344
	s_waitcnt vmcnt(7) lgkmcnt(7)
	v_mfma_f32_16x16x32_f16 v[74:77], v[202:205], v[58:61], v[74:77]
	s_waitcnt lgkmcnt(6)
	v_mfma_f32_16x16x32_f16 v[150:153], v[202:205], v[86:89], v[150:153]
	s_waitcnt lgkmcnt(5)
	v_mfma_f32_16x16x32_f16 v[154:157], v[202:205], v[94:97], v[154:157]
	s_waitcnt lgkmcnt(4)
	v_mfma_f32_16x16x32_f16 v[158:161], v[202:205], v[102:105], v[158:161]
	s_waitcnt lgkmcnt(3)
	v_mfma_f32_16x16x32_f16 v[162:165], v[202:205], v[186:189], v[162:165]
	s_waitcnt lgkmcnt(2)
	v_mfma_f32_16x16x32_f16 v[166:169], v[202:205], v[190:193], v[166:169]
	s_waitcnt lgkmcnt(1)
	v_mfma_f32_16x16x32_f16 v[170:173], v[202:205], v[198:201], v[170:173]
	s_waitcnt lgkmcnt(0)
	v_mfma_f32_16x16x32_f16 v[22:25], v[202:205], v[134:137], v[22:25]
	v_mfma_f32_16x16x32_f16 v[30:33], v[146:149], v[58:61], v[30:33]
	v_mfma_f32_16x16x32_f16 v[38:41], v[146:149], v[86:89], v[38:41]
	v_mfma_f32_16x16x32_f16 v[46:49], v[146:149], v[94:97], v[46:49]
	v_mfma_f32_16x16x32_f16 v[50:53], v[146:149], v[102:105], v[50:53]
	v_mfma_f32_16x16x32_f16 v[174:177], v[146:149], v[186:189], v[174:177]
	v_mfma_f32_16x16x32_f16 v[178:181], v[146:149], v[190:193], v[178:181]
	v_mfma_f32_16x16x32_f16 v[182:185], v[146:149], v[198:201], v[182:185]
	v_mfma_f32_16x16x32_f16 v[4:7], v[146:149], v[134:137], v[4:7]
	s_waitcnt vmcnt(6)
	v_mfma_f32_16x16x32_f16 v[14:17], v[206:209], v[58:61], v[14:17]
	v_mfma_f32_16x16x32_f16 v[26:29], v[206:209], v[86:89], v[26:29]
	v_mfma_f32_16x16x32_f16 v[34:37], v[206:209], v[94:97], v[34:37]
	v_mfma_f32_16x16x32_f16 v[42:45], v[206:209], v[102:105], v[42:45]
	v_mfma_f32_16x16x32_f16 v[54:57], v[206:209], v[186:189], v[54:57]
	v_mfma_f32_16x16x32_f16 v[58:61], v[206:209], v[190:193], v[62:65]
	v_mfma_f32_16x16x32_f16 v[62:65], v[206:209], v[198:201], v[78:81]
	v_mfma_f32_16x16x32_f16 v[0:3], v[206:209], v[134:137], v[0:3]
	s_nop 1
	ds_read_b128 v[78:81], v138
	ds_read_b128 v[86:89], v138 offset:8192
	ds_read_b128 v[94:97], v138 offset:16384
	ds_read_b128 v[102:105], v138 offset:24576
	ds_read_b128 v[134:137], v138 offset:32768
	ds_read_b128 v[146:149], v138 offset:40960
	ds_read_b128 v[186:189], v138 offset:49152
	ds_read_b128 v[190:193], v138 offset:57344
	s_waitcnt vmcnt(5) lgkmcnt(7)
	v_mfma_f32_16x16x32_f16 v[74:77], v[10:13], v[78:81], v[74:77]
	s_waitcnt lgkmcnt(6)
	v_mfma_f32_16x16x32_f16 v[150:153], v[10:13], v[86:89], v[150:153]
	s_waitcnt lgkmcnt(5)
	v_mfma_f32_16x16x32_f16 v[154:157], v[10:13], v[94:97], v[154:157]
	s_waitcnt lgkmcnt(4)
	v_mfma_f32_16x16x32_f16 v[158:161], v[10:13], v[102:105], v[158:161]
	s_waitcnt lgkmcnt(3)
	v_mfma_f32_16x16x32_f16 v[162:165], v[10:13], v[134:137], v[162:165]
	s_waitcnt lgkmcnt(2)
	v_mfma_f32_16x16x32_f16 v[166:169], v[10:13], v[146:149], v[166:169]
	s_waitcnt lgkmcnt(1)
	v_mfma_f32_16x16x32_f16 v[170:173], v[10:13], v[186:189], v[170:173]
	s_waitcnt lgkmcnt(0)
	v_mfma_f32_16x16x32_f16 v[8:11], v[10:13], v[190:193], v[22:25]
	s_waitcnt vmcnt(4)
	v_mfma_f32_16x16x32_f16 v[22:25], v[122:125], v[78:81], v[30:33]
	v_mfma_f32_16x16x32_f16 v[30:33], v[122:125], v[86:89], v[38:41]
	v_mfma_f32_16x16x32_f16 v[198:201], v[122:125], v[94:97], v[46:49]
	v_mfma_f32_16x16x32_f16 v[48:51], v[122:125], v[102:105], v[50:53]
	v_mfma_f32_16x16x32_f16 v[174:177], v[122:125], v[134:137], v[174:177]
	v_mfma_f32_16x16x32_f16 v[178:181], v[122:125], v[146:149], v[178:181]
	v_mfma_f32_16x16x32_f16 v[182:185], v[122:125], v[186:189], v[182:185]
	v_mfma_f32_16x16x32_f16 v[4:7], v[122:125], v[190:193], v[4:7]
	s_waitcnt vmcnt(3)
	v_mfma_f32_16x16x32_f16 v[12:15], v[126:129], v[78:81], v[14:17]
	v_mfma_f32_16x16x32_f16 v[78:81], v[126:129], v[86:89], v[26:29]
	v_mfma_f32_16x16x32_f16 v[86:89], v[126:129], v[94:97], v[34:37]
	v_mfma_f32_16x16x32_f16 v[40:43], v[126:129], v[102:105], v[42:45]
	v_mfma_f32_16x16x32_f16 v[94:97], v[126:129], v[134:137], v[54:57]
	v_mfma_f32_16x16x32_f16 v[102:105], v[126:129], v[146:149], v[58:61]
	v_mfma_f32_16x16x32_f16 v[64:67], v[126:129], v[186:189], v[62:65]
	v_mfma_f32_16x16x32_f16 v[0:3], v[126:129], v[190:193], v[0:3]
	s_nop 1
	ds_read_b128 v[60:63], v140
	ds_read_b128 v[122:125], v140 offset:8192
	ds_read_b128 v[126:129], v140 offset:16384
	ds_read_b128 v[134:137], v140 offset:24576
	ds_read_b128 v[146:149], v140 offset:32768
	ds_read_b128 v[186:189], v140 offset:40960
	ds_read_b128 v[190:193], v140 offset:49152
	ds_read_b128 v[202:205], v140 offset:57344
	s_waitcnt vmcnt(2) lgkmcnt(7)
	v_mfma_f32_16x16x32_f16 v[74:77], v[18:21], v[60:63], v[74:77]
	s_waitcnt lgkmcnt(6)
	v_mfma_f32_16x16x32_f16 v[150:153], v[18:21], v[122:125], v[150:153]
	s_waitcnt lgkmcnt(5)
	v_mfma_f32_16x16x32_f16 v[154:157], v[18:21], v[126:129], v[154:157]
	s_waitcnt lgkmcnt(4)
	v_mfma_f32_16x16x32_f16 v[158:161], v[18:21], v[134:137], v[158:161]
	s_waitcnt lgkmcnt(3)
	v_mfma_f32_16x16x32_f16 v[56:59], v[18:21], v[146:149], v[162:165]
	s_waitcnt lgkmcnt(2)
	v_mfma_f32_16x16x32_f16 v[52:55], v[18:21], v[186:189], v[166:169]
	s_waitcnt lgkmcnt(1)
	v_mfma_f32_16x16x32_f16 v[44:47], v[18:21], v[190:193], v[170:173]
	s_waitcnt lgkmcnt(0)
	v_mfma_f32_16x16x32_f16 v[36:39], v[18:21], v[202:205], v[8:11]
	s_waitcnt vmcnt(1)
	v_mfma_f32_16x16x32_f16 v[162:165], v[106:109], v[60:63], v[22:25]
	v_mfma_f32_16x16x32_f16 v[166:169], v[106:109], v[122:125], v[30:33]
	v_mfma_f32_16x16x32_f16 v[170:173], v[106:109], v[126:129], v[198:201]
	v_mfma_f32_16x16x32_f16 v[198:201], v[106:109], v[134:137], v[48:51]
	v_mfma_f32_16x16x32_f16 v[32:35], v[106:109], v[146:149], v[174:177]
	v_mfma_f32_16x16x32_f16 v[24:27], v[106:109], v[186:189], v[178:181]
	v_mfma_f32_16x16x32_f16 v[20:23], v[106:109], v[190:193], v[182:185]
	v_mfma_f32_16x16x32_f16 v[16:19], v[106:109], v[202:205], v[4:7]
	s_waitcnt vmcnt(0)
	v_mfma_f32_16x16x32_f16 v[106:109], v[194:197], v[60:63], v[12:15]
	v_mfma_f32_16x16x32_f16 v[78:81], v[194:197], v[122:125], v[78:81]
	v_mfma_f32_16x16x32_f16 v[86:89], v[194:197], v[126:129], v[86:89]
	v_mfma_f32_16x16x32_f16 v[60:63], v[194:197], v[134:137], v[40:43]
	v_mfma_f32_16x16x32_f16 v[12:15], v[194:197], v[146:149], v[94:97]
	v_mfma_f32_16x16x32_f16 v[8:11], v[194:197], v[186:189], v[102:105]
	v_mfma_f32_16x16x32_f16 v[4:7], v[194:197], v[190:193], v[64:67]
	v_mfma_f32_16x16x32_f16 v[0:3], v[194:197], v[202:205], v[0:3]
	global_load_dwordx4 v[48:51], v[120:121], off offset:1536
	global_load_dwordx4 v[40:43], v[120:121], off offset:1600
	global_load_dwordx4 v[28:31], v[120:121], off offset:1664
	v_mov_b32_e32 v94, v155
	v_mov_b32_e32 v95, v156
	v_mov_b32_e32 v96, v159
	v_mov_b32_e32 v97, v160
	v_mov_b32_e32 v64, v151
	v_mov_b32_e32 v65, v152
	v_mov_b32_e32 v102, v167
	v_mov_b32_e32 v103, v168
	v_mov_b32_e32 v104, v171
	v_mov_b32_e32 v105, v172
	v_mov_b32_e32 v118, v199
	v_mov_b32_e32 v119, v200
	s_barrier
	s_waitcnt vmcnt(2)
	v_pk_add_f32 v[74:75], v[74:75], v[48:49]
	v_add_f32_e32 v82, v150, v48
	v_pk_mov_b32 v[120:121], v[48:49], v[50:51] op_sel:[1,0]
	v_add_f32_e32 v49, v153, v51
	s_waitcnt vmcnt(1)
	v_pk_add_f32 v[122:123], v[162:163], v[40:41]
	v_add_f32_e32 v98, v166, v40
	v_pk_mov_b32 v[66:67], v[40:41], v[42:43] op_sel:[1,0]
	v_add_f32_e32 v41, v169, v43
	v_pk_add_f32 v[76:77], v[76:77], v[50:51]
	v_add_f32_e32 v50, v154, v48
	v_add_f32_e32 v85, v157, v51
	v_add_f32_e32 v90, v158, v48
	v_add_f32_e32 v93, v161, v51
	v_pk_add_f32 v[124:125], v[164:165], v[42:43]
	v_add_f32_e32 v42, v170, v40
	v_add_f32_e32 v101, v173, v43
	v_add_f32_e32 v126, v198, v40
	v_add_f32_e32 v127, v201, v43
	v_cvt_f16_f32_e32 v82, v82
	v_cvt_f16_f32_e32 v49, v49
	v_cvt_f16_f32_e32 v98, v98
	v_cvt_f16_f32_e32 v41, v41
	v_cvt_pk_f16_f32 v74, v74, v75
	v_cvt_pk_f16_f32 v75, v76, v77
	v_cvt_f16_f32_e32 v50, v50
	v_pk_add_f32 v[76:77], v[94:95], v[120:121]
	v_cvt_f16_f32_e32 v85, v85
	v_cvt_f16_f32_e32 v90, v90
	v_pk_add_f32 v[94:95], v[96:97], v[120:121]
	v_cvt_f16_f32_e32 v93, v93
	v_cvt_pk_f16_f32 v96, v122, v123
	v_cvt_f16_f32_e32 v42, v42
	v_cvt_f16_f32_e32 v101, v101
	v_cvt_f16_f32_e32 v122, v126
	v_cvt_f16_f32_e32 v123, v127
	v_pk_add_f32 v[64:65], v[64:65], v[120:121]
	v_pk_add_f32 v[102:103], v[102:103], v[66:67]
	v_pk_add_f32 v[104:105], v[104:105], v[66:67]
	v_pk_add_f32 v[118:119], v[118:119], v[66:67]
	v_cvt_pk_f16_f32 v65, v64, v65
	v_cvt_pk_f16_f32 v76, v76, v77
	v_cvt_pk_f16_f32 v77, v94, v95
	v_cvt_pk_f16_f32 v95, v102, v103
	s_waitcnt vmcnt(0)
	v_pk_add_f32 v[106:107], v[106:107], v[28:29]
	v_pk_add_f32 v[108:109], v[108:109], v[30:31]
	v_cvt_pk_f16_f32 v97, v124, v125
	v_cvt_pk_f16_f32 v102, v104, v105
	v_cvt_pk_f16_f32 v103, v118, v119
	v_pack_b32_f16 v64, v82, v65
	v_alignbit_b32 v65, v49, v65, 16
	v_pack_b32_f16 v94, v98, v95
	v_alignbit_b32 v95, v41, v95, 16
	v_add_f32_e32 v78, v78, v28
	v_cvt_pk_f16_f32 v106, v106, v107
	v_cvt_pk_f16_f32 v107, v108, v109
	ds_write2_b64 v130, v[74:75], v[96:97] offset1:4
	ds_write_b64 v130, v[106:107] offset:64
	v_pack_b32_f16 v74, v50, v76
	v_alignbit_b32 v75, v85, v76, 16
	v_pack_b32_f16 v76, v90, v77
	v_alignbit_b32 v77, v93, v77, 16
	v_pack_b32_f16 v96, v42, v102
	v_alignbit_b32 v97, v101, v102, 16
	v_pack_b32_f16 v102, v122, v103
	v_alignbit_b32 v103, v123, v103, 16
	ds_write2_b64 v132, v[64:65], v[94:95] offset0:32 offset1:36
	ds_write2_b64 v131, v[74:75], v[96:97] offset0:64 offset1:68
	ds_write2_b64 v91, v[76:77], v[102:103] offset0:96 offset1:100
	v_pk_mov_b32 v[64:65], v[28:29], v[30:31] op_sel:[1,0]
	v_add_f32_e32 v29, v81, v31
	v_cvt_f16_f32_e32 v78, v78
	v_cvt_f16_f32_e32 v29, v29
	v_mov_b32_e32 v74, v79
	v_mov_b32_e32 v75, v80
	v_pk_add_f32 v[74:75], v[74:75], v[64:65]
	v_add_f32_e32 v56, v56, v48
	v_cvt_pk_f16_f32 v30, v74, v75
	v_pack_b32_f16 v74, v78, v30
	v_alignbit_b32 v75, v29, v30, 16
	v_add_f32_e32 v29, v86, v28
	v_add_f32_e32 v30, v89, v31
	v_cvt_f16_f32_e32 v29, v29
	v_cvt_f16_f32_e32 v30, v30
	ds_write_b64 v130, v[74:75] offset:12608
	v_mov_b32_e32 v74, v87
	v_mov_b32_e32 v75, v88
	v_pk_add_f32 v[74:75], v[74:75], v[64:65]
	v_add_f32_e32 v52, v52, v48
	v_cvt_pk_f16_f32 v41, v74, v75
	v_pack_b32_f16 v74, v29, v41
	v_alignbit_b32 v75, v30, v41, 16
	v_add_f32_e32 v29, v60, v28
	v_add_f32_e32 v30, v63, v31
	v_cvt_f16_f32_e32 v29, v29
	v_cvt_f16_f32_e32 v30, v30
	v_mov_b32_e32 v60, v61
	v_mov_b32_e32 v61, v62
	v_pk_add_f32 v[60:61], v[60:61], v[64:65]
	ds_write_b64 v130, v[74:75] offset:25152
	v_cvt_pk_f16_f32 v41, v60, v61
	v_pack_b32_f16 v60, v29, v41
	v_alignbit_b32 v61, v30, v41, 16
	ds_write_b64 v130, v[60:61] offset:37696
	s_waitcnt lgkmcnt(0)
	s_barrier
	ds_read_b128 v[60:63], v83
	ds_read_b128 v[74:77], v84
	v_add_u32_e32 v29, 0x300, v111
	v_add_u32_e32 v30, v29, v112
	v_add_f32_e32 v44, v44, v48
	s_waitcnt lgkmcnt(1)
	buffer_store_dwordx4 v[60:63], v30, s[0:3], 0 offen sc1
	v_add_u32_e32 v30, 0x300, v113
	ds_read_b128 v[60:63], v92
	v_add_u32_e32 v41, v30, v114
	s_waitcnt lgkmcnt(1)
	buffer_store_dwordx4 v[74:77], v41, s[0:3], 0 offen sc1
	ds_read_b128 v[74:77], v99
	v_add_u32_e32 v41, 0x300, v115
	v_add_u32_e32 v42, v41, v116
	s_waitcnt lgkmcnt(1)
	buffer_store_dwordx4 v[60:63], v42, s[0:3], 0 offen sc1
	v_add_u32_e32 v42, 0x300, v117
	ds_read_b128 v[60:63], v100
	v_add_u32_e32 v49, v42, v142
	s_waitcnt lgkmcnt(1)
	buffer_store_dwordx4 v[74:77], v49, s[0:3], 0 offen sc1
	ds_read_b128 v[74:77], v110
	v_add_u32_e32 v49, 0x300, v143
	v_add_u32_e32 v50, v49, v141
	s_waitcnt lgkmcnt(1)
	buffer_store_dwordx4 v[60:63], v50, s[0:3], 0 offen sc1
	v_add_u32_e32 v50, 0x300, v144
	v_add_f32_e32 v36, v36, v48
	v_add_u32_e32 v60, v50, v145
	s_waitcnt lgkmcnt(0)
	buffer_store_dwordx4 v[74:77], v60, s[0:3], 0 offen sc1
	v_cvt_f16_f32_e32 v60, v56
	v_mov_b32_e32 v56, v57
	v_mov_b32_e32 v57, v58
	v_add_f32_e32 v58, v59, v51
	v_cvt_f16_f32_e32 v58, v58
	v_pk_add_f32 v[56:57], v[56:57], v[120:121]
	v_add_f32_e32 v32, v32, v40
	v_cvt_pk_f16_f32 v57, v56, v57
	v_pack_b32_f16 v56, v60, v57
	v_alignbit_b32 v57, v58, v57, 16
	v_cvt_f16_f32_e32 v58, v52
	v_mov_b32_e32 v52, v53
	v_mov_b32_e32 v53, v54
	v_add_f32_e32 v54, v55, v51
	v_cvt_f16_f32_e32 v54, v54
	v_pk_add_f32 v[52:53], v[52:53], v[120:121]
	v_add_f32_e32 v24, v24, v40
	v_cvt_pk_f16_f32 v53, v52, v53
	v_pack_b32_f16 v52, v58, v53
	v_alignbit_b32 v53, v54, v53, 16
	v_cvt_f16_f32_e32 v54, v44
	v_mov_b32_e32 v44, v45
	v_mov_b32_e32 v45, v46
	v_add_f32_e32 v46, v47, v51
	v_cvt_f16_f32_e32 v46, v46
	v_pk_add_f32 v[44:45], v[44:45], v[120:121]
	s_nop 0
	v_cvt_pk_f16_f32 v45, v44, v45
	v_pack_b32_f16 v44, v54, v45
	v_alignbit_b32 v45, v46, v45, 16
	v_cvt_f16_f32_e32 v46, v36
	v_mov_b32_e32 v36, v37
	v_mov_b32_e32 v37, v38
	v_add_f32_e32 v38, v39, v51
	v_cvt_f16_f32_e32 v38, v38
	v_pk_add_f32 v[36:37], v[36:37], v[120:121]
	s_barrier
	v_cvt_pk_f16_f32 v37, v36, v37
	v_pack_b32_f16 v36, v46, v37
	v_alignbit_b32 v37, v38, v37, 16
	v_cvt_f16_f32_e32 v38, v32
	v_mov_b32_e32 v32, v33
	v_mov_b32_e32 v33, v34
	v_add_f32_e32 v34, v35, v43
	v_cvt_f16_f32_e32 v34, v34
	v_pk_add_f32 v[32:33], v[32:33], v[66:67]
	s_nop 0
	v_cvt_pk_f16_f32 v33, v32, v33
	v_pack_b32_f16 v32, v38, v33
	v_alignbit_b32 v33, v34, v33, 16
	ds_write2_b64 v130, v[56:57], v[32:33] offset1:4
	v_cvt_f16_f32_e32 v32, v24
	v_mov_b32_e32 v24, v25
	v_mov_b32_e32 v25, v26
	v_add_f32_e32 v26, v27, v43
	v_cvt_f16_f32_e32 v26, v26
	v_pk_add_f32 v[24:25], v[24:25], v[66:67]
	v_add_f32_e32 v20, v20, v40
	v_cvt_pk_f16_f32 v25, v24, v25
	v_pack_b32_f16 v24, v32, v25
	v_alignbit_b32 v25, v26, v25, 16
	ds_write2_b64 v132, v[52:53], v[24:25] offset0:32 offset1:36
	v_cvt_f16_f32_e32 v24, v20
	v_mov_b32_e32 v20, v21
	v_mov_b32_e32 v21, v22
	v_add_f32_e32 v22, v23, v43
	v_cvt_f16_f32_e32 v22, v22
	v_pk_add_f32 v[20:21], v[20:21], v[66:67]
	v_add_f32_e32 v16, v16, v40
	v_cvt_pk_f16_f32 v21, v20, v21
	v_pack_b32_f16 v20, v24, v21
	v_alignbit_b32 v21, v22, v21, 16
	ds_write2_b64 v131, v[44:45], v[20:21] offset0:64 offset1:68
	v_cvt_f16_f32_e32 v20, v16
	v_mov_b32_e32 v16, v17
	v_mov_b32_e32 v17, v18
	v_add_f32_e32 v18, v19, v43
	v_cvt_f16_f32_e32 v18, v18
	v_pk_add_f32 v[16:17], v[16:17], v[66:67]
	v_add_f32_e32 v12, v12, v28
	v_cvt_pk_f16_f32 v17, v16, v17
	v_pack_b32_f16 v16, v20, v17
	v_alignbit_b32 v17, v18, v17, 16
	ds_write2_b64 v91, v[36:37], v[16:17] offset0:96 offset1:100
	v_cvt_f16_f32_e32 v16, v12
	v_mov_b32_e32 v12, v13
	v_mov_b32_e32 v13, v14
	v_add_f32_e32 v14, v15, v31
	v_cvt_f16_f32_e32 v14, v14
	v_pk_add_f32 v[12:13], v[12:13], v[64:65]
	v_add_f32_e32 v8, v8, v28
	v_cvt_pk_f16_f32 v13, v12, v13
	v_pack_b32_f16 v12, v16, v13
	v_alignbit_b32 v13, v14, v13, 16
	ds_write_b64 v130, v[12:13] offset:64
	v_cvt_f16_f32_e32 v12, v8
	v_mov_b32_e32 v8, v9
	v_mov_b32_e32 v9, v10
	v_add_f32_e32 v10, v11, v31
	v_cvt_f16_f32_e32 v10, v10
	v_pk_add_f32 v[8:9], v[8:9], v[64:65]
	v_add_f32_e32 v4, v4, v28
	v_cvt_pk_f16_f32 v9, v8, v9
	v_pack_b32_f16 v8, v12, v9
	v_alignbit_b32 v9, v10, v9, 16
	ds_write_b64 v130, v[8:9] offset:12608
	v_cvt_f16_f32_e32 v8, v4
	v_mov_b32_e32 v4, v5
	v_mov_b32_e32 v5, v6
	v_add_f32_e32 v6, v7, v31
	v_cvt_f16_f32_e32 v6, v6
	v_pk_add_f32 v[4:5], v[4:5], v[64:65]
	v_add_f32_e32 v0, v0, v28
	v_cvt_pk_f16_f32 v5, v4, v5
	v_pack_b32_f16 v4, v8, v5
	v_alignbit_b32 v5, v6, v5, 16
	ds_write_b64 v130, v[4:5] offset:25152
	v_cvt_f16_f32_e32 v4, v0
	v_mov_b32_e32 v0, v1
	v_mov_b32_e32 v1, v2
	v_add_f32_e32 v2, v3, v31
	v_cvt_f16_f32_e32 v2, v2
	v_pk_add_f32 v[0:1], v[0:1], v[64:65]
	v_add_u32_e32 v8, v29, v68
	v_cvt_pk_f16_f32 v1, v0, v1
	v_pack_b32_f16 v0, v4, v1
	v_alignbit_b32 v1, v2, v1, 16
	ds_write_b64 v130, v[0:1] offset:37696
	s_waitcnt lgkmcnt(0)
	s_barrier
	ds_read_b128 v[0:3], v83
	ds_read_b128 v[4:7], v84
	v_add_u32_e32 v12, v42, v70
	s_waitcnt lgkmcnt(1)
	buffer_store_dwordx4 v[0:3], v8, s[0:3], 0 offen sc1
	ds_read_b128 v[0:3], v92
	v_add_u32_e32 v8, v30, v69
	s_waitcnt lgkmcnt(1)
	buffer_store_dwordx4 v[4:7], v8, s[0:3], 0 offen sc1
	v_add_u32_e32 v8, v41, v72
	ds_read_b128 v[4:7], v99
	s_waitcnt lgkmcnt(1)
	buffer_store_dwordx4 v[0:3], v8, s[0:3], 0 offen sc1
	ds_read_b128 v[0:3], v100
	ds_read_b128 v[8:11], v110
	s_waitcnt lgkmcnt(2)
	buffer_store_dwordx4 v[4:7], v12, s[0:3], 0 offen sc1
	s_nop 1
	v_add_u32_e32 v4, v49, v71
	s_waitcnt lgkmcnt(1)
	buffer_store_dwordx4 v[0:3], v4, s[0:3], 0 offen sc1
	s_nop 1
	v_add_u32_e32 v0, v50, v73
	s_waitcnt lgkmcnt(0)
	buffer_store_dwordx4 v[8:11], v0, s[0:3], 0 offen sc1
	s_endpgm

.LBB3_82:
	s_setprio 0
	s_mul_i32 s0, s9, s3
	s_lshl_b32 s1, s30, 6
	s_add_i32 s0, s0, s8
	s_or_b32 s1, s1, s31
	s_or_b32 s7, s1, s11
	s_mul_i32 s4, s0, 0x60000
	s_mul_hi_i32 s1, s0, 0x60000
	s_waitcnt lgkmcnt(0)
	s_add_u32 s6, s12, s4
	s_mulk_i32 s0, 0x300
	s_addc_u32 s8, s13, s1
	s_ashr_i32 s1, s0, 31
	s_lshl_b64 s[0:1], s[0:1], 2
	s_add_u32 s4, s14, s0
	s_addc_u32 s5, s15, s1
	s_mul_i32 s0, s2, 0x1800000
	s_mul_hi_u32 s1, s3, 0x1800000
	s_add_i32 s1, s1, s0
	s_mul_i32 s0, s3, 0x1800000
	s_add_u32 s0, s20, s0
	v_readfirstlane_b32 s2, v0
	s_addc_u32 s1, s21, s1
	s_lshr_b32 s9, s2, 6
	s_and_b32 s1, s1, 0xffff
	s_mul_i32 s2, s9, 0x6000
	v_and_b32_e32 v2, 63, v0
	s_mul_hi_u32 s3, s9, 0x6000
	s_add_u32 s2, s6, s2
	s_addc_u32 s3, s8, s3
	v_lshlrev_b32_e32 v82, 4, v2
	v_mov_b32_e32 v83, 0
	v_lshl_add_u64 v[118:119], s[2:3], 0, v[82:83]
	s_movk_i32 s6, 0x1000
	v_add_co_u32_e32 v50, vcc, s6, v118
	s_movk_i32 s6, 0x2000
	s_nop 0
	v_addc_co_u32_e32 v51, vcc, 0, v119, vcc
	v_add_co_u32_e32 v52, vcc, s6, v118
	global_load_dwordx4 v[2:5], v82, s[2:3] offset:1024
	global_load_dwordx4 v[6:9], v82, s[2:3] offset:2048
	v_addc_co_u32_e32 v53, vcc, 0, v119, vcc
	global_load_dwordx4 v[10:13], v82, s[2:3] offset:3072
	global_load_dwordx4 v[14:17], v[52:53], off offset:-4096
	global_load_dwordx4 v[18:21], v[50:51], off offset:1024
	global_load_dwordx4 v[22:25], v[50:51], off offset:2048
	global_load_dwordx4 v[26:29], v82, s[2:3]
	global_load_dwordx4 v[30:33], v[50:51], off offset:3072
	global_load_dwordx4 v[34:37], v[52:53], off
	global_load_dwordx4 v[38:41], v[52:53], off offset:1024
	global_load_dwordx4 v[42:45], v[52:53], off offset:2048
	global_load_dwordx4 v[46:49], v[52:53], off offset:3072
	s_movk_i32 s2, 0x3000
	v_add_co_u32_e32 v116, vcc, s2, v118
	s_movk_i32 s2, 0x4000
	s_nop 0
	v_addc_co_u32_e32 v117, vcc, 0, v119, vcc
	v_add_co_u32_e32 v156, vcc, s2, v118
	s_nop 1
	v_addc_co_u32_e32 v157, vcc, 0, v119, vcc
	s_barrier
	global_load_dwordx4 v[50:53], v[156:157], off offset:-4096
	global_load_dwordx4 v[54:57], v[116:117], off offset:1024
	global_load_dwordx4 v[58:61], v[116:117], off offset:2048
	v_mul_u32_u24_e32 v62, 0x556, v0
	v_lshlrev_b32_e32 v132, 9, v1
	v_lshrrev_b32_e32 v142, 16, v62
	v_xor_b32_e32 v62, v158, v1
	v_lshl_or_b32 v135, v62, 4, v132
	ds_read_b128 v[62:65], v135
	ds_read_b128 v[66:69], v135 offset:8192
	ds_read_b128 v[70:73], v135 offset:16384
	ds_read_b128 v[74:77], v135 offset:24576
	ds_read_b128 v[78:81], v135 offset:32768
	ds_read_b128 v[84:87], v135 offset:40960
	ds_read_b128 v[88:91], v135 offset:49152
	ds_read_b128 v[92:95], v135 offset:57344
	s_mul_i32 s6, s9, 48
	v_lshl_or_b32 v82, v158, 2, s6
	s_mul_i32 s6, s9, 0x60
	s_add_i32 s6, s6, 0x10000
	v_lshlrev_b32_e32 v96, 3, v142
	s_movk_i32 s9, 0x47
	v_lshl_or_b32 v248, v158, 3, s6
	s_or_b32 s6, s7, 8
	v_bitop3_b32 v143, v96, s9, v142 bitop3:0xc8
	s_mov_b32 s2, 0x1800000
	s_mov_b32 s3, 0x20000
	s_mov_b32 s8, 0x10000
	v_or_b32_e32 v140, s6, v143
	s_waitcnt vmcnt(8) lgkmcnt(7)
	v_mfma_f32_16x16x32_f16 v[96:99], v[26:29], v[62:65], 0
	s_waitcnt lgkmcnt(6)
	v_mfma_f32_16x16x32_f16 v[100:103], v[26:29], v[66:69], 0
	s_waitcnt lgkmcnt(5)
	v_mfma_f32_16x16x32_f16 v[104:107], v[26:29], v[70:73], 0
	s_waitcnt lgkmcnt(4)
	v_mfma_f32_16x16x32_f16 v[108:111], v[26:29], v[74:77], 0
	s_waitcnt lgkmcnt(3)
	v_mfma_f32_16x16x32_f16 v[112:115], v[26:29], v[78:81], 0
	s_waitcnt lgkmcnt(2)
	v_mfma_f32_16x16x32_f16 v[120:123], v[26:29], v[84:87], 0
	s_waitcnt lgkmcnt(1)
	v_mfma_f32_16x16x32_f16 v[124:127], v[26:29], v[88:91], 0
	s_waitcnt lgkmcnt(0)
	v_mfma_f32_16x16x32_f16 v[26:29], v[26:29], v[92:95], 0
	v_mfma_f32_16x16x32_f16 v[128:131], v[2:5], v[62:65], 0
	v_mfma_f32_16x16x32_f16 v[136:139], v[2:5], v[66:69], 0
	v_mfma_f32_16x16x32_f16 v[144:147], v[2:5], v[70:73], 0
	v_mfma_f32_16x16x32_f16 v[148:151], v[2:5], v[74:77], 0
	v_mfma_f32_16x16x32_f16 v[152:155], v[2:5], v[78:81], 0
	v_mfma_f32_16x16x32_f16 v[160:163], v[2:5], v[84:87], 0
	v_mfma_f32_16x16x32_f16 v[164:167], v[2:5], v[88:91], 0
	v_mfma_f32_16x16x32_f16 v[2:5], v[2:5], v[92:95], 0
	v_mfma_f32_16x16x32_f16 v[62:65], v[6:9], v[62:65], 0
	v_mfma_f32_16x16x32_f16 v[66:69], v[6:9], v[66:69], 0
	v_mfma_f32_16x16x32_f16 v[70:73], v[6:9], v[70:73], 0
	v_mfma_f32_16x16x32_f16 v[74:77], v[6:9], v[74:77], 0
	v_mfma_f32_16x16x32_f16 v[78:81], v[6:9], v[78:81], 0
	v_mfma_f32_16x16x32_f16 v[84:87], v[6:9], v[84:87], 0
	v_mfma_f32_16x16x32_f16 v[88:91], v[6:9], v[88:91], 0
	v_mfma_f32_16x16x32_f16 v[6:9], v[6:9], v[92:95], 0
	global_load_dwordx4 v[92:95], v[116:117], off offset:3072
	global_load_dwordx4 v[168:171], v[156:157], off
	global_load_dwordx4 v[172:175], v[156:157], off offset:1024
	v_bitop3_b32 v116, v158, v1, 4 bitop3:0x36
	v_lshl_or_b32 v133, v116, 4, v132
	ds_read_b128 v[176:179], v133
	ds_read_b128 v[180:183], v133 offset:8192
	ds_read_b128 v[184:187], v133 offset:16384
	ds_read_b128 v[188:191], v133 offset:24576
	ds_read_b128 v[192:195], v133 offset:32768
	ds_read_b128 v[196:199], v133 offset:40960
	ds_read_b128 v[200:203], v133 offset:49152
	ds_read_b128 v[204:207], v133 offset:57344
	s_waitcnt lgkmcnt(7)
	v_mfma_f32_16x16x32_f16 v[96:99], v[10:13], v[176:179], v[96:99]
	s_waitcnt lgkmcnt(6)
	v_mfma_f32_16x16x32_f16 v[100:103], v[10:13], v[180:183], v[100:103]
	s_waitcnt lgkmcnt(5)
	v_mfma_f32_16x16x32_f16 v[104:107], v[10:13], v[184:187], v[104:107]
	s_waitcnt lgkmcnt(4)
	v_mfma_f32_16x16x32_f16 v[108:111], v[10:13], v[188:191], v[108:111]
	s_waitcnt lgkmcnt(3)
	v_mfma_f32_16x16x32_f16 v[112:115], v[10:13], v[192:195], v[112:115]
	s_waitcnt lgkmcnt(2)
	v_mfma_f32_16x16x32_f16 v[120:123], v[10:13], v[196:199], v[120:123]
	s_waitcnt lgkmcnt(1)
	v_mfma_f32_16x16x32_f16 v[124:127], v[10:13], v[200:203], v[124:127]
	s_waitcnt lgkmcnt(0)
	v_mfma_f32_16x16x32_f16 v[10:13], v[10:13], v[204:207], v[26:29]
	v_mfma_f32_16x16x32_f16 v[26:29], v[14:17], v[176:179], v[128:131]
	v_mfma_f32_16x16x32_f16 v[128:131], v[14:17], v[180:183], v[136:139]
	v_mfma_f32_16x16x32_f16 v[136:139], v[14:17], v[184:187], v[144:147]
	v_mfma_f32_16x16x32_f16 v[144:147], v[14:17], v[188:191], v[148:151]
	v_mfma_f32_16x16x32_f16 v[148:151], v[14:17], v[192:195], v[152:155]
	v_mfma_f32_16x16x32_f16 v[152:155], v[14:17], v[196:199], v[160:163]
	v_mfma_f32_16x16x32_f16 v[160:163], v[14:17], v[200:203], v[164:167]
	v_mfma_f32_16x16x32_f16 v[2:5], v[14:17], v[204:207], v[2:5]
	v_mfma_f32_16x16x32_f16 v[14:17], v[18:21], v[176:179], v[62:65]
	v_mfma_f32_16x16x32_f16 v[62:65], v[18:21], v[180:183], v[66:69]
	v_mfma_f32_16x16x32_f16 v[66:69], v[18:21], v[184:187], v[70:73]
	v_mfma_f32_16x16x32_f16 v[70:73], v[18:21], v[188:191], v[74:77]
	v_mfma_f32_16x16x32_f16 v[74:77], v[18:21], v[192:195], v[78:81]
	v_mfma_f32_16x16x32_f16 v[78:81], v[18:21], v[196:199], v[84:87]
	v_mfma_f32_16x16x32_f16 v[84:87], v[18:21], v[200:203], v[88:91]
	v_mfma_f32_16x16x32_f16 v[6:9], v[18:21], v[204:207], v[6:9]
	s_movk_i32 s9, 0x5000
	v_add_co_u32_e32 v116, vcc, s9, v118
	global_load_dwordx4 v[88:91], v[156:157], off offset:2048
	global_load_dwordx4 v[164:167], v[156:157], off offset:3072
	v_addc_co_u32_e32 v117, vcc, 0, v119, vcc
	global_load_dwordx4 v[176:179], v[116:117], off
	v_bitop3_b32 v18, v158, v1, 8 bitop3:0x36
	v_lshl_or_b32 v134, v18, 4, v132
	ds_read_b128 v[18:21], v134
	ds_read_b128 v[180:183], v134 offset:8192
	ds_read_b128 v[184:187], v134 offset:16384
	ds_read_b128 v[188:191], v134 offset:24576
	ds_read_b128 v[192:195], v134 offset:32768
	ds_read_b128 v[196:199], v134 offset:40960
	ds_read_b128 v[200:203], v134 offset:49152
	ds_read_b128 v[204:207], v134 offset:57344
	s_waitcnt lgkmcnt(7)
	v_mfma_f32_16x16x32_f16 v[96:99], v[22:25], v[18:21], v[96:99]
	s_waitcnt lgkmcnt(6)
	v_mfma_f32_16x16x32_f16 v[100:103], v[22:25], v[180:183], v[100:103]
	s_waitcnt lgkmcnt(5)
	v_mfma_f32_16x16x32_f16 v[104:107], v[22:25], v[184:187], v[104:107]
	s_waitcnt lgkmcnt(4)
	v_mfma_f32_16x16x32_f16 v[108:111], v[22:25], v[188:191], v[108:111]
	s_waitcnt lgkmcnt(3)
	v_mfma_f32_16x16x32_f16 v[112:115], v[22:25], v[192:195], v[112:115]
	s_waitcnt lgkmcnt(2)
	v_mfma_f32_16x16x32_f16 v[120:123], v[22:25], v[196:199], v[120:123]
	s_waitcnt lgkmcnt(1)
	v_mfma_f32_16x16x32_f16 v[124:127], v[22:25], v[200:203], v[124:127]
	s_waitcnt lgkmcnt(0)
	v_mfma_f32_16x16x32_f16 v[10:13], v[22:25], v[204:207], v[10:13]
	s_waitcnt vmcnt(13)
	v_mfma_f32_16x16x32_f16 v[22:25], v[30:33], v[18:21], v[26:29]
	v_mfma_f32_16x16x32_f16 v[26:29], v[30:33], v[180:183], v[128:131]
	v_mfma_f32_16x16x32_f16 v[128:131], v[30:33], v[184:187], v[136:139]
	v_mfma_f32_16x16x32_f16 v[144:147], v[30:33], v[188:191], v[144:147]
	v_mfma_f32_16x16x32_f16 v[148:151], v[30:33], v[192:195], v[148:151]
	v_mfma_f32_16x16x32_f16 v[152:155], v[30:33], v[196:199], v[152:155]
	v_mfma_f32_16x16x32_f16 v[160:163], v[30:33], v[200:203], v[160:163]
	v_mfma_f32_16x16x32_f16 v[2:5], v[30:33], v[204:207], v[2:5]
	s_waitcnt vmcnt(12)
	v_mfma_f32_16x16x32_f16 v[14:17], v[34:37], v[18:21], v[14:17]
	v_mfma_f32_16x16x32_f16 v[18:21], v[34:37], v[180:183], v[62:65]
	v_mfma_f32_16x16x32_f16 v[30:33], v[34:37], v[184:187], v[66:69]
	v_mfma_f32_16x16x32_f16 v[62:65], v[34:37], v[188:191], v[70:73]
	v_mfma_f32_16x16x32_f16 v[66:69], v[34:37], v[192:195], v[74:77]
	v_mfma_f32_16x16x32_f16 v[70:73], v[34:37], v[196:199], v[78:81]
	v_mfma_f32_16x16x32_f16 v[74:77], v[34:37], v[200:203], v[84:87]
	v_mfma_f32_16x16x32_f16 v[6:9], v[34:37], v[204:207], v[6:9]
	s_nop 0
	global_load_dwordx4 v[78:81], v[116:117], off offset:1024
	global_load_dwordx4 v[180:183], v[116:117], off offset:2048
	global_load_dwordx4 v[184:187], v[116:117], off offset:3072
	v_bitop3_b32 v34, v158, v1, 12 bitop3:0x36
	v_lshl_or_b32 v136, v34, 4, v132
	ds_read_b128 v[34:37], v136
	ds_read_b128 v[84:87], v136 offset:8192
	ds_read_b128 v[188:191], v136 offset:16384
	ds_read_b128 v[192:195], v136 offset:24576
	ds_read_b128 v[196:199], v136 offset:32768
	ds_read_b128 v[200:203], v136 offset:40960
	ds_read_b128 v[204:207], v136 offset:49152
	ds_read_b128 v[208:211], v136 offset:57344
	s_waitcnt vmcnt(14) lgkmcnt(7)
	v_mfma_f32_16x16x32_f16 v[96:99], v[38:41], v[34:37], v[96:99]
	s_waitcnt lgkmcnt(6)
	v_mfma_f32_16x16x32_f16 v[100:103], v[38:41], v[84:87], v[100:103]
	s_waitcnt lgkmcnt(5)
	v_mfma_f32_16x16x32_f16 v[104:107], v[38:41], v[188:191], v[104:107]
	s_waitcnt lgkmcnt(4)
	v_mfma_f32_16x16x32_f16 v[108:111], v[38:41], v[192:195], v[108:111]
	s_waitcnt lgkmcnt(3)
	v_mfma_f32_16x16x32_f16 v[112:115], v[38:41], v[196:199], v[112:115]
	s_waitcnt lgkmcnt(2)
	v_mfma_f32_16x16x32_f16 v[120:123], v[38:41], v[200:203], v[120:123]
	s_waitcnt lgkmcnt(1)
	v_mfma_f32_16x16x32_f16 v[124:127], v[38:41], v[204:207], v[124:127]
	s_waitcnt lgkmcnt(0)
	v_mfma_f32_16x16x32_f16 v[212:215], v[38:41], v[208:211], v[10:13]
	s_waitcnt vmcnt(13)
	v_mfma_f32_16x16x32_f16 v[22:25], v[42:45], v[34:37], v[22:25]
	v_mfma_f32_16x16x32_f16 v[216:219], v[42:45], v[84:87], v[26:29]
	v_mfma_f32_16x16x32_f16 v[128:131], v[42:45], v[188:191], v[128:131]
	v_mfma_f32_16x16x32_f16 v[144:147], v[42:45], v[192:195], v[144:147]
	v_mfma_f32_16x16x32_f16 v[148:151], v[42:45], v[196:199], v[148:151]
	v_mfma_f32_16x16x32_f16 v[152:155], v[42:45], v[200:203], v[152:155]
	v_mfma_f32_16x16x32_f16 v[160:163], v[42:45], v[204:207], v[160:163]
	v_mfma_f32_16x16x32_f16 v[2:5], v[42:45], v[208:211], v[2:5]
	s_waitcnt vmcnt(12)
	v_mfma_f32_16x16x32_f16 v[14:17], v[46:49], v[34:37], v[14:17]
	v_mfma_f32_16x16x32_f16 v[18:21], v[46:49], v[84:87], v[18:21]
	v_mfma_f32_16x16x32_f16 v[30:33], v[46:49], v[188:191], v[30:33]
	v_mfma_f32_16x16x32_f16 v[34:37], v[46:49], v[192:195], v[62:65]
	v_mfma_f32_16x16x32_f16 v[42:45], v[46:49], v[196:199], v[66:69]
	v_mfma_f32_16x16x32_f16 v[62:65], v[46:49], v[200:203], v[70:73]
	v_mfma_f32_16x16x32_f16 v[66:69], v[46:49], v[204:207], v[74:77]
	v_mfma_f32_16x16x32_f16 v[6:9], v[46:49], v[208:211], v[6:9]
	s_mov_b32 s9, 0x30000
	v_add_co_u32_e32 v116, vcc, s9, v118
	s_mov_b32 s9, 0x31000
	s_nop 0
	v_addc_co_u32_e32 v117, vcc, 0, v119, vcc
	v_add_co_u32_e32 v156, vcc, s9, v118
	v_bitop3_b32 v46, v158, v1, 16 bitop3:0x36
	s_nop 0
	v_addc_co_u32_e32 v157, vcc, 0, v119, vcc
	global_load_dwordx4 v[38:41], v[156:157], off offset:-4096
	global_load_dwordx4 v[26:29], v[116:117], off offset:1024
	global_load_dwordx4 v[10:13], v[116:117], off offset:2048
	v_lshl_or_b32 v137, v46, 4, v132
	ds_read_b128 v[46:49], v137
	ds_read_b128 v[70:73], v137 offset:8192
	ds_read_b128 v[74:77], v137 offset:16384
	ds_read_b128 v[84:87], v137 offset:24576
	ds_read_b128 v[188:191], v137 offset:32768
	ds_read_b128 v[192:195], v137 offset:40960
	ds_read_b128 v[196:199], v137 offset:49152
	ds_read_b128 v[200:203], v137 offset:57344
	s_waitcnt vmcnt(14) lgkmcnt(7)
	v_mfma_f32_16x16x32_f16 v[96:99], v[50:53], v[46:49], v[96:99]
	s_waitcnt lgkmcnt(6)
	v_mfma_f32_16x16x32_f16 v[100:103], v[50:53], v[70:73], v[100:103]
	s_waitcnt lgkmcnt(5)
	v_mfma_f32_16x16x32_f16 v[104:107], v[50:53], v[74:77], v[104:107]
	s_waitcnt lgkmcnt(4)
	v_mfma_f32_16x16x32_f16 v[108:111], v[50:53], v[84:87], v[108:111]
	s_waitcnt lgkmcnt(3)
	v_mfma_f32_16x16x32_f16 v[112:115], v[50:53], v[188:191], v[112:115]
	s_waitcnt lgkmcnt(2)
	v_mfma_f32_16x16x32_f16 v[120:123], v[50:53], v[192:195], v[120:123]
	s_waitcnt lgkmcnt(1)
	v_mfma_f32_16x16x32_f16 v[124:127], v[50:53], v[196:199], v[124:127]
	s_waitcnt lgkmcnt(0)
	v_mfma_f32_16x16x32_f16 v[50:53], v[50:53], v[200:203], v[212:215]
	s_waitcnt vmcnt(13)
	v_mfma_f32_16x16x32_f16 v[204:207], v[54:57], v[46:49], v[22:25]
	v_mfma_f32_16x16x32_f16 v[208:211], v[54:57], v[70:73], v[216:219]
	v_mfma_f32_16x16x32_f16 v[128:131], v[54:57], v[74:77], v[128:131]
	v_mfma_f32_16x16x32_f16 v[144:147], v[54:57], v[84:87], v[144:147]
	v_mfma_f32_16x16x32_f16 v[148:151], v[54:57], v[188:191], v[148:151]
	v_mfma_f32_16x16x32_f16 v[152:155], v[54:57], v[192:195], v[152:155]
	v_mfma_f32_16x16x32_f16 v[160:163], v[54:57], v[196:199], v[160:163]
	v_mfma_f32_16x16x32_f16 v[54:57], v[54:57], v[200:203], v[2:5]
	s_waitcnt vmcnt(12)
	v_mfma_f32_16x16x32_f16 v[14:17], v[58:61], v[46:49], v[14:17]
	v_mfma_f32_16x16x32_f16 v[18:21], v[58:61], v[70:73], v[18:21]
	v_mfma_f32_16x16x32_f16 v[30:33], v[58:61], v[74:77], v[30:33]
	v_mfma_f32_16x16x32_f16 v[34:37], v[58:61], v[84:87], v[34:37]
	v_mfma_f32_16x16x32_f16 v[42:45], v[58:61], v[188:191], v[42:45]
	v_mfma_f32_16x16x32_f16 v[46:49], v[58:61], v[192:195], v[62:65]
	v_mfma_f32_16x16x32_f16 v[62:65], v[58:61], v[196:199], v[66:69]
	v_mfma_f32_16x16x32_f16 v[58:61], v[58:61], v[200:203], v[6:9]
	global_load_dwordx4 v[22:25], v[116:117], off offset:3072
	s_nop 1
	global_load_dwordx4 v[6:9], v[156:157], off
	global_load_dwordx4 v[2:5], v[156:157], off offset:1024
	v_bitop3_b32 v66, v158, v1, 20 bitop3:0x36
	v_lshl_or_b32 v138, v66, 4, v132
	ds_read_b128 v[66:69], v138
	ds_read_b128 v[70:73], v138 offset:8192
	ds_read_b128 v[74:77], v138 offset:16384
	ds_read_b128 v[84:87], v138 offset:24576
	ds_read_b128 v[188:191], v138 offset:32768
	ds_read_b128 v[192:195], v138 offset:40960
	ds_read_b128 v[196:199], v138 offset:49152
	ds_read_b128 v[200:203], v138 offset:57344
	s_waitcnt vmcnt(14) lgkmcnt(7)
	v_mfma_f32_16x16x32_f16 v[96:99], v[92:95], v[66:69], v[96:99]
	s_waitcnt lgkmcnt(6)
	v_mfma_f32_16x16x32_f16 v[100:103], v[92:95], v[70:73], v[100:103]
	s_waitcnt lgkmcnt(5)
	v_mfma_f32_16x16x32_f16 v[104:107], v[92:95], v[74:77], v[104:107]
	s_waitcnt lgkmcnt(4)
	v_mfma_f32_16x16x32_f16 v[108:111], v[92:95], v[84:87], v[108:111]
	s_waitcnt lgkmcnt(3)
	v_mfma_f32_16x16x32_f16 v[112:115], v[92:95], v[188:191], v[112:115]
	s_waitcnt lgkmcnt(2)
	v_mfma_f32_16x16x32_f16 v[212:215], v[92:95], v[192:195], v[120:123]
	s_waitcnt lgkmcnt(1)
	v_mfma_f32_16x16x32_f16 v[124:127], v[92:95], v[196:199], v[124:127]
	s_waitcnt lgkmcnt(0)
	v_mfma_f32_16x16x32_f16 v[50:53], v[92:95], v[200:203], v[50:53]
	s_waitcnt vmcnt(13)
	v_mfma_f32_16x16x32_f16 v[92:95], v[168:171], v[66:69], v[204:207]
	v_mfma_f32_16x16x32_f16 v[204:207], v[168:171], v[70:73], v[208:211]
	v_mfma_f32_16x16x32_f16 v[128:131], v[168:171], v[74:77], v[128:131]
	v_mfma_f32_16x16x32_f16 v[144:147], v[168:171], v[84:87], v[144:147]
	v_mfma_f32_16x16x32_f16 v[148:151], v[168:171], v[188:191], v[148:151]
	v_mfma_f32_16x16x32_f16 v[152:155], v[168:171], v[192:195], v[152:155]
	v_mfma_f32_16x16x32_f16 v[160:163], v[168:171], v[196:199], v[160:163]
	v_mfma_f32_16x16x32_f16 v[54:57], v[168:171], v[200:203], v[54:57]
	s_waitcnt vmcnt(12)
	v_mfma_f32_16x16x32_f16 v[66:69], v[172:175], v[66:69], v[14:17]
	v_mfma_f32_16x16x32_f16 v[70:73], v[172:175], v[70:73], v[18:21]
	v_mfma_f32_16x16x32_f16 v[74:77], v[172:175], v[74:77], v[30:33]
	v_mfma_f32_16x16x32_f16 v[34:37], v[172:175], v[84:87], v[34:37]
	v_mfma_f32_16x16x32_f16 v[42:45], v[172:175], v[188:191], v[42:45]
	v_mfma_f32_16x16x32_f16 v[46:49], v[172:175], v[192:195], v[46:49]
	v_mfma_f32_16x16x32_f16 v[62:65], v[172:175], v[196:199], v[62:65]
	v_mfma_f32_16x16x32_f16 v[58:61], v[172:175], v[200:203], v[58:61]
	s_mov_b32 s9, 0x33000
	v_add_co_u32_e32 v122, vcc, s9, v118
	global_load_dwordx4 v[30:33], v[156:157], off offset:2048
	global_load_dwordx4 v[14:17], v[156:157], off offset:3072
	v_addc_co_u32_e32 v123, vcc, 0, v119, vcc
	global_load_dwordx4 v[18:21], v[122:123], off offset:-4096
	v_bitop3_b32 v84, v158, v1, 24 bitop3:0x36
	v_lshl_or_b32 v139, v84, 4, v132
	ds_read_b128 v[84:87], v139
	ds_read_b128 v[168:171], v139 offset:8192
	ds_read_b128 v[172:175], v139 offset:16384
	ds_read_b128 v[188:191], v139 offset:24576
	ds_read_b128 v[192:195], v139 offset:32768
	ds_read_b128 v[196:199], v139 offset:40960
	ds_read_b128 v[200:203], v139 offset:49152
	ds_read_b128 v[208:211], v139 offset:57344
	s_mov_b32 s9, 0x32000
	v_add_co_u32_e32 v116, vcc, s9, v118
	s_nop 1
	v_addc_co_u32_e32 v117, vcc, 0, v119, vcc
	s_waitcnt vmcnt(14) lgkmcnt(7)
	v_mfma_f32_16x16x32_f16 v[96:99], v[88:91], v[84:87], v[96:99]
	s_waitcnt lgkmcnt(6)
	v_mfma_f32_16x16x32_f16 v[100:103], v[88:91], v[168:171], v[100:103]
	s_waitcnt lgkmcnt(5)
	v_mfma_f32_16x16x32_f16 v[104:107], v[88:91], v[172:175], v[104:107]
	s_waitcnt lgkmcnt(4)
	v_mfma_f32_16x16x32_f16 v[108:111], v[88:91], v[188:191], v[108:111]
	s_waitcnt lgkmcnt(3)
	v_mfma_f32_16x16x32_f16 v[112:115], v[88:91], v[192:195], v[112:115]
	s_waitcnt lgkmcnt(2)
	v_mfma_f32_16x16x32_f16 v[212:215], v[88:91], v[196:199], v[212:215]
	s_waitcnt lgkmcnt(1)
	v_mfma_f32_16x16x32_f16 v[124:127], v[88:91], v[200:203], v[124:127]
	s_waitcnt lgkmcnt(0)
	v_mfma_f32_16x16x32_f16 v[50:53], v[88:91], v[208:211], v[50:53]
	s_waitcnt vmcnt(13)
	v_mfma_f32_16x16x32_f16 v[90:93], v[164:167], v[84:87], v[92:95]
	v_mfma_f32_16x16x32_f16 v[204:207], v[164:167], v[168:171], v[204:207]
	v_mfma_f32_16x16x32_f16 v[128:131], v[164:167], v[172:175], v[128:131]
	v_mfma_f32_16x16x32_f16 v[144:147], v[164:167], v[188:191], v[144:147]
	v_mfma_f32_16x16x32_f16 v[148:151], v[164:167], v[192:195], v[148:151]
	v_mfma_f32_16x16x32_f16 v[152:155], v[164:167], v[196:199], v[152:155]
	v_mfma_f32_16x16x32_f16 v[160:163], v[164:167], v[200:203], v[160:163]
	v_mfma_f32_16x16x32_f16 v[54:57], v[164:167], v[208:211], v[54:57]
	s_waitcnt vmcnt(12)
	v_mfma_f32_16x16x32_f16 v[164:167], v[176:179], v[84:87], v[66:69]
	v_mfma_f32_16x16x32_f16 v[168:171], v[176:179], v[168:171], v[70:73]
	v_mfma_f32_16x16x32_f16 v[172:175], v[176:179], v[172:175], v[74:77]
	v_mfma_f32_16x16x32_f16 v[188:191], v[176:179], v[188:191], v[34:37]
	v_mfma_f32_16x16x32_f16 v[192:195], v[176:179], v[192:195], v[42:45]
	v_mfma_f32_16x16x32_f16 v[196:199], v[176:179], v[196:199], v[46:49]
	v_mfma_f32_16x16x32_f16 v[200:203], v[176:179], v[200:203], v[62:65]
	v_mfma_f32_16x16x32_f16 v[176:179], v[176:179], v[208:211], v[58:61]
	s_nop 0
	global_load_dwordx4 v[46:49], v[116:117], off offset:1024
	global_load_dwordx4 v[42:45], v[116:117], off offset:2048
	global_load_dwordx4 v[34:37], v[116:117], off offset:3072
	v_bitop3_b32 v58, v158, v1, 28 bitop3:0x36
	v_lshl_or_b32 v141, v58, 4, v132
	ds_read_b128 v[58:61], v141
	ds_read_b128 v[62:65], v141 offset:8192
	ds_read_b128 v[156:159], v141 offset:16384
	ds_read_b128 v[208:211], v141 offset:24576
	ds_read_b128 v[216:219], v141 offset:32768
	ds_read_b128 v[220:223], v141 offset:40960
	ds_read_b128 v[224:227], v141 offset:49152
	ds_read_b128 v[228:231], v141 offset:57344
	s_waitcnt vmcnt(14) lgkmcnt(7)
	v_mfma_f32_16x16x32_f16 v[232:235], v[78:81], v[58:61], v[96:99]
	s_waitcnt lgkmcnt(6)
	v_mfma_f32_16x16x32_f16 v[236:239], v[78:81], v[62:65], v[100:103]
	s_waitcnt lgkmcnt(5)
	v_mfma_f32_16x16x32_f16 v[240:243], v[78:81], v[156:159], v[104:107]
	s_waitcnt lgkmcnt(4)
	v_mfma_f32_16x16x32_f16 v[244:247], v[78:81], v[208:211], v[108:111]
	s_waitcnt lgkmcnt(3)
	v_mfma_f32_16x16x32_f16 v[106:109], v[78:81], v[216:219], v[112:115]
	s_waitcnt lgkmcnt(2)
	v_mfma_f32_16x16x32_f16 v[102:105], v[78:81], v[220:223], v[212:215]
	s_waitcnt lgkmcnt(1)
	v_mfma_f32_16x16x32_f16 v[94:97], v[78:81], v[224:227], v[124:127]
	s_waitcnt lgkmcnt(0)
	v_mfma_f32_16x16x32_f16 v[86:89], v[78:81], v[228:231], v[50:53]
	s_waitcnt vmcnt(13)
	v_mfma_f32_16x16x32_f16 v[124:127], v[180:183], v[58:61], v[90:93]
	v_mfma_f32_16x16x32_f16 v[204:207], v[180:183], v[62:65], v[204:207]
	v_mfma_f32_16x16x32_f16 v[212:215], v[180:183], v[156:159], v[128:131]
	v_mfma_f32_16x16x32_f16 v[144:147], v[180:183], v[208:211], v[144:147]
	v_mfma_f32_16x16x32_f16 v[78:81], v[180:183], v[216:219], v[148:151]
	v_mfma_f32_16x16x32_f16 v[74:77], v[180:183], v[220:223], v[152:155]
	v_mfma_f32_16x16x32_f16 v[70:73], v[180:183], v[224:227], v[160:163]
	v_mfma_f32_16x16x32_f16 v[66:69], v[180:183], v[228:231], v[54:57]
	s_waitcnt vmcnt(12)
	v_mfma_f32_16x16x32_f16 v[148:151], v[184:187], v[58:61], v[164:167]
	v_mfma_f32_16x16x32_f16 v[152:155], v[184:187], v[62:65], v[168:171]
	v_mfma_f32_16x16x32_f16 v[114:117], v[184:187], v[156:159], v[172:175]
	v_mfma_f32_16x16x32_f16 v[110:113], v[184:187], v[208:211], v[188:191]
	v_mfma_f32_16x16x32_f16 v[62:65], v[184:187], v[216:219], v[192:195]
	v_mfma_f32_16x16x32_f16 v[58:61], v[184:187], v[220:223], v[196:199]
	v_mfma_f32_16x16x32_f16 v[54:57], v[184:187], v[224:227], v[200:203]
	v_mfma_f32_16x16x32_f16 v[50:53], v[184:187], v[228:231], v[176:179]
	v_lshl_add_u64 v[120:121], v[82:83], 2, s[4:5]
	global_load_dwordx4 v[98:101], v[120:121], off
	global_load_dwordx4 v[90:93], v[120:121], off offset:64
	global_load_dwordx4 v[82:85], v[120:121], off offset:128
	s_movk_i32 s4, 0x310
	v_mad_u32_u24 v130, v1, s4, v248
	v_mov_b32_e32 v156, v237
	v_mov_b32_e32 v157, v238
	v_mov_b32_e32 v158, v241
	v_mov_b32_e32 v159, v242
	v_mov_b32_e32 v160, v245
	v_mov_b32_e32 v161, v246
	v_mov_b32_e32 v162, v205
	v_mov_b32_e32 v163, v206
	v_mov_b32_e32 v167, v146
	v_mov_b32_e32 v164, v213
	v_mov_b32_e32 v165, v214
	v_mov_b32_e32 v166, v145
	s_barrier
	v_add_u32_e32 v132, 0x3000, v130
	v_add_u32_e32 v131, 0x6000, v130
	s_mov_b32 s5, 0xfffffd0
	v_mul_lo_u32 v174, v142, s5
	s_movk_i32 s4, 0x600
	s_movk_i32 s9, 0xc7
	s_waitcnt vmcnt(2)
	v_pk_add_f32 v[168:169], v[232:233], v[98:99]
	v_pk_add_f32 v[170:171], v[234:235], v[100:101]
	v_add_f32_e32 v1, v236, v98
	v_pk_mov_b32 v[128:129], v[98:99], v[100:101] op_sel:[1,0]
	v_add_f32_e32 v99, v239, v101
	s_waitcnt vmcnt(1)
	v_pk_add_f32 v[124:125], v[124:125], v[90:91]
	v_pk_add_f32 v[172:173], v[126:127], v[92:93]
	v_add_f32_e32 v178, v204, v90
	v_pk_mov_b32 v[126:127], v[90:91], v[92:93] op_sel:[1,0]
	v_add_f32_e32 v91, v207, v93
	v_add_f32_e32 v100, v240, v98
	v_add_f32_e32 v175, v243, v101
	v_add_f32_e32 v92, v212, v90
	v_add_f32_e32 v179, v215, v93
	v_add_f32_e32 v181, v147, v93
	v_cvt_pk_f16_f32 v147, v170, v171
	v_cvt_f16_f32_e32 v1, v1
	v_cvt_f16_f32_e32 v99, v99
	v_cvt_f16_f32_e32 v171, v178
	v_cvt_f16_f32_e32 v91, v91
	v_cvt_pk_f16_f32 v146, v168, v169
	v_cvt_f16_f32_e32 v100, v100
	v_cvt_f16_f32_e32 v168, v175
	v_cvt_pk_f16_f32 v124, v124, v125
	v_cvt_pk_f16_f32 v125, v172, v173
	v_cvt_f16_f32_e32 v92, v92
	v_cvt_f16_f32_e32 v172, v179
	v_add_f32_e32 v180, v144, v90
	s_waitcnt vmcnt(0)
	v_pk_add_f32 v[144:145], v[148:149], v[82:83]
	v_pk_add_f32 v[148:149], v[156:157], v[128:129]
	v_pk_add_f32 v[156:157], v[158:159], v[128:129]
	v_pk_add_f32 v[158:159], v[160:161], v[128:129]
	v_pk_add_f32 v[160:161], v[162:163], v[126:127]
	v_pk_add_f32 v[162:163], v[164:165], v[126:127]
	v_cvt_pk_f16_f32 v144, v144, v145
	v_cvt_pk_f16_f32 v145, v148, v149
	v_cvt_pk_f16_f32 v148, v156, v157
	v_cvt_pk_f16_f32 v157, v160, v161
	v_cvt_pk_f16_f32 v149, v158, v159
	v_cvt_pk_f16_f32 v159, v162, v163
	ds_write2_b64 v130, v[146:147], v[124:125] offset1:4
	v_pack_b32_f16 v124, v1, v145
	v_alignbit_b32 v125, v99, v145, 16
	v_pack_b32_f16 v156, v171, v157
	v_alignbit_b32 v157, v91, v157, 16
	v_pack_b32_f16 v146, v100, v148
	v_alignbit_b32 v147, v168, v148, 16
	v_pack_b32_f16 v158, v92, v159
	v_alignbit_b32 v159, v172, v159, 16
	ds_write2_b64 v132, v[124:125], v[156:157] offset0:32 offset1:36
	ds_write2_b64 v131, v[146:147], v[158:159] offset0:64 offset1:68
	v_pk_add_f32 v[124:125], v[150:151], v[84:85]
	v_add_f32_e32 v1, v152, v82
	v_cvt_pk_f16_f32 v145, v124, v125
	v_pk_mov_b32 v[124:125], v[82:83], v[84:85] op_sel:[1,0]
	v_add_f32_e32 v83, v155, v85
	v_cvt_f16_f32_e32 v1, v1
	v_cvt_f16_f32_e32 v83, v83
	ds_write_b64 v130, v[144:145] offset:64
	v_mov_b32_e32 v144, v153
	v_mov_b32_e32 v145, v154
	v_pk_add_f32 v[144:145], v[144:145], v[124:125]
	v_add_f32_e32 v176, v244, v98
	v_cvt_pk_f16_f32 v84, v144, v145
	v_pack_b32_f16 v144, v1, v84
	v_alignbit_b32 v145, v83, v84, 16
	v_add_f32_e32 v1, v114, v82
	v_add_f32_e32 v83, v117, v85
	v_cvt_f16_f32_e32 v1, v1
	v_cvt_f16_f32_e32 v83, v83
	v_mov_b32_e32 v114, v115
	v_mov_b32_e32 v115, v116
	v_pk_add_f32 v[114:115], v[114:115], v[124:125]
	v_add_f32_e32 v177, v247, v101
	v_cvt_pk_f16_f32 v84, v114, v115
	v_pack_b32_f16 v114, v1, v84
	v_alignbit_b32 v115, v83, v84, 16
	v_add_f32_e32 v1, v110, v82
	v_add_f32_e32 v83, v113, v85
	v_cvt_f16_f32_e32 v1, v1
	v_cvt_f16_f32_e32 v83, v83
	v_mov_b32_e32 v110, v111
	v_mov_b32_e32 v111, v112
	v_cvt_f16_f32_e32 v169, v176
	v_cvt_f16_f32_e32 v170, v177
	v_cvt_f16_f32_e32 v173, v180
	v_pk_add_f32 v[164:165], v[166:167], v[126:127]
	v_cvt_f16_f32_e32 v166, v181
	v_pk_add_f32 v[110:111], v[110:111], v[124:125]
	v_cvt_pk_f16_f32 v161, v164, v165
	v_cvt_pk_f16_f32 v84, v110, v111
	v_pack_b32_f16 v110, v1, v84
	v_alignbit_b32 v111, v83, v84, 16
	ds_write_b64 v130, v[110:111] offset:37696
	v_add_lshl_u32 v111, v174, v0, 4
	v_mul_u32_u24_e32 v83, 0x310, v142
	v_pack_b32_f16 v148, v169, v149
	v_alignbit_b32 v149, v170, v149, 16
	v_pack_b32_f16 v160, v173, v161
	v_alignbit_b32 v161, v166, v161, 16
	v_add_u32_e32 v91, 0x9000, v130
	v_add3_u32 v83, v111, v83, s8
	v_or_b32_e32 v84, 0x200, v0
	ds_write2_b64 v91, v[148:149], v[160:161] offset0:96 offset1:100
	ds_write_b64 v130, v[144:145] offset:12608
	ds_write_b64 v130, v[114:115] offset:25152
	s_waitcnt lgkmcnt(0)
	s_barrier
	ds_read_b128 v[114:117], v83
	v_mul_u32_u24_e32 v92, 0x556, v84
	v_lshrrev_b32_e32 v92, 16, v92
	v_or_b32_e32 v1, s7, v143
	v_mul_lo_u32 v99, v92, s5
	v_mul_lo_u32 v112, v1, s4
	v_add_lshl_u32 v113, v99, v84, 4
	v_mul_u32_u24_e32 v84, 0x310, v92
	v_add_u32_e32 v1, v112, v111
	v_add3_u32 v84, v113, v84, s8
	ds_read_b128 v[142:145], v84
	s_waitcnt lgkmcnt(1)
	buffer_store_dwordx4 v[114:117], v1, s[0:3], 0 offen sc1
	v_lshlrev_b32_e32 v1, 3, v92
	v_bitop3_b32 v154, v1, s9, v92 bitop3:0xc8
	v_or_b32_e32 v1, s7, v154
	v_mul_lo_u32 v114, v1, s4
	v_add_u32_e32 v1, v114, v113
	s_waitcnt lgkmcnt(0)
	buffer_store_dwordx4 v[142:145], v1, s[0:3], 0 offen sc1
	v_or_b32_e32 v1, 0x400, v0
	v_mul_u32_u24_e32 v92, 0x556, v1
	v_lshrrev_b32_e32 v92, 16, v92
	v_mul_lo_u32 v99, v92, s5
	v_lshlrev_b32_e32 v100, 3, v92
	s_movk_i32 s9, 0x1c7
	v_bitop3_b32 v155, v100, s9, v92 bitop3:0xc8
	v_add_lshl_u32 v115, v99, v1, 4
	v_mul_u32_u24_e32 v92, 0x310, v92
	v_or_b32_e32 v100, s7, v155
	v_add3_u32 v92, v115, v92, s8
	v_or_b32_e32 v99, 0x600, v0
	v_mul_lo_u32 v116, v100, s4
	ds_read_b128 v[142:145], v92
	v_mul_u32_u24_e32 v100, 0x556, v99
	v_lshrrev_b32_e32 v100, 16, v100
	v_mul_lo_u32 v110, v100, s5
	v_add_lshl_u32 v117, v110, v99, 4
	v_mul_u32_u24_e32 v99, 0x310, v100
	v_add_u32_e32 v1, v116, v115
	v_add3_u32 v99, v117, v99, s8
	ds_read_b128 v[146:149], v99
	s_waitcnt lgkmcnt(1)
	buffer_store_dwordx4 v[142:145], v1, s[0:3], 0 offen sc1
	v_lshlrev_b32_e32 v1, 3, v100
	v_bitop3_b32 v156, v1, s9, v100 bitop3:0xc8
	v_add_u32_e32 v1, s7, v156
	v_mul_lo_u32 v142, v1, s4
	v_add_u32_e32 v1, v142, v117
	s_waitcnt lgkmcnt(0)
	buffer_store_dwordx4 v[146:149], v1, s[0:3], 0 offen sc1
	v_or_b32_e32 v1, 0x800, v0
	v_mul_u32_u24_e32 v100, 0xaab, v1
	v_lshrrev_b32_e32 v100, 17, v100
	v_mul_lo_u32 v110, v100, s5
	v_lshlrev_b32_e32 v143, 3, v100
	v_bitop3_b32 v157, v143, s9, v100 bitop3:0xc8
	v_add_lshl_u32 v144, v110, v1, 4
	v_mul_u32_u24_e32 v100, 0x310, v100
	v_or_b32_e32 v0, 0xa00, v0
	v_add3_u32 v100, v100, v144, s8
	v_mul_u32_u24_e32 v110, 0xaab, v0
	ds_read_b128 v[146:149], v100
	v_lshrrev_b32_e32 v158, 17, v110
	v_mul_lo_u32 v110, v158, s5
	v_or_b32_e32 v143, s7, v157
	v_add_lshl_u32 v145, v110, v0, 4
	v_mul_u32_u24_e32 v0, 0x310, v158
	v_mul_lo_u32 v143, v143, s4
	v_add3_u32 v110, v0, v145, s8
	v_add_u32_e32 v1, v143, v144
	ds_read_b128 v[150:153], v110
	v_lshlrev_b32_e32 v0, 3, v158
	s_movk_i32 s5, 0x3c7
	s_waitcnt lgkmcnt(1)
	buffer_store_dwordx4 v[146:149], v1, s[0:3], 0 offen sc1
	v_mov_b32_e32 v1, v108
	v_add_f32_e32 v102, v102, v98
	v_bitop3_b32 v147, v0, s5, v158 bitop3:0xc8
	v_add_u32_e32 v0, s7, v147
	v_mul_lo_u32 v146, v0, s4
	v_add_u32_e32 v0, v146, v145
	s_waitcnt lgkmcnt(0)
	buffer_store_dwordx4 v[150:153], v0, s[0:3], 0 offen sc1
	v_add_f32_e32 v0, v106, v98
	v_cvt_f16_f32_e32 v106, v0
	v_mov_b32_e32 v0, v107
	v_pk_add_f32 v[0:1], v[0:1], v[128:129]
	v_add_f32_e32 v94, v94, v98
	v_cvt_pk_f16_f32 v1, v0, v1
	v_pack_b32_f16 v0, v106, v1
	v_cvt_f16_f32_e32 v106, v102
	v_mov_b32_e32 v102, v103
	v_mov_b32_e32 v103, v104
	v_add_f32_e32 v104, v105, v101
	v_cvt_f16_f32_e32 v104, v104
	v_pk_add_f32 v[102:103], v[102:103], v[128:129]
	v_add_f32_e32 v86, v86, v98
	v_cvt_pk_f16_f32 v103, v102, v103
	v_pack_b32_f16 v102, v106, v103
	v_alignbit_b32 v103, v104, v103, 16
	v_cvt_f16_f32_e32 v104, v94
	v_mov_b32_e32 v94, v95
	v_mov_b32_e32 v95, v96
	v_add_f32_e32 v96, v97, v101
	v_cvt_f16_f32_e32 v96, v96
	v_pk_add_f32 v[94:95], v[94:95], v[128:129]
	v_add_f32_e32 v78, v78, v90
	v_cvt_pk_f16_f32 v95, v94, v95
	v_pack_b32_f16 v94, v104, v95
	v_alignbit_b32 v95, v96, v95, 16
	v_cvt_f16_f32_e32 v96, v86
	v_mov_b32_e32 v86, v87
	v_mov_b32_e32 v87, v88
	v_add_f32_e32 v88, v89, v101
	v_cvt_f16_f32_e32 v88, v88
	v_pk_add_f32 v[86:87], v[86:87], v[128:129]
	v_add_f32_e32 v107, v109, v101
	v_cvt_pk_f16_f32 v87, v86, v87
	v_pack_b32_f16 v86, v96, v87
	v_alignbit_b32 v87, v88, v87, 16
	v_cvt_f16_f32_e32 v88, v78
	v_mov_b32_e32 v78, v79
	v_mov_b32_e32 v79, v80
	v_add_f32_e32 v80, v81, v93
	v_cvt_f16_f32_e32 v107, v107
	v_cvt_f16_f32_e32 v80, v80
	v_pk_add_f32 v[78:79], v[78:79], v[126:127]
	s_nop 0
	v_cvt_pk_f16_f32 v79, v78, v79
	v_alignbit_b32 v1, v107, v1, 16
	v_pack_b32_f16 v78, v88, v79
	v_alignbit_b32 v79, v80, v79, 16
	s_barrier
	ds_write2_b64 v130, v[0:1], v[78:79] offset1:4
	v_add_f32_e32 v0, v74, v90
	v_cvt_f16_f32_e32 v74, v0
	v_mov_b32_e32 v0, v75
	v_add_f32_e32 v75, v77, v93
	v_cvt_f16_f32_e32 v75, v75
	v_mov_b32_e32 v1, v76
	v_pk_add_f32 v[0:1], v[0:1], v[126:127]
	s_nop 0
	v_cvt_pk_f16_f32 v1, v0, v1
	v_pack_b32_f16 v0, v74, v1
	v_alignbit_b32 v1, v75, v1, 16
	ds_write2_b64 v132, v[102:103], v[0:1] offset0:32 offset1:36
	v_add_f32_e32 v0, v70, v90
	v_cvt_f16_f32_e32 v70, v0
	v_mov_b32_e32 v0, v71
	v_add_f32_e32 v71, v73, v93
	v_cvt_f16_f32_e32 v71, v71
	v_mov_b32_e32 v1, v72
	v_pk_add_f32 v[0:1], v[0:1], v[126:127]
	s_nop 0
	v_cvt_pk_f16_f32 v1, v0, v1
	v_pack_b32_f16 v0, v70, v1
	v_alignbit_b32 v1, v71, v1, 16
	ds_write2_b64 v131, v[94:95], v[0:1] offset0:64 offset1:68
	v_add_f32_e32 v0, v66, v90
	v_cvt_f16_f32_e32 v66, v0
	v_mov_b32_e32 v0, v67
	v_add_f32_e32 v67, v69, v93
	v_cvt_f16_f32_e32 v67, v67
	v_mov_b32_e32 v1, v68
	v_pk_add_f32 v[0:1], v[0:1], v[126:127]
	v_mul_lo_u32 v68, v140, s4
	v_cvt_pk_f16_f32 v1, v0, v1
	v_pack_b32_f16 v0, v66, v1
	v_alignbit_b32 v1, v67, v1, 16
	ds_write2_b64 v91, v[86:87], v[0:1] offset0:96 offset1:100
	v_add_f32_e32 v0, v62, v82
	v_cvt_f16_f32_e32 v62, v0
	v_mov_b32_e32 v0, v63
	v_add_f32_e32 v63, v65, v85
	v_cvt_f16_f32_e32 v63, v63
	v_mov_b32_e32 v1, v64
	v_pk_add_f32 v[0:1], v[0:1], v[124:125]
	s_nop 0
	v_cvt_pk_f16_f32 v1, v0, v1
	v_pack_b32_f16 v0, v62, v1
	v_alignbit_b32 v1, v63, v1, 16
	ds_write_b64 v130, v[0:1] offset:64
	v_add_f32_e32 v0, v58, v82
	v_cvt_f16_f32_e32 v58, v0
	v_mov_b32_e32 v0, v59
	v_add_f32_e32 v59, v61, v85
	v_cvt_f16_f32_e32 v59, v59
	v_mov_b32_e32 v1, v60
	v_pk_add_f32 v[0:1], v[0:1], v[124:125]
	s_nop 0
	v_cvt_pk_f16_f32 v1, v0, v1
	v_pack_b32_f16 v0, v58, v1
	v_alignbit_b32 v1, v59, v1, 16
	ds_write_b64 v130, v[0:1] offset:12608
	v_add_f32_e32 v0, v54, v82
	v_cvt_f16_f32_e32 v54, v0
	v_mov_b32_e32 v0, v55
	v_add_f32_e32 v55, v57, v85
	v_cvt_f16_f32_e32 v55, v55
	v_mov_b32_e32 v1, v56
	v_pk_add_f32 v[0:1], v[0:1], v[124:125]
	s_nop 0
	v_cvt_pk_f16_f32 v1, v0, v1
	v_pack_b32_f16 v0, v54, v1
	v_alignbit_b32 v1, v55, v1, 16
	ds_write_b64 v130, v[0:1] offset:25152
	v_add_f32_e32 v0, v50, v82
	v_cvt_f16_f32_e32 v50, v0
	v_mov_b32_e32 v0, v51
	v_add_f32_e32 v51, v53, v85
	v_cvt_f16_f32_e32 v51, v51
	v_mov_b32_e32 v1, v52
	v_pk_add_f32 v[0:1], v[0:1], v[124:125]
	s_nop 0
	v_cvt_pk_f16_f32 v1, v0, v1
	v_pack_b32_f16 v0, v50, v1
	v_alignbit_b32 v1, v51, v1, 16
	ds_write_b64 v130, v[0:1] offset:37696
	s_waitcnt lgkmcnt(0)
	s_barrier
	global_load_dwordx4 v[50:53], v[122:123], off
	global_load_dwordx4 v[54:57], v[122:123], off offset:1024
	global_load_dwordx4 v[58:61], v[122:123], off offset:2048
	ds_read_b128 v[62:65], v83
	ds_read_b128 v[70:73], v84
	v_add_u32_e32 v0, v68, v111
	ds_read_b128 v[74:77], v99
	s_waitcnt lgkmcnt(2)
	buffer_store_dwordx4 v[62:65], v0, s[0:3], 0 offen sc1
	v_or_b32_e32 v0, s6, v154
	v_mul_lo_u32 v69, v0, s4
	ds_read_b128 v[62:65], v92
	v_add_u32_e32 v0, v69, v113
	s_waitcnt lgkmcnt(2)
	buffer_store_dwordx4 v[70:73], v0, s[0:3], 0 offen sc1
	v_or_b32_e32 v0, s6, v155
	s_nop 0
	v_mul_lo_u32 v72, v0, s4
	v_add_u32_e32 v0, v72, v115
	s_waitcnt lgkmcnt(0)
	buffer_store_dwordx4 v[62:65], v0, s[0:3], 0 offen sc1
	v_add_u32_e32 v0, s6, v156
	v_mul_lo_u32 v70, v0, s4
	ds_read_b128 v[62:65], v100
	v_add_u32_e32 v0, v70, v117
	buffer_store_dwordx4 v[74:77], v0, s[0:3], 0 offen sc1
	v_or_b32_e32 v0, s6, v157
	v_mul_lo_u32 v71, v0, s4
	v_add_u32_e32 v0, v71, v144
	ds_read_b128 v[74:77], v110
	s_waitcnt lgkmcnt(1)
	buffer_store_dwordx4 v[62:65], v0, s[0:3], 0 offen sc1
	ds_read_b128 v[62:65], v135
	ds_read_b128 v[78:81], v135 offset:8192
	ds_read_b128 v[86:89], v135 offset:16384
	ds_read_b128 v[94:97], v135 offset:24576
	ds_read_b128 v[102:105], v135 offset:32768
	ds_read_b128 v[106:109], v135 offset:40960
	ds_read_b128 v[124:127], v135 offset:49152
	ds_read_b128 v[148:151], v135 offset:57344
	v_add_u32_e32 v0, s6, v147
	v_mul_lo_u32 v73, v0, s4
	v_add_u32_e32 v0, v73, v145
	s_waitcnt lgkmcnt(8)
	buffer_store_dwordx4 v[74:77], v0, s[0:3], 0 offen sc1
	s_waitcnt lgkmcnt(7)
	s_nop 0
	v_mfma_f32_16x16x32_f16 v[74:77], v[38:41], v[62:65], 0
	s_waitcnt lgkmcnt(6)
	v_mfma_f32_16x16x32_f16 v[152:155], v[38:41], v[78:81], 0
	s_waitcnt lgkmcnt(5)
	v_mfma_f32_16x16x32_f16 v[156:159], v[38:41], v[86:89], 0
	s_waitcnt lgkmcnt(4)
	v_mfma_f32_16x16x32_f16 v[160:163], v[38:41], v[94:97], 0
	s_waitcnt lgkmcnt(3)
	v_mfma_f32_16x16x32_f16 v[164:167], v[38:41], v[102:105], 0
	s_waitcnt lgkmcnt(2)
	v_mfma_f32_16x16x32_f16 v[168:171], v[38:41], v[106:109], 0
	s_waitcnt lgkmcnt(1)
	v_mfma_f32_16x16x32_f16 v[172:175], v[38:41], v[124:127], 0
	s_waitcnt lgkmcnt(0)
	v_mfma_f32_16x16x32_f16 v[38:41], v[38:41], v[148:151], 0
	v_mfma_f32_16x16x32_f16 v[176:179], v[26:29], v[62:65], 0
	v_mfma_f32_16x16x32_f16 v[180:183], v[26:29], v[78:81], 0
	v_mfma_f32_16x16x32_f16 v[184:187], v[26:29], v[86:89], 0
	v_mfma_f32_16x16x32_f16 v[188:191], v[26:29], v[94:97], 0
	v_mfma_f32_16x16x32_f16 v[192:195], v[26:29], v[102:105], 0
	v_mfma_f32_16x16x32_f16 v[196:199], v[26:29], v[106:109], 0
	v_mfma_f32_16x16x32_f16 v[200:203], v[26:29], v[124:127], 0
	v_mfma_f32_16x16x32_f16 v[26:29], v[26:29], v[148:151], 0
	v_mfma_f32_16x16x32_f16 v[62:65], v[10:13], v[62:65], 0
	v_mfma_f32_16x16x32_f16 v[78:81], v[10:13], v[78:81], 0
	v_mfma_f32_16x16x32_f16 v[86:89], v[10:13], v[86:89], 0
	v_mfma_f32_16x16x32_f16 v[94:97], v[10:13], v[94:97], 0
	v_mfma_f32_16x16x32_f16 v[102:105], v[10:13], v[102:105], 0
	v_mfma_f32_16x16x32_f16 v[106:109], v[10:13], v[106:109], 0
	v_mfma_f32_16x16x32_f16 v[124:127], v[10:13], v[124:127], 0
	v_mfma_f32_16x16x32_f16 v[10:13], v[10:13], v[148:151], 0
	s_mov_b32 s4, 0x34000
	v_add_co_u32_e32 v66, vcc, s4, v118
	s_mov_b32 s4, 0x35000
	s_nop 0
	v_addc_co_u32_e32 v67, vcc, 0, v119, vcc
	v_add_co_u32_e32 v118, vcc, s4, v118
	s_nop 1
	v_addc_co_u32_e32 v119, vcc, 0, v119, vcc
	global_load_dwordx4 v[148:151], v[118:119], off offset:-4096
	global_load_dwordx4 v[204:207], v[122:123], off offset:3072
	global_load_dwordx4 v[208:211], v[66:67], off offset:1024
	ds_read_b128 v[212:215], v133
	ds_read_b128 v[216:219], v133 offset:8192
	ds_read_b128 v[220:223], v133 offset:16384
	ds_read_b128 v[224:227], v133 offset:24576
	ds_read_b128 v[228:231], v133 offset:32768
	ds_read_b128 v[232:235], v133 offset:40960
	ds_read_b128 v[236:239], v133 offset:49152
	ds_read_b128 v[240:243], v133 offset:57344
	s_waitcnt lgkmcnt(7)
	v_mfma_f32_16x16x32_f16 v[74:77], v[22:25], v[212:215], v[74:77]
	s_waitcnt lgkmcnt(6)
	v_mfma_f32_16x16x32_f16 v[152:155], v[22:25], v[216:219], v[152:155]
	s_waitcnt lgkmcnt(5)
	v_mfma_f32_16x16x32_f16 v[156:159], v[22:25], v[220:223], v[156:159]
	s_waitcnt lgkmcnt(4)
	v_mfma_f32_16x16x32_f16 v[160:163], v[22:25], v[224:227], v[160:163]
	s_waitcnt lgkmcnt(3)
	v_mfma_f32_16x16x32_f16 v[164:167], v[22:25], v[228:231], v[164:167]
	s_waitcnt lgkmcnt(2)
	v_mfma_f32_16x16x32_f16 v[168:171], v[22:25], v[232:235], v[168:171]
	s_waitcnt lgkmcnt(1)
	v_mfma_f32_16x16x32_f16 v[172:175], v[22:25], v[236:239], v[172:175]
	s_waitcnt lgkmcnt(0)
	v_mfma_f32_16x16x32_f16 v[22:25], v[22:25], v[240:243], v[38:41]
	v_mfma_f32_16x16x32_f16 v[38:41], v[6:9], v[212:215], v[176:179]
	v_mfma_f32_16x16x32_f16 v[176:179], v[6:9], v[216:219], v[180:183]
	v_mfma_f32_16x16x32_f16 v[180:183], v[6:9], v[220:223], v[184:187]
	v_mfma_f32_16x16x32_f16 v[184:187], v[6:9], v[224:227], v[188:191]
	v_mfma_f32_16x16x32_f16 v[188:191], v[6:9], v[228:231], v[192:195]
	v_mfma_f32_16x16x32_f16 v[192:195], v[6:9], v[232:235], v[196:199]
	v_mfma_f32_16x16x32_f16 v[196:199], v[6:9], v[236:239], v[200:203]
	v_mfma_f32_16x16x32_f16 v[6:9], v[6:9], v[240:243], v[26:29]
	v_mfma_f32_16x16x32_f16 v[26:29], v[2:5], v[212:215], v[62:65]
	v_mfma_f32_16x16x32_f16 v[62:65], v[2:5], v[216:219], v[78:81]
	v_mfma_f32_16x16x32_f16 v[78:81], v[2:5], v[220:223], v[86:89]
	v_mfma_f32_16x16x32_f16 v[86:89], v[2:5], v[224:227], v[94:97]
	v_mfma_f32_16x16x32_f16 v[94:97], v[2:5], v[228:231], v[102:105]
	v_mfma_f32_16x16x32_f16 v[102:105], v[2:5], v[232:235], v[106:109]
	v_mfma_f32_16x16x32_f16 v[106:109], v[2:5], v[236:239], v[124:127]
	v_mfma_f32_16x16x32_f16 v[0:3], v[2:5], v[240:243], v[10:13]
	s_nop 2
	global_load_dwordx4 v[10:13], v[66:67], off offset:2048
	global_load_dwordx4 v[122:125], v[66:67], off offset:3072
	global_load_dwordx4 v[126:129], v[118:119], off
	ds_read_b128 v[200:203], v134
	ds_read_b128 v[212:215], v134 offset:8192
	ds_read_b128 v[216:219], v134 offset:16384
	ds_read_b128 v[220:223], v134 offset:24576
	ds_read_b128 v[224:227], v134 offset:32768
	ds_read_b128 v[228:231], v134 offset:40960
	ds_read_b128 v[232:235], v134 offset:49152
	ds_read_b128 v[236:239], v134 offset:57344
	s_waitcnt lgkmcnt(7)
	v_mfma_f32_16x16x32_f16 v[74:77], v[30:33], v[200:203], v[74:77]
	s_waitcnt lgkmcnt(6)
	v_mfma_f32_16x16x32_f16 v[152:155], v[30:33], v[212:215], v[152:155]
	s_waitcnt lgkmcnt(5)
	v_mfma_f32_16x16x32_f16 v[156:159], v[30:33], v[216:219], v[156:159]
	s_waitcnt lgkmcnt(4)
	v_mfma_f32_16x16x32_f16 v[160:163], v[30:33], v[220:223], v[160:163]
	s_waitcnt lgkmcnt(3)
	v_mfma_f32_16x16x32_f16 v[164:167], v[30:33], v[224:227], v[164:167]
	s_waitcnt lgkmcnt(2)
	v_mfma_f32_16x16x32_f16 v[168:171], v[30:33], v[228:231], v[168:171]
	s_waitcnt lgkmcnt(1)
	v_mfma_f32_16x16x32_f16 v[172:175], v[30:33], v[232:235], v[172:175]
	s_waitcnt lgkmcnt(0)
	v_mfma_f32_16x16x32_f16 v[22:25], v[30:33], v[236:239], v[22:25]
	v_mfma_f32_16x16x32_f16 v[30:33], v[14:17], v[200:203], v[38:41]
	v_mfma_f32_16x16x32_f16 v[38:41], v[14:17], v[212:215], v[176:179]
	v_mfma_f32_16x16x32_f16 v[176:179], v[14:17], v[216:219], v[180:183]
	v_mfma_f32_16x16x32_f16 v[180:183], v[14:17], v[220:223], v[184:187]
	v_mfma_f32_16x16x32_f16 v[184:187], v[14:17], v[224:227], v[188:191]
	v_mfma_f32_16x16x32_f16 v[188:191], v[14:17], v[228:231], v[192:195]
	v_mfma_f32_16x16x32_f16 v[192:195], v[14:17], v[232:235], v[196:199]
	v_mfma_f32_16x16x32_f16 v[4:7], v[14:17], v[236:239], v[6:9]
	v_mfma_f32_16x16x32_f16 v[14:17], v[18:21], v[200:203], v[26:29]
	v_mfma_f32_16x16x32_f16 v[26:29], v[18:21], v[212:215], v[62:65]
	v_mfma_f32_16x16x32_f16 v[62:65], v[18:21], v[216:219], v[78:81]
	v_mfma_f32_16x16x32_f16 v[78:81], v[18:21], v[220:223], v[86:89]
	v_mfma_f32_16x16x32_f16 v[86:89], v[18:21], v[224:227], v[94:97]
	v_mfma_f32_16x16x32_f16 v[94:97], v[18:21], v[228:231], v[102:105]
	v_mfma_f32_16x16x32_f16 v[102:105], v[18:21], v[232:235], v[106:109]
	v_mfma_f32_16x16x32_f16 v[0:3], v[18:21], v[236:239], v[0:3]
	global_load_dwordx4 v[18:21], v[118:119], off offset:1024
	s_nop 0
	global_load_dwordx4 v[106:109], v[118:119], off offset:2048
	global_load_dwordx4 v[196:199], v[118:119], off offset:3072
	ds_read_b128 v[200:203], v136
	ds_read_b128 v[212:215], v136 offset:8192
	ds_read_b128 v[216:219], v136 offset:16384
	ds_read_b128 v[220:223], v136 offset:24576
	ds_read_b128 v[224:227], v136 offset:32768
	ds_read_b128 v[228:231], v136 offset:40960
	ds_read_b128 v[232:235], v136 offset:49152
	ds_read_b128 v[236:239], v136 offset:57344
	s_waitcnt lgkmcnt(7)
	v_mfma_f32_16x16x32_f16 v[74:77], v[46:49], v[200:203], v[74:77]
	s_waitcnt lgkmcnt(6)
	v_mfma_f32_16x16x32_f16 v[152:155], v[46:49], v[212:215], v[152:155]
	s_waitcnt lgkmcnt(5)
	v_mfma_f32_16x16x32_f16 v[156:159], v[46:49], v[216:219], v[156:159]
	s_waitcnt lgkmcnt(4)
	v_mfma_f32_16x16x32_f16 v[160:163], v[46:49], v[220:223], v[160:163]
	s_waitcnt lgkmcnt(3)
	v_mfma_f32_16x16x32_f16 v[164:167], v[46:49], v[224:227], v[164:167]
	s_waitcnt lgkmcnt(2)
	v_mfma_f32_16x16x32_f16 v[168:171], v[46:49], v[228:231], v[168:171]
	s_waitcnt lgkmcnt(1)
	v_mfma_f32_16x16x32_f16 v[172:175], v[46:49], v[232:235], v[172:175]
	s_waitcnt lgkmcnt(0)
	v_mfma_f32_16x16x32_f16 v[22:25], v[46:49], v[236:239], v[22:25]
	v_mfma_f32_16x16x32_f16 v[30:33], v[42:45], v[200:203], v[30:33]
	v_mfma_f32_16x16x32_f16 v[38:41], v[42:45], v[212:215], v[38:41]
	v_mfma_f32_16x16x32_f16 v[46:49], v[42:45], v[216:219], v[176:179]
	v_mfma_f32_16x16x32_f16 v[176:179], v[42:45], v[220:223], v[180:183]
	v_mfma_f32_16x16x32_f16 v[180:183], v[42:45], v[224:227], v[184:187]
	v_mfma_f32_16x16x32_f16 v[184:187], v[42:45], v[228:231], v[188:191]
	v_mfma_f32_16x16x32_f16 v[188:191], v[42:45], v[232:235], v[192:195]
	v_mfma_f32_16x16x32_f16 v[4:7], v[42:45], v[236:239], v[4:7]
	v_mfma_f32_16x16x32_f16 v[14:17], v[34:37], v[200:203], v[14:17]
	v_mfma_f32_16x16x32_f16 v[26:29], v[34:37], v[212:215], v[26:29]
	v_mfma_f32_16x16x32_f16 v[42:45], v[34:37], v[216:219], v[62:65]
	v_mfma_f32_16x16x32_f16 v[62:65], v[34:37], v[220:223], v[78:81]
	v_mfma_f32_16x16x32_f16 v[78:81], v[34:37], v[224:227], v[86:89]
	v_mfma_f32_16x16x32_f16 v[86:89], v[34:37], v[228:231], v[94:97]
	v_mfma_f32_16x16x32_f16 v[94:97], v[34:37], v[232:235], v[102:105]
	v_mfma_f32_16x16x32_f16 v[0:3], v[34:37], v[236:239], v[0:3]
	ds_read_b128 v[34:37], v137
	s_nop 0
	ds_read_b128 v[102:105], v137 offset:8192
	ds_read_b128 v[192:195], v137 offset:16384
	ds_read_b128 v[200:203], v137 offset:24576
	ds_read_b128 v[212:215], v137 offset:32768
	ds_read_b128 v[216:219], v137 offset:40960
	ds_read_b128 v[220:223], v137 offset:49152
	ds_read_b128 v[134:137], v137 offset:57344
	s_waitcnt vmcnt(17) lgkmcnt(7)
	v_mfma_f32_16x16x32_f16 v[74:77], v[50:53], v[34:37], v[74:77]
	s_waitcnt lgkmcnt(6)
	v_mfma_f32_16x16x32_f16 v[152:155], v[50:53], v[102:105], v[152:155]
	s_waitcnt lgkmcnt(5)
	v_mfma_f32_16x16x32_f16 v[156:159], v[50:53], v[192:195], v[156:159]
	s_waitcnt lgkmcnt(4)
	v_mfma_f32_16x16x32_f16 v[160:163], v[50:53], v[200:203], v[160:163]
	s_waitcnt lgkmcnt(3)
	v_mfma_f32_16x16x32_f16 v[164:167], v[50:53], v[212:215], v[164:167]
	s_waitcnt lgkmcnt(2)
	v_mfma_f32_16x16x32_f16 v[168:171], v[50:53], v[216:219], v[168:171]
	s_waitcnt lgkmcnt(1)
	v_mfma_f32_16x16x32_f16 v[172:175], v[50:53], v[220:223], v[172:175]
	s_waitcnt lgkmcnt(0)
	v_mfma_f32_16x16x32_f16 v[22:25], v[50:53], v[134:137], v[22:25]
	s_waitcnt vmcnt(16)
	v_mfma_f32_16x16x32_f16 v[30:33], v[54:57], v[34:37], v[30:33]
	v_mfma_f32_16x16x32_f16 v[38:41], v[54:57], v[102:105], v[38:41]
	v_mfma_f32_16x16x32_f16 v[46:49], v[54:57], v[192:195], v[46:49]
	v_mfma_f32_16x16x32_f16 v[50:53], v[54:57], v[200:203], v[176:179]
	v_mfma_f32_16x16x32_f16 v[176:179], v[54:57], v[212:215], v[180:183]
	v_mfma_f32_16x16x32_f16 v[180:183], v[54:57], v[216:219], v[184:187]
	v_mfma_f32_16x16x32_f16 v[184:187], v[54:57], v[220:223], v[188:191]
	v_mfma_f32_16x16x32_f16 v[4:7], v[54:57], v[134:137], v[4:7]
	s_waitcnt vmcnt(15)
	v_mfma_f32_16x16x32_f16 v[14:17], v[58:61], v[34:37], v[14:17]
	v_mfma_f32_16x16x32_f16 v[26:29], v[58:61], v[102:105], v[26:29]
	v_mfma_f32_16x16x32_f16 v[34:37], v[58:61], v[192:195], v[42:45]
	v_mfma_f32_16x16x32_f16 v[42:45], v[58:61], v[200:203], v[62:65]
	v_mfma_f32_16x16x32_f16 v[54:57], v[58:61], v[212:215], v[78:81]
	v_mfma_f32_16x16x32_f16 v[62:65], v[58:61], v[216:219], v[86:89]
	v_mfma_f32_16x16x32_f16 v[78:81], v[58:61], v[220:223], v[94:97]
	v_mfma_f32_16x16x32_f16 v[0:3], v[58:61], v[134:137], v[0:3]
	ds_read_b128 v[58:61], v138
	ds_read_b128 v[86:89], v138 offset:8192
	ds_read_b128 v[94:97], v138 offset:16384
	ds_read_b128 v[102:105], v138 offset:24576
	ds_read_b128 v[134:137], v138 offset:32768
	ds_read_b128 v[188:191], v138 offset:40960
	ds_read_b128 v[192:195], v138 offset:49152
	ds_read_b128 v[200:203], v138 offset:57344
	s_waitcnt vmcnt(7) lgkmcnt(7)
	v_mfma_f32_16x16x32_f16 v[74:77], v[204:207], v[58:61], v[74:77]
	s_waitcnt lgkmcnt(6)
	v_mfma_f32_16x16x32_f16 v[152:155], v[204:207], v[86:89], v[152:155]
	s_waitcnt lgkmcnt(5)
	v_mfma_f32_16x16x32_f16 v[156:159], v[204:207], v[94:97], v[156:159]
	s_waitcnt lgkmcnt(4)
	v_mfma_f32_16x16x32_f16 v[160:163], v[204:207], v[102:105], v[160:163]
	s_waitcnt lgkmcnt(3)
	v_mfma_f32_16x16x32_f16 v[164:167], v[204:207], v[134:137], v[164:167]
	s_waitcnt lgkmcnt(2)
	v_mfma_f32_16x16x32_f16 v[168:171], v[204:207], v[188:191], v[168:171]
	s_waitcnt lgkmcnt(1)
	v_mfma_f32_16x16x32_f16 v[172:175], v[204:207], v[192:195], v[172:175]
	s_waitcnt lgkmcnt(0)
	v_mfma_f32_16x16x32_f16 v[22:25], v[204:207], v[200:203], v[22:25]
	v_mfma_f32_16x16x32_f16 v[30:33], v[148:151], v[58:61], v[30:33]
	v_mfma_f32_16x16x32_f16 v[38:41], v[148:151], v[86:89], v[38:41]
	v_mfma_f32_16x16x32_f16 v[46:49], v[148:151], v[94:97], v[46:49]
	v_mfma_f32_16x16x32_f16 v[50:53], v[148:151], v[102:105], v[50:53]
	v_mfma_f32_16x16x32_f16 v[176:179], v[148:151], v[134:137], v[176:179]
	v_mfma_f32_16x16x32_f16 v[180:183], v[148:151], v[188:191], v[180:183]
	v_mfma_f32_16x16x32_f16 v[184:187], v[148:151], v[192:195], v[184:187]
	v_mfma_f32_16x16x32_f16 v[4:7], v[148:151], v[200:203], v[4:7]
	s_waitcnt vmcnt(6)
	v_mfma_f32_16x16x32_f16 v[14:17], v[208:211], v[58:61], v[14:17]
	v_mfma_f32_16x16x32_f16 v[26:29], v[208:211], v[86:89], v[26:29]
	v_mfma_f32_16x16x32_f16 v[34:37], v[208:211], v[94:97], v[34:37]
	v_mfma_f32_16x16x32_f16 v[42:45], v[208:211], v[102:105], v[42:45]
	v_mfma_f32_16x16x32_f16 v[54:57], v[208:211], v[134:137], v[54:57]
	v_mfma_f32_16x16x32_f16 v[58:61], v[208:211], v[188:191], v[62:65]
	v_mfma_f32_16x16x32_f16 v[62:65], v[208:211], v[192:195], v[78:81]
	v_mfma_f32_16x16x32_f16 v[0:3], v[208:211], v[200:203], v[0:3]
	s_nop 1
	ds_read_b128 v[78:81], v139
	ds_read_b128 v[86:89], v139 offset:8192
	ds_read_b128 v[94:97], v139 offset:16384
	ds_read_b128 v[102:105], v139 offset:24576
	ds_read_b128 v[134:137], v139 offset:32768
	ds_read_b128 v[148:151], v139 offset:40960
	ds_read_b128 v[188:191], v139 offset:49152
	ds_read_b128 v[192:195], v139 offset:57344
	s_waitcnt vmcnt(5) lgkmcnt(7)
	v_mfma_f32_16x16x32_f16 v[74:77], v[10:13], v[78:81], v[74:77]
	s_waitcnt lgkmcnt(6)
	v_mfma_f32_16x16x32_f16 v[152:155], v[10:13], v[86:89], v[152:155]
	s_waitcnt lgkmcnt(5)
	v_mfma_f32_16x16x32_f16 v[156:159], v[10:13], v[94:97], v[156:159]
	s_waitcnt lgkmcnt(4)
	v_mfma_f32_16x16x32_f16 v[160:163], v[10:13], v[102:105], v[160:163]
	s_waitcnt lgkmcnt(3)
	v_mfma_f32_16x16x32_f16 v[164:167], v[10:13], v[134:137], v[164:167]
	s_waitcnt lgkmcnt(2)
	v_mfma_f32_16x16x32_f16 v[168:171], v[10:13], v[148:151], v[168:171]
	s_waitcnt lgkmcnt(1)
	v_mfma_f32_16x16x32_f16 v[172:175], v[10:13], v[188:191], v[172:175]
	s_waitcnt lgkmcnt(0)
	v_mfma_f32_16x16x32_f16 v[8:11], v[10:13], v[192:195], v[22:25]
	s_waitcnt vmcnt(4)
	v_mfma_f32_16x16x32_f16 v[22:25], v[122:125], v[78:81], v[30:33]
	v_mfma_f32_16x16x32_f16 v[30:33], v[122:125], v[86:89], v[38:41]
	v_mfma_f32_16x16x32_f16 v[200:203], v[122:125], v[94:97], v[46:49]
	v_mfma_f32_16x16x32_f16 v[48:51], v[122:125], v[102:105], v[50:53]
	v_mfma_f32_16x16x32_f16 v[176:179], v[122:125], v[134:137], v[176:179]
	v_mfma_f32_16x16x32_f16 v[180:183], v[122:125], v[148:151], v[180:183]
	v_mfma_f32_16x16x32_f16 v[184:187], v[122:125], v[188:191], v[184:187]
	v_mfma_f32_16x16x32_f16 v[4:7], v[122:125], v[192:195], v[4:7]
	s_waitcnt vmcnt(3)
	v_mfma_f32_16x16x32_f16 v[12:15], v[126:129], v[78:81], v[14:17]
	v_mfma_f32_16x16x32_f16 v[78:81], v[126:129], v[86:89], v[26:29]
	v_mfma_f32_16x16x32_f16 v[86:89], v[126:129], v[94:97], v[34:37]
	v_mfma_f32_16x16x32_f16 v[40:43], v[126:129], v[102:105], v[42:45]
	v_mfma_f32_16x16x32_f16 v[94:97], v[126:129], v[134:137], v[54:57]
	v_mfma_f32_16x16x32_f16 v[102:105], v[126:129], v[148:151], v[58:61]
	v_mfma_f32_16x16x32_f16 v[64:67], v[126:129], v[188:191], v[62:65]
	v_mfma_f32_16x16x32_f16 v[0:3], v[126:129], v[192:195], v[0:3]
	s_nop 1
	ds_read_b128 v[60:63], v141
	ds_read_b128 v[122:125], v141 offset:8192
	ds_read_b128 v[126:129], v141 offset:16384
	ds_read_b128 v[134:137], v141 offset:24576
	ds_read_b128 v[148:151], v141 offset:32768
	ds_read_b128 v[188:191], v141 offset:40960
	ds_read_b128 v[192:195], v141 offset:49152
	ds_read_b128 v[138:141], v141 offset:57344
	s_waitcnt vmcnt(2) lgkmcnt(7)
	v_mfma_f32_16x16x32_f16 v[74:77], v[18:21], v[60:63], v[74:77]
	s_waitcnt lgkmcnt(6)
	v_mfma_f32_16x16x32_f16 v[152:155], v[18:21], v[122:125], v[152:155]
	s_waitcnt lgkmcnt(5)
	v_mfma_f32_16x16x32_f16 v[156:159], v[18:21], v[126:129], v[156:159]
	s_waitcnt lgkmcnt(4)
	v_mfma_f32_16x16x32_f16 v[160:163], v[18:21], v[134:137], v[160:163]
	s_waitcnt lgkmcnt(3)
	v_mfma_f32_16x16x32_f16 v[56:59], v[18:21], v[148:151], v[164:167]
	s_waitcnt lgkmcnt(2)
	v_mfma_f32_16x16x32_f16 v[52:55], v[18:21], v[188:191], v[168:171]
	s_waitcnt lgkmcnt(1)
	v_mfma_f32_16x16x32_f16 v[44:47], v[18:21], v[192:195], v[172:175]
	s_waitcnt lgkmcnt(0)
	v_mfma_f32_16x16x32_f16 v[36:39], v[18:21], v[138:141], v[8:11]
	s_waitcnt vmcnt(1)
	v_mfma_f32_16x16x32_f16 v[164:167], v[106:109], v[60:63], v[22:25]
	v_mfma_f32_16x16x32_f16 v[168:171], v[106:109], v[122:125], v[30:33]
	v_mfma_f32_16x16x32_f16 v[172:175], v[106:109], v[126:129], v[200:203]
	v_mfma_f32_16x16x32_f16 v[200:203], v[106:109], v[134:137], v[48:51]
	v_mfma_f32_16x16x32_f16 v[32:35], v[106:109], v[148:151], v[176:179]
	v_mfma_f32_16x16x32_f16 v[24:27], v[106:109], v[188:191], v[180:183]
	v_mfma_f32_16x16x32_f16 v[20:23], v[106:109], v[192:195], v[184:187]
	v_mfma_f32_16x16x32_f16 v[16:19], v[106:109], v[138:141], v[4:7]
	s_waitcnt vmcnt(0)
	v_mfma_f32_16x16x32_f16 v[106:109], v[196:199], v[60:63], v[12:15]
	v_mfma_f32_16x16x32_f16 v[78:81], v[196:199], v[122:125], v[78:81]
	v_mfma_f32_16x16x32_f16 v[86:89], v[196:199], v[126:129], v[86:89]
	v_mfma_f32_16x16x32_f16 v[60:63], v[196:199], v[134:137], v[40:43]
	v_mfma_f32_16x16x32_f16 v[12:15], v[196:199], v[148:151], v[94:97]
	v_mfma_f32_16x16x32_f16 v[8:11], v[196:199], v[188:191], v[102:105]
	v_mfma_f32_16x16x32_f16 v[4:7], v[196:199], v[192:195], v[64:67]
	v_mfma_f32_16x16x32_f16 v[0:3], v[196:199], v[138:141], v[0:3]
	global_load_dwordx4 v[48:51], v[120:121], off offset:1536
	global_load_dwordx4 v[40:43], v[120:121], off offset:1600
	global_load_dwordx4 v[28:31], v[120:121], off offset:1664
	v_mov_b32_e32 v94, v157
	v_mov_b32_e32 v95, v158
	v_mov_b32_e32 v96, v161
	v_mov_b32_e32 v97, v162
	v_mov_b32_e32 v64, v153
	v_mov_b32_e32 v65, v154
	v_mov_b32_e32 v102, v169
	v_mov_b32_e32 v103, v170
	v_mov_b32_e32 v104, v173
	v_mov_b32_e32 v105, v174
	v_mov_b32_e32 v118, v201
	v_mov_b32_e32 v119, v202
	s_barrier
	s_waitcnt vmcnt(2)
	v_pk_add_f32 v[74:75], v[74:75], v[48:49]
	v_add_f32_e32 v82, v152, v48
	v_pk_mov_b32 v[120:121], v[48:49], v[50:51] op_sel:[1,0]
	v_add_f32_e32 v49, v155, v51
	s_waitcnt vmcnt(1)
	v_pk_add_f32 v[122:123], v[164:165], v[40:41]
	v_add_f32_e32 v98, v168, v40
	v_pk_mov_b32 v[66:67], v[40:41], v[42:43] op_sel:[1,0]
	v_add_f32_e32 v41, v171, v43
	v_pk_add_f32 v[76:77], v[76:77], v[50:51]
	v_add_f32_e32 v50, v156, v48
	v_add_f32_e32 v85, v159, v51
	v_add_f32_e32 v90, v160, v48
	v_add_f32_e32 v93, v163, v51
	v_pk_add_f32 v[124:125], v[166:167], v[42:43]
	v_add_f32_e32 v42, v172, v40
	v_add_f32_e32 v101, v175, v43
	v_add_f32_e32 v126, v200, v40
	v_add_f32_e32 v127, v203, v43
	v_cvt_f16_f32_e32 v82, v82
	v_cvt_f16_f32_e32 v49, v49
	v_cvt_f16_f32_e32 v98, v98
	v_cvt_f16_f32_e32 v41, v41
	v_cvt_pk_f16_f32 v74, v74, v75
	v_cvt_pk_f16_f32 v75, v76, v77
	v_cvt_f16_f32_e32 v50, v50
	v_pk_add_f32 v[76:77], v[94:95], v[120:121]
	v_cvt_f16_f32_e32 v85, v85
	v_cvt_f16_f32_e32 v90, v90
	v_pk_add_f32 v[94:95], v[96:97], v[120:121]
	v_cvt_f16_f32_e32 v93, v93
	v_cvt_pk_f16_f32 v96, v122, v123
	v_cvt_f16_f32_e32 v42, v42
	v_cvt_f16_f32_e32 v101, v101
	v_cvt_f16_f32_e32 v122, v126
	v_cvt_f16_f32_e32 v123, v127
	v_pk_add_f32 v[64:65], v[64:65], v[120:121]
	v_pk_add_f32 v[102:103], v[102:103], v[66:67]
	v_pk_add_f32 v[104:105], v[104:105], v[66:67]
	v_pk_add_f32 v[118:119], v[118:119], v[66:67]
	v_cvt_pk_f16_f32 v65, v64, v65
	v_cvt_pk_f16_f32 v76, v76, v77
	v_cvt_pk_f16_f32 v77, v94, v95
	v_cvt_pk_f16_f32 v95, v102, v103
	s_waitcnt vmcnt(0)
	v_pk_add_f32 v[106:107], v[106:107], v[28:29]
	v_pk_add_f32 v[108:109], v[108:109], v[30:31]
	v_cvt_pk_f16_f32 v97, v124, v125
	v_cvt_pk_f16_f32 v102, v104, v105
	v_cvt_pk_f16_f32 v103, v118, v119
	v_pack_b32_f16 v64, v82, v65
	v_alignbit_b32 v65, v49, v65, 16
	v_pack_b32_f16 v94, v98, v95
	v_alignbit_b32 v95, v41, v95, 16
	v_add_f32_e32 v78, v78, v28
	v_cvt_pk_f16_f32 v106, v106, v107
	v_cvt_pk_f16_f32 v107, v108, v109
	ds_write2_b64 v130, v[74:75], v[96:97] offset1:4
	ds_write_b64 v130, v[106:107] offset:64
	v_pack_b32_f16 v74, v50, v76
	v_alignbit_b32 v75, v85, v76, 16
	v_pack_b32_f16 v76, v90, v77
	v_alignbit_b32 v77, v93, v77, 16
	v_pack_b32_f16 v96, v42, v102
	v_alignbit_b32 v97, v101, v102, 16
	v_pack_b32_f16 v102, v122, v103
	v_alignbit_b32 v103, v123, v103, 16
	ds_write2_b64 v132, v[64:65], v[94:95] offset0:32 offset1:36
	ds_write2_b64 v131, v[74:75], v[96:97] offset0:64 offset1:68
	ds_write2_b64 v91, v[76:77], v[102:103] offset0:96 offset1:100
	v_pk_mov_b32 v[64:65], v[28:29], v[30:31] op_sel:[1,0]
	v_add_f32_e32 v29, v81, v31
	v_cvt_f16_f32_e32 v78, v78
	v_cvt_f16_f32_e32 v29, v29
	v_mov_b32_e32 v74, v79
	v_mov_b32_e32 v75, v80
	v_pk_add_f32 v[74:75], v[74:75], v[64:65]
	v_add_f32_e32 v56, v56, v48
	v_cvt_pk_f16_f32 v30, v74, v75
	v_pack_b32_f16 v74, v78, v30
	v_alignbit_b32 v75, v29, v30, 16
	v_add_f32_e32 v29, v86, v28
	v_add_f32_e32 v30, v89, v31
	v_cvt_f16_f32_e32 v29, v29
	v_cvt_f16_f32_e32 v30, v30
	ds_write_b64 v130, v[74:75] offset:12608
	v_mov_b32_e32 v74, v87
	v_mov_b32_e32 v75, v88
	v_pk_add_f32 v[74:75], v[74:75], v[64:65]
	v_add_f32_e32 v52, v52, v48
	v_cvt_pk_f16_f32 v41, v74, v75
	v_pack_b32_f16 v74, v29, v41
	v_alignbit_b32 v75, v30, v41, 16
	v_add_f32_e32 v29, v60, v28
	v_add_f32_e32 v30, v63, v31
	v_cvt_f16_f32_e32 v29, v29
	v_cvt_f16_f32_e32 v30, v30
	v_mov_b32_e32 v60, v61
	v_mov_b32_e32 v61, v62
	v_pk_add_f32 v[60:61], v[60:61], v[64:65]
	ds_write_b64 v130, v[74:75] offset:25152
	v_cvt_pk_f16_f32 v41, v60, v61
	v_pack_b32_f16 v60, v29, v41
	v_alignbit_b32 v61, v30, v41, 16
	ds_write_b64 v130, v[60:61] offset:37696
	s_waitcnt lgkmcnt(0)
	s_barrier
	ds_read_b128 v[60:63], v83
	ds_read_b128 v[74:77], v84
	v_add_u32_e32 v29, 0x300, v111
	v_add_u32_e32 v30, v29, v112
	v_add_f32_e32 v44, v44, v48
	s_waitcnt lgkmcnt(1)
	buffer_store_dwordx4 v[60:63], v30, s[0:3], 0 offen sc1
	v_add_u32_e32 v30, 0x300, v113
	ds_read_b128 v[60:63], v92
	v_add_u32_e32 v41, v30, v114
	s_waitcnt lgkmcnt(1)
	buffer_store_dwordx4 v[74:77], v41, s[0:3], 0 offen sc1
	ds_read_b128 v[74:77], v99
	v_add_u32_e32 v41, 0x300, v115
	v_add_u32_e32 v42, v41, v116
	s_waitcnt lgkmcnt(1)
	buffer_store_dwordx4 v[60:63], v42, s[0:3], 0 offen sc1
	v_add_u32_e32 v42, 0x300, v117
	ds_read_b128 v[60:63], v100
	v_add_u32_e32 v49, v42, v142
	s_waitcnt lgkmcnt(1)
	buffer_store_dwordx4 v[74:77], v49, s[0:3], 0 offen sc1
	ds_read_b128 v[74:77], v110
	v_add_u32_e32 v49, 0x300, v144
	v_add_u32_e32 v50, v49, v143
	s_waitcnt lgkmcnt(1)
	buffer_store_dwordx4 v[60:63], v50, s[0:3], 0 offen sc1
	v_add_u32_e32 v50, 0x300, v145
	v_add_f32_e32 v36, v36, v48
	v_add_u32_e32 v60, v50, v146
	s_waitcnt lgkmcnt(0)
	buffer_store_dwordx4 v[74:77], v60, s[0:3], 0 offen sc1
	v_cvt_f16_f32_e32 v60, v56
	v_mov_b32_e32 v56, v57
	v_mov_b32_e32 v57, v58
	v_add_f32_e32 v58, v59, v51
	v_cvt_f16_f32_e32 v58, v58
	v_pk_add_f32 v[56:57], v[56:57], v[120:121]
	v_add_f32_e32 v32, v32, v40
	v_cvt_pk_f16_f32 v57, v56, v57
	v_pack_b32_f16 v56, v60, v57
	v_alignbit_b32 v57, v58, v57, 16
	v_cvt_f16_f32_e32 v58, v52
	v_mov_b32_e32 v52, v53
	v_mov_b32_e32 v53, v54
	v_add_f32_e32 v54, v55, v51
	v_cvt_f16_f32_e32 v54, v54
	v_pk_add_f32 v[52:53], v[52:53], v[120:121]
	v_add_f32_e32 v24, v24, v40
	v_cvt_pk_f16_f32 v53, v52, v53
	v_pack_b32_f16 v52, v58, v53
	v_alignbit_b32 v53, v54, v53, 16
	v_cvt_f16_f32_e32 v54, v44
	v_mov_b32_e32 v44, v45
	v_mov_b32_e32 v45, v46
	v_add_f32_e32 v46, v47, v51
	v_cvt_f16_f32_e32 v46, v46
	v_pk_add_f32 v[44:45], v[44:45], v[120:121]
	s_nop 0
	v_cvt_pk_f16_f32 v45, v44, v45
	v_pack_b32_f16 v44, v54, v45
	v_alignbit_b32 v45, v46, v45, 16
	v_cvt_f16_f32_e32 v46, v36
	v_mov_b32_e32 v36, v37
	v_mov_b32_e32 v37, v38
	v_add_f32_e32 v38, v39, v51
	v_cvt_f16_f32_e32 v38, v38
	v_pk_add_f32 v[36:37], v[36:37], v[120:121]
	s_barrier
	v_cvt_pk_f16_f32 v37, v36, v37
	v_pack_b32_f16 v36, v46, v37
	v_alignbit_b32 v37, v38, v37, 16
	v_cvt_f16_f32_e32 v38, v32
	v_mov_b32_e32 v32, v33
	v_mov_b32_e32 v33, v34
	v_add_f32_e32 v34, v35, v43
	v_cvt_f16_f32_e32 v34, v34
	v_pk_add_f32 v[32:33], v[32:33], v[66:67]
	s_nop 0
	v_cvt_pk_f16_f32 v33, v32, v33
	v_pack_b32_f16 v32, v38, v33
	v_alignbit_b32 v33, v34, v33, 16
	ds_write2_b64 v130, v[56:57], v[32:33] offset1:4
	v_cvt_f16_f32_e32 v32, v24
	v_mov_b32_e32 v24, v25
	v_mov_b32_e32 v25, v26
	v_add_f32_e32 v26, v27, v43
	v_cvt_f16_f32_e32 v26, v26
	v_pk_add_f32 v[24:25], v[24:25], v[66:67]
	v_add_f32_e32 v20, v20, v40
	v_cvt_pk_f16_f32 v25, v24, v25
	v_pack_b32_f16 v24, v32, v25
	v_alignbit_b32 v25, v26, v25, 16
	ds_write2_b64 v132, v[52:53], v[24:25] offset0:32 offset1:36
	v_cvt_f16_f32_e32 v24, v20
	v_mov_b32_e32 v20, v21
	v_mov_b32_e32 v21, v22
	v_add_f32_e32 v22, v23, v43
	v_cvt_f16_f32_e32 v22, v22
	v_pk_add_f32 v[20:21], v[20:21], v[66:67]
	v_add_f32_e32 v16, v16, v40
	v_cvt_pk_f16_f32 v21, v20, v21
	v_pack_b32_f16 v20, v24, v21
	v_alignbit_b32 v21, v22, v21, 16
	ds_write2_b64 v131, v[44:45], v[20:21] offset0:64 offset1:68
	v_cvt_f16_f32_e32 v20, v16
	v_mov_b32_e32 v16, v17
	v_mov_b32_e32 v17, v18
	v_add_f32_e32 v18, v19, v43
	v_cvt_f16_f32_e32 v18, v18
	v_pk_add_f32 v[16:17], v[16:17], v[66:67]
	v_add_f32_e32 v12, v12, v28
	v_cvt_pk_f16_f32 v17, v16, v17
	v_pack_b32_f16 v16, v20, v17
	v_alignbit_b32 v17, v18, v17, 16
	ds_write2_b64 v91, v[36:37], v[16:17] offset0:96 offset1:100
	v_cvt_f16_f32_e32 v16, v12
	v_mov_b32_e32 v12, v13
	v_mov_b32_e32 v13, v14
	v_add_f32_e32 v14, v15, v31
	v_cvt_f16_f32_e32 v14, v14
	v_pk_add_f32 v[12:13], v[12:13], v[64:65]
	v_add_f32_e32 v8, v8, v28
	v_cvt_pk_f16_f32 v13, v12, v13
	v_pack_b32_f16 v12, v16, v13
	v_alignbit_b32 v13, v14, v13, 16
	ds_write_b64 v130, v[12:13] offset:64
	v_cvt_f16_f32_e32 v12, v8
	v_mov_b32_e32 v8, v9
	v_mov_b32_e32 v9, v10
	v_add_f32_e32 v10, v11, v31
	v_cvt_f16_f32_e32 v10, v10
	v_pk_add_f32 v[8:9], v[8:9], v[64:65]
	v_add_f32_e32 v4, v4, v28
	v_cvt_pk_f16_f32 v9, v8, v9
	v_pack_b32_f16 v8, v12, v9
	v_alignbit_b32 v9, v10, v9, 16
	ds_write_b64 v130, v[8:9] offset:12608
	v_cvt_f16_f32_e32 v8, v4
	v_mov_b32_e32 v4, v5
	v_mov_b32_e32 v5, v6
	v_add_f32_e32 v6, v7, v31
	v_cvt_f16_f32_e32 v6, v6
	v_pk_add_f32 v[4:5], v[4:5], v[64:65]
	v_add_f32_e32 v0, v0, v28
	v_cvt_pk_f16_f32 v5, v4, v5
	v_pack_b32_f16 v4, v8, v5
	v_alignbit_b32 v5, v6, v5, 16
	ds_write_b64 v130, v[4:5] offset:25152
	v_cvt_f16_f32_e32 v4, v0
	v_mov_b32_e32 v0, v1
	v_mov_b32_e32 v1, v2
	v_add_f32_e32 v2, v3, v31
	v_cvt_f16_f32_e32 v2, v2
	v_pk_add_f32 v[0:1], v[0:1], v[64:65]
	v_add_u32_e32 v8, v29, v68
	v_cvt_pk_f16_f32 v1, v0, v1
	v_pack_b32_f16 v0, v4, v1
	v_alignbit_b32 v1, v2, v1, 16
	ds_write_b64 v130, v[0:1] offset:37696
	s_waitcnt lgkmcnt(0)
	s_barrier
	ds_read_b128 v[0:3], v83
	ds_read_b128 v[4:7], v84
	v_add_u32_e32 v12, v42, v70
	s_waitcnt lgkmcnt(1)
	buffer_store_dwordx4 v[0:3], v8, s[0:3], 0 offen sc1
	ds_read_b128 v[0:3], v92
	v_add_u32_e32 v8, v30, v69
	s_waitcnt lgkmcnt(1)
	buffer_store_dwordx4 v[4:7], v8, s[0:3], 0 offen sc1
	v_add_u32_e32 v8, v41, v72
	ds_read_b128 v[4:7], v99
	s_waitcnt lgkmcnt(1)
	buffer_store_dwordx4 v[0:3], v8, s[0:3], 0 offen sc1
	ds_read_b128 v[0:3], v100
	ds_read_b128 v[8:11], v110
	s_waitcnt lgkmcnt(2)
	buffer_store_dwordx4 v[4:7], v12, s[0:3], 0 offen sc1
	s_nop 1
	v_add_u32_e32 v4, v49, v71
	s_waitcnt lgkmcnt(1)
	buffer_store_dwordx4 v[0:3], v4, s[0:3], 0 offen sc1
	s_nop 1
	v_add_u32_e32 v0, v50, v73
	s_waitcnt lgkmcnt(0)
	buffer_store_dwordx4 v[8:11], v0, s[0:3], 0 offen sc1
	s_endpgm
	.p2alignl 8, 3212836864

.LBB4_155:
	s_setprio 0
	s_load_dword s0, s[0:1], 0x88
	s_lshl_b32 s1, s45, 6
	s_and_b32 s1, s1, 0xfffffe00
	s_or_b32 s2, s1, s44
	v_readfirstlane_b32 s4, v0
	s_waitcnt lgkmcnt(0)
	s_mul_i32 s3, s0, 0x60000
	s_mul_hi_i32 s1, s0, 0x60000
	s_add_u32 s3, s28, s3
	s_mulk_i32 s0, 0x300
	s_addc_u32 s5, s29, s1
	s_ashr_i32 s1, s0, 31
	s_lshl_b64 s[0:1], s[0:1], 2
	s_add_u32 s0, s30, s0
	s_addc_u32 s1, s31, s1
	s_lshr_b32 s6, s4, 6
	s_and_b32 s25, s25, 0xffff
	s_mul_i32 s4, s6, 0x6000
	v_and_b32_e32 v2, 63, v0
	s_mul_hi_u32 s7, s6, 0x6000
	s_add_u32 s4, s3, s4
	s_addc_u32 s5, s5, s7
	v_lshlrev_b32_e32 v56, 4, v2
	v_mov_b32_e32 v57, 0
	v_lshl_add_u64 v[54:55], s[4:5], 0, v[56:57]
	s_movk_i32 s3, 0x1000
	v_add_co_u32_e32 v50, vcc, s3, v54
	s_movk_i32 s3, 0x2000
	s_nop 0
	v_addc_co_u32_e32 v51, vcc, 0, v55, vcc
	v_add_co_u32_e32 v52, vcc, s3, v54
	global_load_dwordx4 v[2:5], v56, s[4:5] offset:1024
	global_load_dwordx4 v[6:9], v56, s[4:5] offset:2048
	v_addc_co_u32_e32 v53, vcc, 0, v55, vcc
	global_load_dwordx4 v[10:13], v56, s[4:5] offset:3072
	global_load_dwordx4 v[14:17], v[52:53], off offset:-4096
	global_load_dwordx4 v[18:21], v[50:51], off offset:1024
	global_load_dwordx4 v[22:25], v[50:51], off offset:2048
	global_load_dwordx4 v[26:29], v56, s[4:5]
	global_load_dwordx4 v[30:33], v[50:51], off offset:3072
	global_load_dwordx4 v[34:37], v[52:53], off
	global_load_dwordx4 v[38:41], v[52:53], off offset:1024
	global_load_dwordx4 v[42:45], v[52:53], off offset:2048
	global_load_dwordx4 v[46:49], v[52:53], off offset:3072
	s_movk_i32 s3, 0x3000
	v_add_co_u32_e32 v58, vcc, s3, v54
	s_movk_i32 s3, 0x4000
	s_nop 0
	v_addc_co_u32_e32 v59, vcc, 0, v55, vcc
	v_add_co_u32_e32 v140, vcc, s3, v54
	s_nop 1
	v_addc_co_u32_e32 v141, vcc, 0, v55, vcc
	s_barrier
	global_load_dwordx4 v[50:53], v[140:141], off offset:-4096
	global_load_dwordx4 v[62:65], v[58:59], off offset:1024
	global_load_dwordx4 v[68:71], v[58:59], off offset:2048
	v_lshlrev_b32_e32 v67, 9, v1
	v_xor_b32_e32 v61, v167, v1
	v_lshl_or_b32 v66, v61, 4, v67
	ds_read_b128 v[72:75], v66
	ds_read_b128 v[76:79], v66 offset:8192
	ds_read_b128 v[80:83], v66 offset:16384
	ds_read_b128 v[84:87], v66 offset:24576
	v_mul_u32_u24_e32 v60, 0x556, v0
	v_lshrrev_b32_e32 v60, 16, v60
	s_mul_i32 s3, s6, 48
	v_lshlrev_b32_e32 v61, 3, v60
	s_movk_i32 s5, 0x47
	v_lshl_or_b32 v56, v167, 2, s3
	s_mov_b32 s3, 0xfffffd0
	v_bitop3_b32 v61, v61, s5, v60 bitop3:0xc8
	s_mov_b32 s27, 0x20000
	s_mov_b32 s26, 0x1800000
	s_mul_i32 s4, s6, 0x60
	v_mul_lo_u32 v150, v60, s3
	v_or_b32_e32 v61, s2, v61
	s_waitcnt vmcnt(8) lgkmcnt(3)
	v_mfma_f32_16x16x32_f16 v[88:91], v[26:29], v[72:75], 0
	s_waitcnt lgkmcnt(2)
	v_mfma_f32_16x16x32_f16 v[92:95], v[26:29], v[76:79], 0
	s_waitcnt lgkmcnt(1)
	v_mfma_f32_16x16x32_f16 v[96:99], v[26:29], v[80:83], 0
	s_waitcnt lgkmcnt(0)
	v_mfma_f32_16x16x32_f16 v[26:29], v[26:29], v[84:87], 0
	v_mfma_f32_16x16x32_f16 v[100:103], v[2:5], v[72:75], 0
	v_mfma_f32_16x16x32_f16 v[104:107], v[2:5], v[76:79], 0
	v_mfma_f32_16x16x32_f16 v[108:111], v[2:5], v[80:83], 0
	v_mfma_f32_16x16x32_f16 v[2:5], v[2:5], v[84:87], 0
	v_mfma_f32_16x16x32_f16 v[112:115], v[6:9], v[72:75], 0
	v_mfma_f32_16x16x32_f16 v[74:77], v[6:9], v[76:79], 0
	v_mfma_f32_16x16x32_f16 v[78:81], v[6:9], v[80:83], 0
	v_mfma_f32_16x16x32_f16 v[6:9], v[6:9], v[84:87], 0
	global_load_dwordx4 v[82:85], v[58:59], off offset:3072
	global_load_dwordx4 v[116:119], v[140:141], off
	global_load_dwordx4 v[120:123], v[140:141], off offset:1024
	v_bitop3_b32 v58, v167, v1, 4 bitop3:0x36
	v_lshl_or_b32 v72, v58, 4, v67
	ds_read_b128 v[124:127], v72
	ds_read_b128 v[128:131], v72 offset:8192
	ds_read_b128 v[132:135], v72 offset:16384
	ds_read_b128 v[136:139], v72 offset:24576
	s_waitcnt lgkmcnt(3)
	v_mfma_f32_16x16x32_f16 v[86:89], v[10:13], v[124:127], v[88:91]
	s_waitcnt lgkmcnt(2)
	v_mfma_f32_16x16x32_f16 v[90:93], v[10:13], v[128:131], v[92:95]
	s_waitcnt lgkmcnt(1)
	v_mfma_f32_16x16x32_f16 v[94:97], v[10:13], v[132:135], v[96:99]
	s_waitcnt lgkmcnt(0)
	v_mfma_f32_16x16x32_f16 v[10:13], v[10:13], v[136:139], v[26:29]
	v_mfma_f32_16x16x32_f16 v[26:29], v[14:17], v[124:127], v[100:103]
	v_mfma_f32_16x16x32_f16 v[98:101], v[14:17], v[128:131], v[104:107]
	v_mfma_f32_16x16x32_f16 v[102:105], v[14:17], v[132:135], v[108:111]
	v_mfma_f32_16x16x32_f16 v[2:5], v[14:17], v[136:139], v[2:5]
	v_mfma_f32_16x16x32_f16 v[14:17], v[18:21], v[124:127], v[112:115]
	v_mfma_f32_16x16x32_f16 v[106:109], v[18:21], v[128:131], v[74:77]
	v_mfma_f32_16x16x32_f16 v[76:79], v[18:21], v[132:135], v[78:81]
	v_mfma_f32_16x16x32_f16 v[6:9], v[18:21], v[136:139], v[6:9]
	s_movk_i32 s5, 0x5000
	v_add_co_u32_e32 v58, vcc, s5, v54
	global_load_dwordx4 v[110:113], v[140:141], off offset:2048
	global_load_dwordx4 v[124:127], v[140:141], off offset:3072
	v_addc_co_u32_e32 v59, vcc, 0, v55, vcc
	global_load_dwordx4 v[128:131], v[58:59], off
	v_bitop3_b32 v18, v167, v1, 8 bitop3:0x36
	v_lshl_or_b32 v74, v18, 4, v67
	ds_read_b128 v[18:21], v74
	ds_read_b128 v[132:135], v74 offset:8192
	ds_read_b128 v[136:139], v74 offset:16384
	ds_read_b128 v[140:143], v74 offset:24576
	s_waitcnt lgkmcnt(3)
	v_mfma_f32_16x16x32_f16 v[86:89], v[22:25], v[18:21], v[86:89]
	s_waitcnt lgkmcnt(2)
	v_mfma_f32_16x16x32_f16 v[90:93], v[22:25], v[132:135], v[90:93]
	s_waitcnt lgkmcnt(1)
	v_mfma_f32_16x16x32_f16 v[94:97], v[22:25], v[136:139], v[94:97]
	s_waitcnt lgkmcnt(0)
	v_mfma_f32_16x16x32_f16 v[10:13], v[22:25], v[140:143], v[10:13]
	s_waitcnt vmcnt(13)
	v_mfma_f32_16x16x32_f16 v[22:25], v[30:33], v[18:21], v[26:29]
	v_mfma_f32_16x16x32_f16 v[26:29], v[30:33], v[132:135], v[98:101]
	v_mfma_f32_16x16x32_f16 v[98:101], v[30:33], v[136:139], v[102:105]
	v_mfma_f32_16x16x32_f16 v[2:5], v[30:33], v[140:143], v[2:5]
	s_waitcnt vmcnt(12)
	v_mfma_f32_16x16x32_f16 v[14:17], v[34:37], v[18:21], v[14:17]
	v_mfma_f32_16x16x32_f16 v[18:21], v[34:37], v[132:135], v[106:109]
	v_mfma_f32_16x16x32_f16 v[30:33], v[34:37], v[136:139], v[76:79]
	v_mfma_f32_16x16x32_f16 v[6:9], v[34:37], v[140:143], v[6:9]
	global_load_dwordx4 v[102:105], v[58:59], off offset:1024
	global_load_dwordx4 v[106:109], v[58:59], off offset:2048
	global_load_dwordx4 v[132:135], v[58:59], off offset:3072
	v_bitop3_b32 v34, v167, v1, 12 bitop3:0x36
	v_lshl_or_b32 v75, v34, 4, v67
	ds_read_b128 v[34:37], v75
	ds_read_b128 v[76:79], v75 offset:8192
	ds_read_b128 v[136:139], v75 offset:16384
	ds_read_b128 v[140:143], v75 offset:24576
	s_waitcnt vmcnt(14) lgkmcnt(3)
	v_mfma_f32_16x16x32_f16 v[86:89], v[38:41], v[34:37], v[86:89]
	s_waitcnt lgkmcnt(2)
	v_mfma_f32_16x16x32_f16 v[90:93], v[38:41], v[76:79], v[90:93]
	s_waitcnt lgkmcnt(1)
	v_mfma_f32_16x16x32_f16 v[94:97], v[38:41], v[136:139], v[94:97]
	s_waitcnt lgkmcnt(0)
	v_mfma_f32_16x16x32_f16 v[10:13], v[38:41], v[140:143], v[10:13]
	s_waitcnt vmcnt(13)
	v_mfma_f32_16x16x32_f16 v[38:41], v[42:45], v[34:37], v[22:25]
	v_mfma_f32_16x16x32_f16 v[144:147], v[42:45], v[76:79], v[26:29]
	v_mfma_f32_16x16x32_f16 v[98:101], v[42:45], v[136:139], v[98:101]
	v_mfma_f32_16x16x32_f16 v[2:5], v[42:45], v[140:143], v[2:5]
	s_waitcnt vmcnt(12)
	v_mfma_f32_16x16x32_f16 v[14:17], v[46:49], v[34:37], v[14:17]
	v_mfma_f32_16x16x32_f16 v[18:21], v[46:49], v[76:79], v[18:21]
	v_mfma_f32_16x16x32_f16 v[30:33], v[46:49], v[136:139], v[30:33]
	v_mfma_f32_16x16x32_f16 v[6:9], v[46:49], v[140:143], v[6:9]
	s_mov_b32 s5, 0x30000
	v_add_co_u32_e32 v58, vcc, s5, v54
	s_mov_b32 s5, 0x31000
	s_nop 0
	v_addc_co_u32_e32 v59, vcc, 0, v55, vcc
	v_add_co_u32_e32 v148, vcc, s5, v54
	v_bitop3_b32 v42, v167, v1, 16 bitop3:0x36
	s_nop 0
	v_addc_co_u32_e32 v149, vcc, 0, v55, vcc
	global_load_dwordx4 v[34:37], v[148:149], off offset:-4096
	global_load_dwordx4 v[26:29], v[58:59], off offset:1024
	global_load_dwordx4 v[22:25], v[58:59], off offset:2048
	v_lshl_or_b32 v76, v42, 4, v67
	ds_read_b128 v[42:45], v76
	ds_read_b128 v[46:49], v76 offset:8192
	ds_read_b128 v[78:81], v76 offset:16384
	ds_read_b128 v[136:139], v76 offset:24576
	s_waitcnt vmcnt(14) lgkmcnt(3)
	v_mfma_f32_16x16x32_f16 v[86:89], v[50:53], v[42:45], v[86:89]
	s_waitcnt lgkmcnt(2)
	v_mfma_f32_16x16x32_f16 v[90:93], v[50:53], v[46:49], v[90:93]
	s_waitcnt lgkmcnt(1)
	v_mfma_f32_16x16x32_f16 v[94:97], v[50:53], v[78:81], v[94:97]
	s_waitcnt lgkmcnt(0)
	v_mfma_f32_16x16x32_f16 v[10:13], v[50:53], v[136:139], v[10:13]
	s_waitcnt vmcnt(13)
	v_mfma_f32_16x16x32_f16 v[38:41], v[62:65], v[42:45], v[38:41]
	v_mfma_f32_16x16x32_f16 v[50:53], v[62:65], v[46:49], v[144:147]
	v_mfma_f32_16x16x32_f16 v[98:101], v[62:65], v[78:81], v[98:101]
	v_mfma_f32_16x16x32_f16 v[62:65], v[62:65], v[136:139], v[2:5]
	s_waitcnt vmcnt(12)
	v_mfma_f32_16x16x32_f16 v[42:45], v[68:71], v[42:45], v[14:17]
	v_mfma_f32_16x16x32_f16 v[18:21], v[68:71], v[46:49], v[18:21]
	v_mfma_f32_16x16x32_f16 v[30:33], v[68:71], v[78:81], v[30:33]
	v_mfma_f32_16x16x32_f16 v[46:49], v[68:71], v[136:139], v[6:9]
	global_load_dwordx4 v[14:17], v[58:59], off offset:3072
	s_nop 1
	global_load_dwordx4 v[6:9], v[148:149], off
	global_load_dwordx4 v[2:5], v[148:149], off offset:1024
	v_bitop3_b32 v58, v167, v1, 20 bitop3:0x36
	v_lshl_or_b32 v77, v58, 4, v67
	ds_read_b128 v[68:71], v77
	ds_read_b128 v[78:81], v77 offset:8192
	ds_read_b128 v[136:139], v77 offset:16384
	ds_read_b128 v[140:143], v77 offset:24576
	s_waitcnt vmcnt(14) lgkmcnt(3)
	v_mfma_f32_16x16x32_f16 v[86:89], v[82:85], v[68:71], v[86:89]
	s_waitcnt lgkmcnt(2)
	v_mfma_f32_16x16x32_f16 v[90:93], v[82:85], v[78:81], v[90:93]
	s_waitcnt lgkmcnt(1)
	v_mfma_f32_16x16x32_f16 v[94:97], v[82:85], v[136:139], v[94:97]
	s_waitcnt lgkmcnt(0)
	v_mfma_f32_16x16x32_f16 v[82:85], v[82:85], v[140:143], v[10:13]
	s_waitcnt vmcnt(13)
	v_mfma_f32_16x16x32_f16 v[38:41], v[116:119], v[68:71], v[38:41]
	v_mfma_f32_16x16x32_f16 v[50:53], v[116:119], v[78:81], v[50:53]
	v_mfma_f32_16x16x32_f16 v[98:101], v[116:119], v[136:139], v[98:101]
	v_mfma_f32_16x16x32_f16 v[62:65], v[116:119], v[140:143], v[62:65]
	s_waitcnt vmcnt(12)
	v_mfma_f32_16x16x32_f16 v[42:45], v[120:123], v[68:71], v[42:45]
	v_mfma_f32_16x16x32_f16 v[68:71], v[120:123], v[78:81], v[18:21]
	v_mfma_f32_16x16x32_f16 v[114:117], v[120:123], v[136:139], v[30:33]
	v_mfma_f32_16x16x32_f16 v[46:49], v[120:123], v[140:143], v[46:49]
	s_mov_b32 s5, 0x33000
	v_add_co_u32_e32 v58, vcc, s5, v54
	global_load_dwordx4 v[18:21], v[148:149], off offset:2048
	global_load_dwordx4 v[10:13], v[148:149], off offset:3072
	v_addc_co_u32_e32 v59, vcc, 0, v55, vcc
	global_load_dwordx4 v[30:33], v[58:59], off offset:-4096
	v_bitop3_b32 v73, v167, v1, 24 bitop3:0x36
	v_lshl_or_b32 v78, v73, 4, v67
	ds_read_b128 v[118:121], v78
	ds_read_b128 v[136:139], v78 offset:8192
	ds_read_b128 v[140:143], v78 offset:16384
	ds_read_b128 v[144:147], v78 offset:24576
	s_mov_b32 s5, 0x32000
	v_add_co_u32_e32 v148, vcc, s5, v54
	s_nop 1
	v_addc_co_u32_e32 v149, vcc, 0, v55, vcc
	s_waitcnt vmcnt(14) lgkmcnt(3)
	v_mfma_f32_16x16x32_f16 v[86:89], v[110:113], v[118:121], v[86:89]
	s_waitcnt lgkmcnt(2)
	v_mfma_f32_16x16x32_f16 v[90:93], v[110:113], v[136:139], v[90:93]
	s_waitcnt lgkmcnt(1)
	v_mfma_f32_16x16x32_f16 v[94:97], v[110:113], v[140:143], v[94:97]
	s_waitcnt lgkmcnt(0)
	v_mfma_f32_16x16x32_f16 v[80:83], v[110:113], v[144:147], v[82:85]
	s_waitcnt vmcnt(13)
	v_mfma_f32_16x16x32_f16 v[110:113], v[124:127], v[118:121], v[38:41]
	v_mfma_f32_16x16x32_f16 v[50:53], v[124:127], v[136:139], v[50:53]
	v_mfma_f32_16x16x32_f16 v[98:101], v[124:127], v[140:143], v[98:101]
	v_mfma_f32_16x16x32_f16 v[62:65], v[124:127], v[144:147], v[62:65]
	s_waitcnt vmcnt(12)
	v_mfma_f32_16x16x32_f16 v[118:121], v[128:131], v[118:121], v[42:45]
	v_mfma_f32_16x16x32_f16 v[68:71], v[128:131], v[136:139], v[68:71]
	v_mfma_f32_16x16x32_f16 v[114:117], v[128:131], v[140:143], v[114:117]
	v_mfma_f32_16x16x32_f16 v[122:125], v[128:131], v[144:147], v[46:49]
	s_nop 2
	global_load_dwordx4 v[46:49], v[148:149], off offset:1024
	global_load_dwordx4 v[42:45], v[148:149], off offset:2048
	global_load_dwordx4 v[38:41], v[148:149], off offset:3072
	v_bitop3_b32 v73, v167, v1, 28 bitop3:0x36
	v_lshl_or_b32 v79, v73, 4, v67
	ds_read_b128 v[126:129], v79
	ds_read_b128 v[136:139], v79 offset:8192
	ds_read_b128 v[140:143], v79 offset:16384
	ds_read_b128 v[144:147], v79 offset:24576
	s_waitcnt vmcnt(14) lgkmcnt(3)
	v_mfma_f32_16x16x32_f16 v[84:87], v[102:105], v[126:129], v[86:89]
	s_waitcnt lgkmcnt(2)
	v_mfma_f32_16x16x32_f16 v[88:91], v[102:105], v[136:139], v[90:93]
	s_waitcnt lgkmcnt(1)
	v_mfma_f32_16x16x32_f16 v[92:95], v[102:105], v[140:143], v[94:97]
	s_waitcnt lgkmcnt(0)
	v_mfma_f32_16x16x32_f16 v[80:83], v[102:105], v[144:147], v[80:83]
	s_waitcnt vmcnt(13)
	v_mfma_f32_16x16x32_f16 v[102:105], v[106:109], v[126:129], v[110:113]
	v_mfma_f32_16x16x32_f16 v[110:113], v[106:109], v[136:139], v[50:53]
	v_mfma_f32_16x16x32_f16 v[96:99], v[106:109], v[140:143], v[98:101]
	v_mfma_f32_16x16x32_f16 v[62:65], v[106:109], v[144:147], v[62:65]
	s_waitcnt vmcnt(12)
	v_mfma_f32_16x16x32_f16 v[106:109], v[132:135], v[126:129], v[118:121]
	v_mfma_f32_16x16x32_f16 v[118:121], v[132:135], v[136:139], v[68:71]
	v_mfma_f32_16x16x32_f16 v[114:117], v[132:135], v[140:143], v[114:117]
	v_mfma_f32_16x16x32_f16 v[50:53], v[132:135], v[144:147], v[122:125]
	v_lshl_add_u64 v[56:57], v[56:57], 2, s[0:1]
	s_nop 1
	global_load_dwordx4 v[122:125], v[56:57], off
	global_load_dwordx4 v[126:129], v[56:57], off offset:64
	global_load_dwordx4 v[130:133], v[56:57], off offset:128
	v_lshl_or_b32 v67, v167, 3, s4
	s_movk_i32 s0, 0x310
	v_mov_b32_e32 v100, v89
	v_mov_b32_e32 v101, v90
	v_mov_b32_e32 v134, v93
	v_mov_b32_e32 v135, v94
	v_mov_b32_e32 v140, v97
	v_mov_b32_e32 v141, v98
	v_mad_u32_u24 v69, v1, s0, v67
	v_mov_b32_e32 v143, v64
	v_mov_b32_e32 v136, v81
	v_mov_b32_e32 v137, v82
	v_mov_b32_e32 v138, v111
	v_mov_b32_e32 v139, v112
	v_mov_b32_e32 v142, v63
	v_add_u32_e32 v73, 0x8000, v69
	s_barrier
	v_add_u32_e32 v70, 0xb000, v69
	v_add_u32_e32 v71, 0xe000, v69
	v_add_u32_e32 v68, 0x9300, v69
	s_movk_i32 s1, 0x600
	s_movk_i32 s6, 0x1c7
	s_waitcnt vmcnt(2)
	v_pk_add_f32 v[84:85], v[84:85], v[122:123]
	v_add_f32_e32 v1, v88, v122
	v_pk_mov_b32 v[88:89], v[122:123], v[124:125] op_sel:[1,0]
	v_add_f32_e32 v67, v91, v125
	v_add_f32_e32 v92, v92, v122
	v_add_f32_e32 v93, v95, v125
	v_add_f32_e32 v94, v80, v122
	v_add_f32_e32 v95, v83, v125
	s_waitcnt vmcnt(1)
	v_add_f32_e32 v97, v110, v126
	v_add_f32_e32 v98, v113, v129
	v_add_f32_e32 v96, v96, v126
	v_add_f32_e32 v99, v99, v129
	v_cvt_pk_f16_f32 v64, v84, v85
	v_cvt_f16_f32_e32 v1, v1
	v_pk_add_f32 v[84:85], v[100:101], v[88:89]
	v_cvt_f16_f32_e32 v67, v67
	v_cvt_f16_f32_e32 v100, v92
	v_cvt_f16_f32_e32 v101, v93
	v_cvt_f16_f32_e32 v94, v94
	v_cvt_f16_f32_e32 v95, v95
	v_cvt_f16_f32_e32 v97, v97
	v_cvt_f16_f32_e32 v98, v98
	v_pk_add_f32 v[86:87], v[86:87], v[124:125]
	v_pk_add_f32 v[80:81], v[102:103], v[126:127]
	v_pk_add_f32 v[82:83], v[104:105], v[128:129]
	v_pk_mov_b32 v[90:91], v[126:127], v[128:129] op_sel:[1,0]
	v_cvt_f16_f32_e32 v96, v96
	v_cvt_f16_f32_e32 v99, v99
	v_add_f32_e32 v102, v62, v126
	v_add_f32_e32 v103, v65, v129
	s_waitcnt vmcnt(0)
	v_pk_add_f32 v[62:63], v[106:107], v[130:131]
	v_cvt_pk_f16_f32 v65, v86, v87
	v_pk_add_f32 v[86:87], v[134:135], v[88:89]
	v_pk_add_f32 v[88:89], v[136:137], v[88:89]
	v_cvt_pk_f16_f32 v80, v80, v81
	v_cvt_pk_f16_f32 v81, v82, v83
	v_pk_add_f32 v[82:83], v[138:139], v[90:91]
	v_pk_add_f32 v[92:93], v[140:141], v[90:91]
	v_cvt_pk_f16_f32 v62, v62, v63
	v_cvt_pk_f16_f32 v63, v84, v85
	v_cvt_pk_f16_f32 v84, v86, v87
	v_cvt_pk_f16_f32 v85, v88, v89
	v_cvt_pk_f16_f32 v86, v82, v83
	v_cvt_pk_f16_f32 v87, v92, v93
	ds_write2_b64 v73, v[64:65], v[80:81] offset1:4
	v_pack_b32_f16 v64, v1, v63
	v_alignbit_b32 v65, v67, v63, 16
	v_pack_b32_f16 v80, v100, v84
	v_alignbit_b32 v81, v101, v84, 16
	v_pack_b32_f16 v82, v94, v85
	v_alignbit_b32 v83, v95, v85, 16
	v_pack_b32_f16 v84, v97, v86
	v_alignbit_b32 v85, v98, v86, 16
	v_pack_b32_f16 v86, v96, v87
	v_alignbit_b32 v87, v99, v87, 16
	ds_write2_b64 v70, v[64:65], v[84:85] offset0:32 offset1:36
	ds_write2_b64 v71, v[80:81], v[86:87] offset0:64 offset1:68
	v_pk_add_f32 v[64:65], v[108:109], v[132:133]
	v_add_f32_e32 v1, v118, v130
	v_cvt_pk_f16_f32 v63, v64, v65
	v_cvt_f16_f32_e32 v1, v1
	v_add_f32_e32 v67, v121, v133
	ds_write_b64 v69, v[62:63] offset:32832
	v_mov_b32_e32 v62, v119
	v_mov_b32_e32 v63, v120
	v_pk_mov_b32 v[64:65], v[130:131], v[132:133] op_sel:[1,0]
	v_cvt_f16_f32_e32 v67, v67
	v_pk_add_f32 v[62:63], v[62:63], v[64:65]
	v_cvt_f16_f32_e32 v102, v102
	v_cvt_pk_f16_f32 v63, v62, v63
	v_pack_b32_f16 v62, v1, v63
	v_add_f32_e32 v1, v114, v130
	v_alignbit_b32 v63, v67, v63, 16
	v_cvt_f16_f32_e32 v1, v1
	ds_write_b64 v69, v[62:63] offset:45376
	v_mov_b32_e32 v62, v115
	v_mov_b32_e32 v63, v116
	v_pk_add_f32 v[62:63], v[62:63], v[64:65]
	v_add_f32_e32 v67, v117, v133
	v_cvt_pk_f16_f32 v63, v62, v63
	v_pack_b32_f16 v62, v1, v63
	v_add_f32_e32 v1, v50, v130
	v_mov_b32_e32 v50, v51
	v_mov_b32_e32 v51, v52
	v_add_f32_e32 v52, v53, v133
	v_cvt_f16_f32_e32 v103, v103
	v_cvt_f16_f32_e32 v67, v67
	v_cvt_f16_f32_e32 v1, v1
	v_cvt_f16_f32_e32 v52, v52
	v_pk_add_f32 v[90:91], v[142:143], v[90:91]
	v_pk_add_f32 v[50:51], v[50:51], v[64:65]
	v_cvt_pk_f16_f32 v89, v90, v91
	v_cvt_pk_f16_f32 v51, v50, v51
	v_pack_b32_f16 v88, v102, v89
	v_alignbit_b32 v89, v103, v89, 16
	v_add_u32_e32 v80, 0x8000, v68
	v_alignbit_b32 v63, v67, v63, 16
	v_pack_b32_f16 v50, v1, v51
	v_alignbit_b32 v51, v52, v51, 16
	ds_write2_b64 v80, v[82:83], v[88:89] offset1:4
	ds_write_b64 v69, v[62:63] offset:57920
	ds_write_b64 v68, v[50:51] offset:32832
	s_waitcnt lgkmcnt(0)
	s_barrier
	global_load_dwordx4 v[82:85], v[58:59], off
	global_load_dwordx4 v[86:89], v[58:59], off offset:1024
	global_load_dwordx4 v[90:93], v[58:59], off offset:2048
	v_add_lshl_u32 v52, v150, v0, 4
	v_mad_u64_u32 v[50:51], s[4:5], v61, s1, v[52:53]
	v_or_b32_e32 v1, 0x200, v0
	v_mad_u32_u24 v51, v60, s0, v52
	v_mul_u32_u24_e32 v52, 0x556, v1
	v_lshrrev_b32_e32 v53, 16, v52
	v_mul_lo_u32 v52, v53, s3
	v_add_lshl_u32 v52, v52, v1, 4
	v_lshlrev_b32_e32 v1, 3, v53
	s_movk_i32 s4, 0xc7
	ds_read_b128 v[60:63], v51 offset:32768
	v_bitop3_b32 v1, v1, s4, v53 bitop3:0xc8
	v_or_b32_e32 v1, s2, v1
	v_mad_u32_u24 v81, v53, s0, v52
	v_mad_u64_u32 v[52:53], s[4:5], v1, s1, v[52:53]
	v_or_b32_e32 v1, 0x400, v0
	v_mul_u32_u24_e32 v53, 0x556, v1
	v_lshrrev_b32_e32 v53, 16, v53
	ds_read_b128 v[94:97], v81 offset:32768
	s_waitcnt lgkmcnt(1)
	buffer_store_dwordx4 v[60:63], v50, s[24:27], 0 offen sc1
	s_waitcnt lgkmcnt(0)
	buffer_store_dwordx4 v[94:97], v52, s[24:27], 0 offen sc1
	v_lshlrev_b32_e32 v61, 3, v53
	v_mul_lo_u32 v60, v53, s3
	v_bitop3_b32 v61, v61, s6, v53 bitop3:0xc8
	v_or_b32_e32 v61, s2, v61
	v_add_lshl_u32 v62, v60, v1, 4
	v_mad_u64_u32 v[60:61], s[4:5], v61, s1, v[62:63]
	v_or_b32_e32 v1, 0x600, v0
	v_mad_u32_u24 v53, v53, s0, v62
	v_mul_u32_u24_e32 v61, 0x556, v1
	ds_read_b128 v[62:65], v53 offset:32768
	v_lshrrev_b32_e32 v67, 16, v61
	v_mul_lo_u32 v94, v67, s3
	v_add_lshl_u32 v98, v94, v1, 4
	v_lshrrev_b32_e32 v1, 13, v61
	v_mad_u32_u24 v160, v67, s0, v98
	v_and_b32_e32 v1, 0x1c0, v1
	v_bfe_u32 v61, v61, 16, 3
	ds_read_b128 v[94:97], v160 offset:32768
	v_or3_b32 v1, s2, v61, v1
	s_waitcnt lgkmcnt(1)
	buffer_store_dwordx4 v[62:65], v60, s[24:27], 0 offen sc1
	s_nop 1
	v_mad_u64_u32 v[62:63], s[4:5], v1, s1, v[98:99]
	v_or_b32_e32 v1, 0x800, v0
	v_mul_u32_u24_e32 v61, 0xaab, v1
	v_lshrrev_b32_e32 v61, 17, v61
	v_mul_lo_u32 v63, v61, s3
	v_lshlrev_b32_e32 v64, 3, v61
	s_waitcnt lgkmcnt(0)
	buffer_store_dwordx4 v[94:97], v62, s[24:27], 0 offen sc1
	v_bitop3_b32 v64, v64, s6, v61 bitop3:0xc8
	v_or_b32_e32 v64, s2, v64
	v_add_lshl_u32 v94, v63, v1, 4
	v_mad_u32_u24 v61, v61, s0, v94
	v_or_b32_e32 v0, 0xa00, v0
	v_mad_u64_u32 v[64:65], s[4:5], v64, s1, v[94:95]
	ds_read_b128 v[94:97], v61 offset:32768
	v_mul_u32_u24_e32 v1, 0xaab, v0
	v_lshrrev_b32_e32 v63, 17, v1
	v_mul_lo_u32 v65, v63, s3
	v_add_lshl_u32 v0, v65, v0, 4
	v_mad_u32_u24 v63, v63, s0, v0
	ds_read_b128 v[98:101], v63 offset:32768
	s_waitcnt lgkmcnt(1)
	buffer_store_dwordx4 v[94:97], v64, s[24:27], 0 offen sc1
	ds_read_b128 v[94:97], v66
	ds_read_b128 v[102:105], v66 offset:8192
	ds_read_b128 v[106:109], v66 offset:16384
	ds_read_b128 v[110:113], v66 offset:24576
	v_lshrrev_b32_e32 v65, 14, v1
	v_and_b32_e32 v65, 0x1c0, v65
	v_bfe_u32 v1, v1, 17, 3
	v_or3_b32 v1, s2, v1, v65
	v_mad_u64_u32 v[66:67], s[0:1], v1, s1, v[0:1]
	s_waitcnt lgkmcnt(4)
	buffer_store_dwordx4 v[98:101], v66, s[24:27], 0 offen sc1
	s_waitcnt lgkmcnt(3)
	s_nop 0
	v_mfma_f32_16x16x32_f16 v[98:101], v[34:37], v[94:97], 0
	s_waitcnt lgkmcnt(2)
	v_mfma_f32_16x16x32_f16 v[114:117], v[34:37], v[102:105], 0
	s_waitcnt lgkmcnt(1)
	v_mfma_f32_16x16x32_f16 v[118:121], v[34:37], v[106:109], 0
	s_waitcnt lgkmcnt(0)
	v_mfma_f32_16x16x32_f16 v[34:37], v[34:37], v[110:113], 0
	v_mfma_f32_16x16x32_f16 v[122:125], v[26:29], v[94:97], 0
	v_mfma_f32_16x16x32_f16 v[126:129], v[26:29], v[102:105], 0
	v_mfma_f32_16x16x32_f16 v[130:133], v[26:29], v[106:109], 0
	v_mfma_f32_16x16x32_f16 v[26:29], v[26:29], v[110:113], 0
	v_mfma_f32_16x16x32_f16 v[94:97], v[22:25], v[94:97], 0
	v_mfma_f32_16x16x32_f16 v[102:105], v[22:25], v[102:105], 0
	v_mfma_f32_16x16x32_f16 v[106:109], v[22:25], v[106:109], 0
	v_mfma_f32_16x16x32_f16 v[22:25], v[22:25], v[110:113], 0
	s_mov_b32 s0, 0x34000
	v_add_co_u32_e32 v158, vcc, s0, v54
	s_mov_b32 s0, 0x35000
	s_nop 0
	v_addc_co_u32_e32 v159, vcc, 0, v55, vcc
	v_add_co_u32_e32 v54, vcc, s0, v54
	s_nop 1
	v_addc_co_u32_e32 v55, vcc, 0, v55, vcc
	global_load_dwordx4 v[110:113], v[54:55], off offset:-4096
	global_load_dwordx4 v[134:137], v[58:59], off offset:3072
	global_load_dwordx4 v[138:141], v[158:159], off offset:1024
	ds_read_b128 v[142:145], v72
	ds_read_b128 v[146:149], v72 offset:8192
	ds_read_b128 v[150:153], v72 offset:16384
	ds_read_b128 v[154:157], v72 offset:24576
	s_waitcnt lgkmcnt(3)
	v_mfma_f32_16x16x32_f16 v[98:101], v[14:17], v[142:145], v[98:101]
	s_waitcnt lgkmcnt(2)
	v_mfma_f32_16x16x32_f16 v[114:117], v[14:17], v[146:149], v[114:117]
	s_waitcnt lgkmcnt(1)
	v_mfma_f32_16x16x32_f16 v[118:121], v[14:17], v[150:153], v[118:121]
	s_waitcnt lgkmcnt(0)
	v_mfma_f32_16x16x32_f16 v[14:17], v[14:17], v[154:157], v[34:37]
	v_mfma_f32_16x16x32_f16 v[34:37], v[6:9], v[142:145], v[122:125]
	v_mfma_f32_16x16x32_f16 v[122:125], v[6:9], v[146:149], v[126:129]
	v_mfma_f32_16x16x32_f16 v[126:129], v[6:9], v[150:153], v[130:133]
	v_mfma_f32_16x16x32_f16 v[6:9], v[6:9], v[154:157], v[26:29]
	v_mfma_f32_16x16x32_f16 v[26:29], v[2:5], v[142:145], v[94:97]
	v_mfma_f32_16x16x32_f16 v[94:97], v[2:5], v[146:149], v[102:105]
	v_mfma_f32_16x16x32_f16 v[102:105], v[2:5], v[150:153], v[106:109]
	v_mfma_f32_16x16x32_f16 v[0:3], v[2:5], v[154:157], v[22:25]
	s_nop 2
	global_load_dwordx4 v[22:25], v[158:159], off offset:2048
	global_load_dwordx4 v[106:109], v[158:159], off offset:3072
	global_load_dwordx4 v[130:133], v[54:55], off
	ds_read_b128 v[142:145], v74
	ds_read_b128 v[146:149], v74 offset:8192
	ds_read_b128 v[150:153], v74 offset:16384
	ds_read_b128 v[154:157], v74 offset:24576
	s_waitcnt lgkmcnt(3)
	v_mfma_f32_16x16x32_f16 v[98:101], v[18:21], v[142:145], v[98:101]
	s_waitcnt lgkmcnt(2)
	v_mfma_f32_16x16x32_f16 v[114:117], v[18:21], v[146:149], v[114:117]
	s_waitcnt lgkmcnt(1)
	v_mfma_f32_16x16x32_f16 v[118:121], v[18:21], v[150:153], v[118:121]
	s_waitcnt lgkmcnt(0)
	v_mfma_f32_16x16x32_f16 v[14:17], v[18:21], v[154:157], v[14:17]
	v_mfma_f32_16x16x32_f16 v[18:21], v[10:13], v[142:145], v[34:37]
	v_mfma_f32_16x16x32_f16 v[34:37], v[10:13], v[146:149], v[122:125]
	v_mfma_f32_16x16x32_f16 v[122:125], v[10:13], v[150:153], v[126:129]
	v_mfma_f32_16x16x32_f16 v[4:7], v[10:13], v[154:157], v[6:9]
	v_mfma_f32_16x16x32_f16 v[8:11], v[30:33], v[142:145], v[26:29]
	v_mfma_f32_16x16x32_f16 v[26:29], v[30:33], v[146:149], v[94:97]
	v_mfma_f32_16x16x32_f16 v[94:97], v[30:33], v[150:153], v[102:105]
	v_mfma_f32_16x16x32_f16 v[0:3], v[30:33], v[154:157], v[0:3]
	global_load_dwordx4 v[30:33], v[54:55], off offset:1024
	s_nop 0
	global_load_dwordx4 v[102:105], v[54:55], off offset:2048
	global_load_dwordx4 v[126:129], v[54:55], off offset:3072
	ds_read_b128 v[142:145], v75
	ds_read_b128 v[146:149], v75 offset:8192
	ds_read_b128 v[150:153], v75 offset:16384
	ds_read_b128 v[154:157], v75 offset:24576
	s_waitcnt lgkmcnt(3)
	v_mfma_f32_16x16x32_f16 v[98:101], v[46:49], v[142:145], v[98:101]
	s_waitcnt lgkmcnt(2)
	v_mfma_f32_16x16x32_f16 v[114:117], v[46:49], v[146:149], v[114:117]
	s_waitcnt lgkmcnt(1)
	v_mfma_f32_16x16x32_f16 v[118:121], v[46:49], v[150:153], v[118:121]
	s_waitcnt lgkmcnt(0)
	v_mfma_f32_16x16x32_f16 v[12:15], v[46:49], v[154:157], v[14:17]
	v_mfma_f32_16x16x32_f16 v[16:19], v[42:45], v[142:145], v[18:21]
	v_mfma_f32_16x16x32_f16 v[34:37], v[42:45], v[146:149], v[34:37]
	v_mfma_f32_16x16x32_f16 v[46:49], v[42:45], v[150:153], v[122:125]
	v_mfma_f32_16x16x32_f16 v[4:7], v[42:45], v[154:157], v[4:7]
	v_mfma_f32_16x16x32_f16 v[8:11], v[38:41], v[142:145], v[8:11]
	v_mfma_f32_16x16x32_f16 v[26:29], v[38:41], v[146:149], v[26:29]
	v_mfma_f32_16x16x32_f16 v[42:45], v[38:41], v[150:153], v[94:97]
	v_mfma_f32_16x16x32_f16 v[0:3], v[38:41], v[154:157], v[0:3]
	ds_read_b128 v[38:41], v76
	s_nop 0
	ds_read_b128 v[94:97], v76 offset:8192
	ds_read_b128 v[122:125], v76 offset:16384
	ds_read_b128 v[142:145], v76 offset:24576
	s_waitcnt vmcnt(17) lgkmcnt(3)
	v_mfma_f32_16x16x32_f16 v[98:101], v[82:85], v[38:41], v[98:101]
	s_waitcnt lgkmcnt(2)
	v_mfma_f32_16x16x32_f16 v[114:117], v[82:85], v[94:97], v[114:117]
	s_waitcnt lgkmcnt(1)
	v_mfma_f32_16x16x32_f16 v[118:121], v[82:85], v[122:125], v[118:121]
	s_waitcnt lgkmcnt(0)
	v_mfma_f32_16x16x32_f16 v[12:15], v[82:85], v[142:145], v[12:15]
	s_waitcnt vmcnt(16)
	v_mfma_f32_16x16x32_f16 v[16:19], v[86:89], v[38:41], v[16:19]
	v_mfma_f32_16x16x32_f16 v[34:37], v[86:89], v[94:97], v[34:37]
	v_mfma_f32_16x16x32_f16 v[46:49], v[86:89], v[122:125], v[46:49]
	v_mfma_f32_16x16x32_f16 v[4:7], v[86:89], v[142:145], v[4:7]
	s_waitcnt vmcnt(15)
	v_mfma_f32_16x16x32_f16 v[8:11], v[90:93], v[38:41], v[8:11]
	v_mfma_f32_16x16x32_f16 v[26:29], v[90:93], v[94:97], v[26:29]
	v_mfma_f32_16x16x32_f16 v[38:41], v[90:93], v[122:125], v[42:45]
	v_mfma_f32_16x16x32_f16 v[0:3], v[90:93], v[142:145], v[0:3]
	s_nop 1
	ds_read_b128 v[42:45], v77
	ds_read_b128 v[82:85], v77 offset:8192
	ds_read_b128 v[86:89], v77 offset:16384
	ds_read_b128 v[74:77], v77 offset:24576
	s_waitcnt vmcnt(7) lgkmcnt(3)
	v_mfma_f32_16x16x32_f16 v[90:93], v[134:137], v[42:45], v[98:101]
	s_waitcnt lgkmcnt(2)
	v_mfma_f32_16x16x32_f16 v[94:97], v[134:137], v[82:85], v[114:117]
	s_waitcnt lgkmcnt(1)
	v_mfma_f32_16x16x32_f16 v[98:101], v[134:137], v[86:89], v[118:121]
	s_waitcnt lgkmcnt(0)
	v_mfma_f32_16x16x32_f16 v[12:15], v[134:137], v[74:77], v[12:15]
	v_mfma_f32_16x16x32_f16 v[16:19], v[110:113], v[42:45], v[16:19]
	v_mfma_f32_16x16x32_f16 v[34:37], v[110:113], v[82:85], v[34:37]
	v_mfma_f32_16x16x32_f16 v[46:49], v[110:113], v[86:89], v[46:49]
	v_mfma_f32_16x16x32_f16 v[4:7], v[110:113], v[74:77], v[4:7]
	s_waitcnt vmcnt(6)
	v_mfma_f32_16x16x32_f16 v[8:11], v[138:141], v[42:45], v[8:11]
	v_mfma_f32_16x16x32_f16 v[26:29], v[138:141], v[82:85], v[26:29]
	v_mfma_f32_16x16x32_f16 v[38:41], v[138:141], v[86:89], v[38:41]
	v_mfma_f32_16x16x32_f16 v[0:3], v[138:141], v[74:77], v[0:3]
	ds_read_b128 v[42:45], v78
	ds_read_b128 v[74:77], v78 offset:8192
	ds_read_b128 v[82:85], v78 offset:16384
	ds_read_b128 v[86:89], v78 offset:24576
	s_waitcnt vmcnt(5) lgkmcnt(3)
	v_mfma_f32_16x16x32_f16 v[90:93], v[22:25], v[42:45], v[90:93]
	s_waitcnt lgkmcnt(2)
	v_mfma_f32_16x16x32_f16 v[94:97], v[22:25], v[74:77], v[94:97]
	s_waitcnt lgkmcnt(1)
	v_mfma_f32_16x16x32_f16 v[98:101], v[22:25], v[82:85], v[98:101]
	s_waitcnt lgkmcnt(0)
	v_mfma_f32_16x16x32_f16 v[12:15], v[22:25], v[86:89], v[12:15]
	s_waitcnt vmcnt(4)
	v_mfma_f32_16x16x32_f16 v[16:19], v[106:109], v[42:45], v[16:19]
	v_mfma_f32_16x16x32_f16 v[20:23], v[106:109], v[74:77], v[34:37]
	v_mfma_f32_16x16x32_f16 v[34:37], v[106:109], v[82:85], v[46:49]
	v_mfma_f32_16x16x32_f16 v[4:7], v[106:109], v[86:89], v[4:7]
	s_waitcnt vmcnt(3)
	v_mfma_f32_16x16x32_f16 v[8:11], v[130:133], v[42:45], v[8:11]
	v_mfma_f32_16x16x32_f16 v[24:27], v[130:133], v[74:77], v[26:29]
	v_mfma_f32_16x16x32_f16 v[38:41], v[130:133], v[82:85], v[38:41]
	v_mfma_f32_16x16x32_f16 v[0:3], v[130:133], v[86:89], v[0:3]
	ds_read_b128 v[42:45], v79
	ds_read_b128 v[46:49], v79 offset:8192
	ds_read_b128 v[74:77], v79 offset:16384
	ds_read_b128 v[82:85], v79 offset:24576
	s_waitcnt vmcnt(2) lgkmcnt(3)
	v_mfma_f32_16x16x32_f16 v[86:89], v[30:33], v[42:45], v[90:93]
	s_waitcnt lgkmcnt(2)
	v_mfma_f32_16x16x32_f16 v[90:93], v[30:33], v[46:49], v[94:97]
	s_waitcnt lgkmcnt(1)
	v_mfma_f32_16x16x32_f16 v[94:97], v[30:33], v[74:77], v[98:101]
	s_waitcnt lgkmcnt(0)
	v_mfma_f32_16x16x32_f16 v[12:15], v[30:33], v[82:85], v[12:15]
	s_waitcnt vmcnt(1)
	v_mfma_f32_16x16x32_f16 v[16:19], v[102:105], v[42:45], v[16:19]
	v_mfma_f32_16x16x32_f16 v[20:23], v[102:105], v[46:49], v[20:23]
	v_mfma_f32_16x16x32_f16 v[28:31], v[102:105], v[74:77], v[34:37]
	v_mfma_f32_16x16x32_f16 v[4:7], v[102:105], v[82:85], v[4:7]
	s_waitcnt vmcnt(0)
	v_mfma_f32_16x16x32_f16 v[8:11], v[126:129], v[42:45], v[8:11]
	v_mfma_f32_16x16x32_f16 v[24:27], v[126:129], v[46:49], v[24:27]
	v_mfma_f32_16x16x32_f16 v[32:35], v[126:129], v[74:77], v[38:41]
	v_mfma_f32_16x16x32_f16 v[0:3], v[126:129], v[82:85], v[0:3]
	s_nop 1
	global_load_dwordx4 v[36:39], v[56:57], off offset:1536
	global_load_dwordx4 v[40:43], v[56:57], off offset:1600
	global_load_dwordx4 v[44:47], v[56:57], off offset:1664
	v_mov_b32_e32 v58, v21
	v_mov_b32_e32 v59, v22
	v_mov_b32_e32 v74, v29
	v_mov_b32_e32 v56, v13
	v_mov_b32_e32 v57, v14
	v_mov_b32_e32 v75, v30
	v_mov_b32_e32 v48, v91
	v_mov_b32_e32 v49, v92
	v_mov_b32_e32 v54, v95
	v_mov_b32_e32 v55, v96
	v_mov_b32_e32 v76, v5
	v_mov_b32_e32 v77, v6
	s_barrier
	s_waitcnt vmcnt(2)
	v_pk_add_f32 v[78:79], v[86:87], v[36:37]
	v_pk_add_f32 v[82:83], v[88:89], v[38:39]
	v_add_f32_e32 v21, v90, v36
	v_pk_mov_b32 v[84:85], v[36:37], v[38:39] op_sel:[1,0]
	v_add_f32_e32 v22, v93, v39
	v_add_f32_e32 v29, v94, v36
	v_add_f32_e32 v36, v12, v36
	v_add_f32_e32 v37, v15, v39
	s_waitcnt vmcnt(1)
	v_add_f32_e32 v38, v20, v40
	v_add_f32_e32 v23, v23, v43
	v_add_f32_e32 v30, v97, v39
	v_pk_add_f32 v[12:13], v[16:17], v[40:41]
	v_pk_add_f32 v[14:15], v[18:19], v[42:43]
	v_pk_mov_b32 v[16:17], v[40:41], v[42:43] op_sel:[1,0]
	v_add_f32_e32 v28, v28, v40
	v_add_f32_e32 v31, v31, v43
	v_add_f32_e32 v39, v4, v40
	v_add_f32_e32 v40, v7, v43
	v_cvt_f16_f32_e32 v41, v21
	v_cvt_f16_f32_e32 v42, v22
	v_cvt_f16_f32_e32 v36, v36
	v_cvt_f16_f32_e32 v37, v37
	v_cvt_f16_f32_e32 v38, v38
	v_cvt_f16_f32_e32 v43, v23
	v_cvt_f16_f32_e32 v29, v29
	v_cvt_f16_f32_e32 v30, v30
	v_cvt_f16_f32_e32 v28, v28
	v_cvt_f16_f32_e32 v31, v31
	v_cvt_f16_f32_e32 v39, v39
	v_cvt_f16_f32_e32 v40, v40
	s_waitcnt vmcnt(0)
	v_pk_add_f32 v[4:5], v[8:9], v[44:45]
	v_pk_add_f32 v[6:7], v[10:11], v[46:47]
	v_pk_add_f32 v[10:11], v[48:49], v[84:85]
	v_pk_add_f32 v[20:21], v[56:57], v[84:85]
	v_cvt_pk_f16_f32 v12, v12, v13
	v_cvt_pk_f16_f32 v13, v14, v15
	v_pk_add_f32 v[14:15], v[58:59], v[16:17]
	v_cvt_pk_f16_f32 v8, v78, v79
	v_cvt_pk_f16_f32 v9, v82, v83
	v_pk_add_f32 v[18:19], v[54:55], v[84:85]
	v_pk_add_f32 v[22:23], v[74:75], v[16:17]
	v_pk_add_f32 v[16:17], v[76:77], v[16:17]
	v_cvt_pk_f16_f32 v4, v4, v5
	v_cvt_pk_f16_f32 v5, v6, v7
	v_cvt_pk_f16_f32 v6, v10, v11
	v_cvt_pk_f16_f32 v10, v20, v21
	v_cvt_pk_f16_f32 v11, v14, v15
	v_cvt_pk_f16_f32 v7, v18, v19
	v_cvt_pk_f16_f32 v14, v22, v23
	v_cvt_pk_f16_f32 v15, v16, v17
	ds_write2_b64 v73, v[8:9], v[12:13] offset1:4
	ds_write_b64 v69, v[4:5] offset:32832
	v_pack_b32_f16 v4, v41, v6
	v_alignbit_b32 v5, v42, v6, 16
	v_pack_b32_f16 v8, v36, v10
	v_alignbit_b32 v9, v37, v10, 16
	v_pack_b32_f16 v10, v38, v11
	v_alignbit_b32 v11, v43, v11, 16
	v_add_f32_e32 v24, v24, v44
	v_pack_b32_f16 v6, v29, v7
	v_alignbit_b32 v7, v30, v7, 16
	v_pack_b32_f16 v12, v28, v14
	v_alignbit_b32 v13, v31, v14, 16
	v_pack_b32_f16 v14, v39, v15
	v_alignbit_b32 v15, v40, v15, 16
	ds_write2_b64 v70, v[4:5], v[10:11] offset0:32 offset1:36
	ds_write2_b64 v71, v[6:7], v[12:13] offset0:64 offset1:68
	ds_write2_b64 v80, v[8:9], v[14:15] offset1:4
	v_add_f32_e32 v8, v27, v47
	v_cvt_f16_f32_e32 v24, v24
	v_cvt_f16_f32_e32 v8, v8
	v_mov_b32_e32 v4, v25
	v_mov_b32_e32 v5, v26
	v_pk_mov_b32 v[6:7], v[44:45], v[46:47] op_sel:[1,0]
	v_add_f32_e32 v9, v35, v47
	v_pk_add_f32 v[4:5], v[4:5], v[6:7]
	v_cvt_f16_f32_e32 v9, v9
	v_cvt_pk_f16_f32 v5, v4, v5
	v_pack_b32_f16 v4, v24, v5
	v_alignbit_b32 v5, v8, v5, 16
	ds_write_b64 v69, v[4:5] offset:45376
	v_add_f32_e32 v4, v32, v44
	v_cvt_f16_f32_e32 v8, v4
	v_mov_b32_e32 v4, v33
	v_mov_b32_e32 v5, v34
	v_pk_add_f32 v[4:5], v[4:5], v[6:7]
	v_add_f32_e32 v0, v0, v44
	v_cvt_pk_f16_f32 v5, v4, v5
	v_pack_b32_f16 v4, v8, v5
	v_alignbit_b32 v5, v9, v5, 16
	ds_write_b64 v69, v[4:5] offset:57920
	v_cvt_f16_f32_e32 v4, v0
	v_mov_b32_e32 v0, v1
	v_mov_b32_e32 v1, v2
	v_add_f32_e32 v2, v3, v47
	v_cvt_f16_f32_e32 v2, v2
	v_pk_add_f32 v[0:1], v[0:1], v[6:7]
	s_nop 0
	v_cvt_pk_f16_f32 v1, v0, v1
	v_pack_b32_f16 v0, v4, v1
	v_alignbit_b32 v1, v2, v1, 16
	ds_write_b64 v68, v[0:1] offset:32832
	s_waitcnt lgkmcnt(0)
	s_barrier
	ds_read_b128 v[0:3], v51 offset:32768
	ds_read_b128 v[4:7], v81 offset:32768
	s_waitcnt lgkmcnt(1)
	buffer_store_dwordx4 v[0:3], v50, s[24:27], 0 offen offset:768 sc1
	ds_read_b128 v[0:3], v53 offset:32768
	ds_read_b128 v[8:11], v160 offset:32768
	ds_read_b128 v[12:15], v61 offset:32768
	ds_read_b128 v[16:19], v63 offset:32768
	s_waitcnt lgkmcnt(4)
	buffer_store_dwordx4 v[4:7], v52, s[24:27], 0 offen offset:768 sc1
	s_waitcnt lgkmcnt(3)
	buffer_store_dwordx4 v[0:3], v60, s[24:27], 0 offen offset:768 sc1
	s_waitcnt lgkmcnt(2)
	buffer_store_dwordx4 v[8:11], v62, s[24:27], 0 offen offset:768 sc1
	s_waitcnt lgkmcnt(1)
	buffer_store_dwordx4 v[12:15], v64, s[24:27], 0 offen offset:768 sc1
	s_waitcnt lgkmcnt(0)
	buffer_store_dwordx4 v[16:19], v66, s[24:27], 0 offen offset:768 sc1
	s_endpgm
	.p2alignl 8, 3212836864
